# packed f32 add/mul/fma in the attention tile bodies split into scalar pairs (bit-identical)
# baseline (speedup 1.0000x reference)
.LBB0_1000:
	ds_bpermute_b32 v3, v137, v152
	v_max_f32_e32 v42, v127, v127
	v_or_b32_e32 v2, s22, v133
	v_lshl_or_b32 v2, v2, 6, v139
	s_add_i32 s29, s29, s74
	s_waitcnt lgkmcnt(0)
	v_add_f32_e32 v3, v152, v3
	ds_bpermute_b32 v4, v138, v3
	s_cmp_le_i32 s29, s27
	s_waitcnt lgkmcnt(0)
	v_add_f32_e32 v3, v3, v4
	v_max_f32_e32 v4, v150, v150
	v_max_f32_e32 v4, v4, v42
	v_sub_f32_e32 v5, v150, v4
	v_sub_f32_e32 v4, v127, v4
	v_mul_f32_e32 v5, 0x3fb8aa3b, v5
	v_mul_f32_e32 v4, 0x3fb8aa3b, v4
	v_exp_f32_e32 v5, v5
	v_exp_f32_e32 v4, v4
	s_nop 0
	v_fmac_f32_e32 v4, v5, v3
	v_div_scale_f32 v3, s[6:7], v4, v4, v5
	v_rcp_f32_e32 v6, v3
	s_nop 0
	v_fma_f32 v7, -v3, v6, 1.0
	v_fmac_f32_e32 v6, v7, v6
	v_div_scale_f32 v7, vcc, v5, v4, v5
	v_mul_f32_e32 v8, v7, v6
	v_fma_f32 v9, -v3, v8, v7
	v_fmac_f32_e32 v8, v9, v6
	v_fma_f32 v3, -v3, v8, v7
	v_div_fmas_f32 v3, v3, v6, v8
	v_div_fixup_f32 v4, v3, v4, v5
	v_mul_f32_e32 v8, v32, v4
	v_mul_f32_e32 v9, v33, v4
	v_mul_f32_e32 v30, v30, v4
	v_mul_f32_e32 v31, v31, v4
	v_mul_f32_e32 v18, v18, v4
	v_mul_f32_e32 v19, v19, v4
	v_cvt_pk_bf16_f32 v30, v30, v31
	v_cvt_pk_bf16_f32 v31, v8, v9
	v_mul_f32_e32 v8, v20, v4
	v_mul_f32_e32 v9, v21, v4
	v_lshlrev_b64 v[6:7], 10, v[130:131]
	v_ashrrev_i32_e32 v3, 31, v2
	v_cvt_pk_bf16_f32 v18, v18, v19
	v_cvt_pk_bf16_f32 v19, v8, v9
	v_mul_f32_e32 v8, v16, v4
	v_mul_f32_e32 v9, v17, v4
	v_mul_f32_e32 v14, v14, v4
	v_mul_f32_e32 v15, v15, v4
	v_lshl_add_u64 v[6:7], s[90:91], 0, v[6:7]
	v_lshlrev_b64 v[2:3], 1, v[2:3]
	v_cvt_pk_bf16_f32 v14, v14, v15
	v_cvt_pk_bf16_f32 v15, v8, v9
	v_mul_f32_e32 v8, v12, v4
	v_mul_f32_e32 v9, v13, v4
	v_mul_f32_e32 v5, v11, v4
	v_mul_f32_e32 v4, v10, v4
	v_lshl_add_u64 v[6:7], v[6:7], 0, v[2:3]
	v_cvt_pk_bf16_f32 v4, v4, v5
	v_cvt_pk_bf16_f32 v5, v8, v9
	global_store_dwordx2 v[6:7], v[4:5], off offset:96
	ds_bpermute_b32 v4, v137, v151
	global_store_dwordx2 v[6:7], v[30:31], off
	global_store_dwordx2 v[6:7], v[18:19], off offset:32
	global_store_dwordx2 v[6:7], v[14:15], off offset:64
	s_waitcnt lgkmcnt(0)
	v_add_f32_e32 v4, v151, v4
	ds_bpermute_b32 v5, v138, v4
	s_waitcnt lgkmcnt(0)
	v_add_f32_e32 v4, v4, v5
	v_max_f32_e32 v5, v149, v149
	v_max_f32_e32 v5, v5, v42
	v_sub_f32_e32 v6, v149, v5
	v_sub_f32_e32 v5, v127, v5
	v_mul_f32_e32 v6, 0x3fb8aa3b, v6
	v_mul_f32_e32 v5, 0x3fb8aa3b, v5
	v_exp_f32_e32 v6, v6
	v_exp_f32_e32 v5, v5
	s_nop 0
	v_fmac_f32_e32 v5, v6, v4
	v_div_scale_f32 v4, s[6:7], v5, v5, v6
	v_rcp_f32_e32 v7, v4
	s_nop 0
	v_fma_f32 v8, -v4, v7, 1.0
	v_fmac_f32_e32 v7, v8, v7
	v_div_scale_f32 v8, vcc, v6, v5, v6
	v_mul_f32_e32 v9, v8, v7
	v_fma_f32 v10, -v4, v9, v8
	v_fmac_f32_e32 v9, v10, v7
	v_fma_f32 v4, -v4, v9, v8
	v_div_fmas_f32 v4, v4, v7, v9
	v_div_fixup_f32 v4, v4, v5, v6
	v_lshlrev_b64 v[6:7], 10, v[128:129]
	v_lshl_add_u64 v[6:7], s[90:91], 0, v[6:7]
	v_mul_f32_e32 v8, v40, v4
	v_mul_f32_e32 v9, v41, v4
	v_mul_f32_e32 v10, v38, v4
	v_mul_f32_e32 v11, v39, v4
	v_lshl_add_u64 v[2:3], v[6:7], 0, v[2:3]
	v_cvt_pk_bf16_f32 v10, v10, v11
	v_cvt_pk_bf16_f32 v11, v8, v9
	v_mul_f32_e32 v6, v36, v4
	v_mul_f32_e32 v7, v37, v4
	v_mul_f32_e32 v8, v34, v4
	v_mul_f32_e32 v9, v35, v4
	global_store_dwordx2 v[2:3], v[10:11], off
	v_cvt_pk_bf16_f32 v8, v8, v9
	v_cvt_pk_bf16_f32 v9, v6, v7
	global_store_dwordx2 v[2:3], v[8:9], off offset:32
	v_mul_f32_e32 v6, v28, v4
	v_mul_f32_e32 v7, v29, v4
	v_mul_f32_e32 v8, v26, v4
	v_mul_f32_e32 v9, v27, v4
	s_nop 0
	v_cvt_pk_bf16_f32 v8, v8, v9
	v_cvt_pk_bf16_f32 v9, v6, v7
	v_mul_f32_e32 v6, v24, v4
	v_mul_f32_e32 v7, v25, v4
	v_mul_f32_e32 v5, v23, v4
	v_mul_f32_e32 v4, v22, v4
	global_store_dwordx2 v[2:3], v[8:9], off offset:64
	v_cvt_pk_bf16_f32 v4, v4, v5
	v_cvt_pk_bf16_f32 v5, v6, v7
	global_store_dwordx2 v[2:3], v[4:5], off offset:96
	s_cbranch_scc0 .LBB0_1030

.LBB0_1019:
	s_max_i32 s42, s36, 0
	s_lshl_b64 s[8:9], s[42:43], 13
	s_lshl_b32 s42, s42, 1
	s_barrier
	s_waitcnt vmcnt(3)
	ds_write_b128 v146, v[200:203]
	s_waitcnt vmcnt(2)
	ds_write_b64 v147, v[204:205] offset:8192
	ds_write_b64 v148, v[206:207] offset:8192
	s_add_i32 s7, s38, 0xffffff81
	s_cmp_lt_i32 s37, 1
	s_cselect_b64 s[8:9], -1, 0
	s_cmp_gt_i32 s6, s10
	s_cselect_b64 s[12:13], -1, 0
	s_or_b64 s[8:9], s[8:9], s[12:13]
	s_cmp_le_i32 s36, s7
	s_cselect_b64 s[12:13], -1, 0
	s_or_b64 s[8:9], s[8:9], s[12:13]
	s_and_b64 vcc, exec, s[8:9]
	s_waitcnt lgkmcnt(0)
	s_barrier
	s_cbranch_vccnz .LBB0_1025
	v_add_u32_e32 v58, v136, v140
	ds_read_b128 v[90:93], v58
	v_sub_u32_e32 v153, s6, v130
	v_lshl_add_u32 v172, v153, 2, v143
	v_add_u32_e32 v59, v136, v141
	v_add_u32_e32 v153, 0xffc, v172
	ds_read_b128 v[94:97], v59
	ds_read_b128 v[98:101], v58 offset:2048
	ds_read_b128 v[102:105], v59 offset:2048
	ds_read_b128 v[106:109], v58 offset:4096
	ds_read_b128 v[110:113], v59 offset:4096
	ds_read_b128 v[114:117], v58 offset:6144
	ds_read_b128 v[118:121], v59 offset:6144
	ds_read_b128 v[86:89], v58 offset:8192
	ds_read_b128 v[82:85], v58 offset:10240
	ds_read_b128 v[78:81], v58 offset:12288
	ds_read_b128 v[74:77], v58 offset:14336
	ds_read_b128 v[70:73], v59 offset:8192
	ds_read_b128 v[66:69], v59 offset:10240
	ds_read_b128 v[62:65], v59 offset:12288
	ds_read_b128 v[58:61], v59 offset:14336
	ds_read2_b32 v[170:171], v153 offset1:1
	s_waitcnt lgkmcnt(14)
	v_mfma_f32_16x16x32_bf16 v[158:161], v[98:101], v[42:45], 0
	v_mfma_f32_16x16x32_bf16 v[154:157], v[90:93], v[42:45], 0
	v_mfma_f32_16x16x32_bf16 v[154:157], v[94:97], v[46:49], v[154:157]
	s_waitcnt lgkmcnt(13)
	v_mfma_f32_16x16x32_bf16 v[158:161], v[102:105], v[46:49], v[158:161]
	s_waitcnt lgkmcnt(12)
	v_mfma_f32_16x16x32_bf16 v[162:165], v[106:109], v[42:45], 0
	s_waitcnt lgkmcnt(0)
	s_nop 2
	v_add_f32_e32 v153, v154, v170
	v_add_f32_e32 v154, v155, v171
	v_add_u32_e32 v155, 0x1004, v172
	ds_read2_b32 v[170:171], v155 offset1:1
	v_mfma_f32_16x16x32_bf16 v[162:165], v[110:113], v[46:49], v[162:165]
	s_waitcnt lgkmcnt(0)
	v_add_f32_e32 v155, v156, v170
	v_add_f32_e32 v156, v157, v171
	v_add_u32_e32 v157, 0x103c, v172
	ds_read2_b32 v[170:171], v157 offset1:1
	v_mfma_f32_16x16x32_bf16 v[166:169], v[114:117], v[42:45], 0
	s_waitcnt lgkmcnt(0)
	v_add_f32_e32 v157, v158, v170
	v_add_f32_e32 v158, v159, v171
	v_add_u32_e32 v159, 0x1044, v172
	ds_read2_b32 v[170:171], v159 offset1:1
	v_mfma_f32_16x16x32_bf16 v[166:169], v[118:121], v[46:49], v[166:169]
	s_waitcnt lgkmcnt(0)
	v_add_f32_e32 v159, v160, v170
	v_add_f32_e32 v160, v161, v171
	v_add_u32_e32 v161, 0x107c, v172
	ds_read2_b32 v[170:171], v161 offset1:1
	s_waitcnt lgkmcnt(0)
	v_add_f32_e32 v161, v162, v170
	v_add_f32_e32 v162, v163, v171
	v_add_u32_e32 v163, 0x1084, v172
	ds_read2_b32 v[170:171], v163 offset1:1
	s_waitcnt lgkmcnt(0)
	v_add_f32_e32 v163, v164, v170
	v_add_f32_e32 v164, v165, v171
	v_add_u32_e32 v165, 0x10bc, v172
	ds_read2_b32 v[170:171], v165 offset1:1
	s_waitcnt lgkmcnt(0)
	v_add_f32_e32 v165, v166, v170
	v_add_f32_e32 v166, v167, v171
	v_add_u32_e32 v167, 0x10c4, v172
	ds_read2_b32 v[170:171], v167 offset1:1
	s_waitcnt lgkmcnt(0)
	v_add_f32_e32 v167, v168, v170
	v_add_f32_e32 v168, v169, v171
	v_max_f32_e32 v169, v153, v154
	v_max3_f32 v169, v169, v155, v156
	v_max3_f32 v169, v169, v157, v158
	v_max3_f32 v169, v169, v159, v160
	v_max3_f32 v169, v169, v161, v162
	v_max3_f32 v169, v169, v163, v164
	v_max3_f32 v169, v169, v165, v166
	v_max3_f32 v169, v169, v167, v168
	v_add_f32_e32 v170, 0x40c00000, v150
	v_cmp_gt_f32_e32 vcc, v169, v170
	s_cbranch_vccz .LBB0_1022
	v_add_f32_e32 v169, 0, v169
	ds_bpermute_b32 v170, v137, v169
	s_waitcnt lgkmcnt(0)
	v_max_f32_e32 v170, v170, v170
	v_max_f32_e32 v169, v169, v170
	ds_bpermute_b32 v170, v138, v169
	s_waitcnt lgkmcnt(0)
	v_max3_f32 v169, v150, v169, v170
	v_sub_f32_e32 v150, v150, v169
	v_mul_f32_e32 v150, 0x3fb8aa3b, v150
	v_exp_f32_e32 v150, v150
	s_nop 0
	v_mul_f32_e32 v152, v152, v150
	v_mul_f32_e32 v32, v32, v150
	v_mul_f32_e32 v33, v33, v150
	v_mul_f32_e32 v30, v30, v150
	v_mul_f32_e32 v31, v31, v150
	v_mul_f32_e32 v20, v20, v150
	v_mul_f32_e32 v21, v21, v150
	v_mul_f32_e32 v18, v18, v150
	v_mul_f32_e32 v19, v19, v150
	v_mul_f32_e32 v16, v16, v150
	v_mul_f32_e32 v17, v17, v150
	v_mul_f32_e32 v14, v14, v150
	v_mul_f32_e32 v15, v15, v150
	v_mul_f32_e32 v12, v12, v150
	v_mul_f32_e32 v13, v13, v150
	v_mul_f32_e32 v10, v10, v150
	v_mul_f32_e32 v11, v11, v150
	v_mov_b32_e32 v150, v169
;     ...
;                         for (int kt = 0; kt < 4; ++kt) { sc[kt] = (f32x4){0.f, 0.f, 0.f, 0.f};
; #pragma unroll
;                             for (int ks = 0; ks < 2; ++ks) { const bf16x8 ak = (MODE != 3) ? akf[kt][ks] : akq[kt][ks];
;                                 sc[kt] = __builtin_amdgcn_mfma_f32_16x16x32_bf16(ak, Bq[qd][ks], sc[kt], 0, 0, 0); } }
;                         if (MODE == 3) {
; #pragma unroll
;                             for (int st = 0; st < 2; ++st)
; #pragma unroll
;                                 for (int dt = 0; dt < 4; ++dt) avq[st][dt] = *(const LAS bf16x8*)(L + LV + (16 * dt + n) * 128 + ((((4 * st + q) ^ n) & 7) << 4));
;                             __builtin_amdgcn_sched_barrier(0);
;                         }
;                         if (!far) {
;                             const LAS float* tp = (MODE == 2) ? biasd + hr * NT + (DOFF - tq + 31 + 16 * p0) + 64 * q : biasd + hr * NT + (DOFF - tq + p0) + 4 * q;
; #pragma unroll
;                             for (int kt = 0; kt < 4; ++kt)
; #pragma unroll
;                                 for (int r = 0; r < 4; ++r) sc[kt][r] += (MODE == 3) ? bia[kt][r] : ((MODE == 2) ? tp[256 * kt + 16 * r] : tp[16 * kt + r]);
;                         }
;                         const float bshift = far ? bfar : 0.f, boff = bshift * 1.4426950408889634f;
;                         float mx;
;                         { float m = fmaxf(fmaxf(sc[0][0], sc[0][1]), sc[0][2]);
;                           m = fmaxf(fmaxf(m, sc[0][3]), sc[1][0]); m = fmaxf(fmaxf(m, sc[1][1]), sc[1][2]); m = fmaxf(fmaxf(m, sc[1][3]), sc[2][0]);
;                           m = fmaxf(fmaxf(m, sc[2][1]), sc[2][2]); m = fmaxf(fmaxf(m, sc[2][3]), sc[3][0]); m = fmaxf(fmaxf(m, sc[3][1]), sc[3][2]); mx = fmaxf(m, sc[3][3]) + bshift; }
;                         if (MODE == 3 && !colsel) mx = -1e30f;
;                         float p[4][4];
;                         constexpr float L2E = 1.4426950408889634f;
;                         if (MODE == 2 && pass == 1) {
;                             const float negm1 = (mrun[qd] < -1e29f ? 0.f : -mrun[qd] * L2E) + boff + linv[qd];
; #pragma unroll
;                             for (int kt = 0; kt < 4; ++kt)
; #pragma unroll
;                                 for (int r = 0; r < 4; ++r) p[kt][r] = __builtin_amdgcn_exp2f(__builtin_fmaf(sc[kt][r], L2E, negm1));
.LBB0_1022:
	v_mfma_f32_16x16x32_bf16 v[90:93], v[90:93], v[2:5], 0
	v_fma_f32 v169, v150, s24, 0
	v_cmp_ngt_f32_e32 vcc, s30, v150
	v_mfma_f32_16x16x32_bf16 v[92:95], v[94:97], v[6:9], v[90:93]
	s_nop 0
	v_cndmask_b32_e32 v169, 0, v169, vcc
	v_fmamk_f32 v153, v153, 0x3fb8aa3b, v169
	v_fmamk_f32 v154, v154, 0x3fb8aa3b, v169
	v_mfma_f32_16x16x32_bf16 v[96:99], v[98:101], v[2:5], 0
	v_sub_u32_e32 v90, s6, v128
	v_fmamk_f32 v155, v155, 0x3fb8aa3b, v169
	v_fmamk_f32 v156, v156, 0x3fb8aa3b, v169
	v_mfma_f32_16x16x32_bf16 v[98:101], v[102:105], v[6:9], v[96:99]
	v_fmamk_f32 v157, v157, 0x3fb8aa3b, v169
	v_fmamk_f32 v158, v158, 0x3fb8aa3b, v169
	v_fmamk_f32 v159, v159, 0x3fb8aa3b, v169
	v_mfma_f32_16x16x32_bf16 v[102:105], v[106:109], v[2:5], 0
	v_fmamk_f32 v160, v160, 0x3fb8aa3b, v169
	v_exp_f32_e32 v153, v153
	v_exp_f32_e32 v154, v154
	v_mfma_f32_16x16x32_bf16 v[102:105], v[110:113], v[6:9], v[102:105]
	v_lshl_add_u32 v110, v90, 2, v143
	v_add_u32_e32 v90, 0xffc, v110
	ds_read2_b32 v[96:97], v90 offset1:1
	v_mfma_f32_16x16x32_bf16 v[106:109], v[114:117], v[2:5], 0
	v_exp_f32_e32 v155, v155
	v_exp_f32_e32 v156, v156
	v_exp_f32_e32 v157, v157
	s_waitcnt lgkmcnt(0)
	v_add_f32_e32 v91, v92, v96
	v_add_u32_e32 v92, 0x1004, v110
	v_add_f32_e32 v90, v93, v97
	ds_read2_b32 v[96:97], v92 offset1:1
	v_mfma_f32_16x16x32_bf16 v[106:109], v[118:121], v[6:9], v[106:109]
	v_exp_f32_e32 v158, v158
	v_exp_f32_e32 v159, v159
	v_exp_f32_e32 v160, v160
	s_waitcnt lgkmcnt(0)
	v_add_f32_e32 v93, v94, v96
	v_add_u32_e32 v94, 0x103c, v110
	v_add_f32_e32 v92, v95, v97
	ds_read2_b32 v[96:97], v94 offset1:1
	v_fmamk_f32 v161, v161, 0x3fb8aa3b, v169
	v_fmamk_f32 v162, v162, 0x3fb8aa3b, v169
	v_fmamk_f32 v163, v163, 0x3fb8aa3b, v169
	v_fmamk_f32 v164, v164, 0x3fb8aa3b, v169
	s_waitcnt lgkmcnt(0)
	v_add_f32_e32 v95, v98, v96
	v_add_u32_e32 v96, 0x1044, v110
	v_add_f32_e32 v94, v99, v97
	ds_read2_b32 v[96:97], v96 offset1:1
	v_fmamk_f32 v165, v165, 0x3fb8aa3b, v169
	v_fmamk_f32 v166, v166, 0x3fb8aa3b, v169
	v_fmamk_f32 v167, v167, 0x3fb8aa3b, v169
	v_fmac_f32_e32 v169, 0x3fb8aa3b, v168
	s_waitcnt lgkmcnt(0)
	v_add_f32_e32 v99, v100, v96
	v_add_u32_e32 v96, 0x107c, v110
	v_add_f32_e32 v98, v101, v97
	ds_read2_b32 v[96:97], v96 offset1:1
	v_exp_f32_e32 v161, v161
	v_exp_f32_e32 v162, v162
	v_exp_f32_e32 v163, v163
	v_exp_f32_e32 v164, v164
	s_waitcnt lgkmcnt(0)
	v_add_f32_e32 v101, v102, v96
	v_add_u32_e32 v96, 0x1084, v110
	v_add_f32_e32 v100, v103, v97
	ds_read2_b32 v[96:97], v96 offset1:1
	v_exp_f32_e32 v165, v165
	v_exp_f32_e32 v166, v166
	v_exp_f32_e32 v167, v167
	v_exp_f32_e32 v168, v169
	s_waitcnt lgkmcnt(0)
	v_add_f32_e32 v103, v104, v96
	v_add_u32_e32 v96, 0x10bc, v110
	v_add_f32_e32 v102, v105, v97
	ds_read2_b32 v[104:105], v96 offset1:1
	v_cvt_pk_bf16_f32 v170, v153, v154
	v_cvt_pk_bf16_f32 v171, v155, v156
	v_cvt_pk_bf16_f32 v172, v157, v158
	v_cvt_pk_bf16_f32 v173, v159, v160
	s_waitcnt lgkmcnt(0)
	v_add_f32_e32 v97, v106, v104
	v_add_u32_e32 v104, 0x10c4, v110
	v_add_f32_e32 v96, v107, v105
	ds_read2_b32 v[106:107], v104 offset1:1
	v_mfma_f32_16x16x32_bf16 v[30:33], v[86:89], v[170:173], v[30:33]
	s_waitcnt lgkmcnt(0)
	v_add_f32_e32 v105, v108, v106
	v_max_f32_e32 v106, v91, v90
	v_mfma_f32_16x16x32_bf16 v[18:21], v[82:85], v[170:173], v[18:21]
	v_max3_f32 v106, v106, v93, v92
	v_max3_f32 v106, v106, v95, v94
	v_max3_f32 v106, v106, v99, v98
	v_mfma_f32_16x16x32_bf16 v[14:17], v[78:81], v[170:173], v[14:17]
	v_max3_f32 v106, v106, v101, v100
	v_max3_f32 v106, v106, v103, v102
	v_add_f32_e32 v104, v109, v107
	v_mfma_f32_16x16x32_bf16 v[10:13], v[74:77], v[170:173], v[10:13]
	v_cvt_pk_bf16_f32 v170, v161, v162
	v_cvt_pk_bf16_f32 v171, v163, v164
	v_cvt_pk_bf16_f32 v172, v165, v166
	v_cvt_pk_bf16_f32 v173, v167, v168
	v_max3_f32 v106, v106, v97, v96
	v_max3_f32 v106, v106, v105, v104
	v_mfma_f32_16x16x32_bf16 v[30:33], v[70:73], v[170:173], v[30:33]
	v_add_f32_e32 v107, 0x40c00000, v149
	v_cmp_gt_f32_e32 vcc, v106, v107
	v_mfma_f32_16x16x32_bf16 v[18:21], v[66:69], v[170:173], v[18:21]
	v_mfma_f32_16x16x32_bf16 v[14:17], v[62:65], v[170:173], v[14:17]
	v_mfma_f32_16x16x32_bf16 v[10:13], v[58:61], v[170:173], v[10:13]
	s_cbranch_vccz .LBB0_1024
	v_add_f32_e32 v106, 0, v106
	ds_bpermute_b32 v107, v137, v106
	s_waitcnt lgkmcnt(0)
	v_max_f32_e32 v107, v107, v107
	v_max_f32_e32 v106, v106, v107
	ds_bpermute_b32 v107, v138, v106
	s_waitcnt lgkmcnt(0)
	v_max3_f32 v107, v149, v106, v107
	v_sub_f32_e32 v106, v149, v107
	v_mul_f32_e32 v106, 0x3fb8aa3b, v106
	v_exp_f32_e32 v106, v106
	v_mov_b32_e32 v149, v107
	v_mul_f32_e32 v151, v151, v106
	v_mul_f32_e32 v40, v40, v106
	v_mul_f32_e32 v41, v41, v106
	v_mul_f32_e32 v38, v38, v106
	v_mul_f32_e32 v39, v39, v106
	v_mul_f32_e32 v36, v36, v106
	v_mul_f32_e32 v37, v37, v106
	v_mul_f32_e32 v34, v34, v106
	v_mul_f32_e32 v35, v35, v106
	v_mul_f32_e32 v28, v28, v106
	v_mul_f32_e32 v29, v29, v106
	v_mul_f32_e32 v26, v26, v106
	v_mul_f32_e32 v27, v27, v106
	v_mul_f32_e32 v24, v24, v106
	v_mul_f32_e32 v25, v25, v106
	v_mul_f32_e32 v22, v22, v106
	v_mul_f32_e32 v23, v23, v106

; #define LAS __attribute__((address_space(3)))
;     ...
;                 __syncthreads();
; #pragma unroll
;                 for (int i = 0; i < TS; ++i) {
;                     *(LAS u32x4*)(L + AT_K + i * AT_TS + st_k) = kreg[i];
;                     if (do_pv) { const u32x2 lo = {vreg[i].x, vreg[i].y}, hi = {vreg[i].z, vreg[i].w};
;                         *(LAS u32x2*)(L + AT_V + i * AT_TS + st_va) = lo; *(LAS u32x2*)(L + AT_V + i * AT_TS + (st_va ^ 16)) = hi; } }
;                 if (rd + 1 < nrounds) AT_ISSUE(rd + 1);
;                 __syncthreads();
; #pragma unroll
;               for (int ts = 0; ts < TS; ++ts) {
;                 const int p0 = p0s[ts]; const int LK = AT_K + ts * AT_TS, LV = AT_V + ts * AT_TS;
;                 if (p0 < 0) continue;
;                 if (MODE == 0) { if (p0 > tw0 + TW - 1 || p0 + 63 < tw0 - 127) continue; }
;                 if (MODE == 1) { if (p0 > tw0 + TW - 1 || p0 + 63 < tw0 - 511) continue; }
;                 if (MODE == 2) { if (16 * p0 + 31 > tw0 + TW - 1) continue; }
;                 if (MODE == 3) { if (p0 > tw0 + TW - 1) continue; }
;                 const bool far = (MODE == 2) ? (tw0 - (16 * (p0 + 63) + 31) >= 790) : ((MODE == 3) ? (tw0 - (p0 + 63) >= 790) : false);
;                 const int jblk = p0 >> 6;
;                 bf16x8 akf[4][2]; bf16x8 avf[2][4];
;                 if (MODE != 3) {
; #pragma unroll
;                     for (int kt = 0; kt < 4; ++kt)
; #pragma unroll
;                         for (int ks = 0; ks < 2; ++ks) akf[kt][ks] = *(const LAS bf16x8*)(L + LK + (16 * kt + n) * 128 + ((((4 * ks + q) ^ n) & 7) << 4));
;                     if (do_pv) {
; #pragma unroll
;                         for (int st = 0; st < 2; ++st)
; #pragma unroll
;                             for (int dt = 0; dt < 4; ++dt) avf[st][dt] = *(const LAS bf16x8*)(L + LV + (16 * dt + n) * 128 + ((((4 * st + q) ^ n) & 7) << 4)); }
;                 }
;                 unsigned tokmask = 0u;
;                 if (MODE == 3) { tokmask = (unsigned)__ballot(lane < TW && ((selm[(wave * TW + (lane & (TW - 1))) * 8 + (jblk >> 5)] >> (jblk & 31)) & 1u)); if (tokmask == 0u) continue; }
; #pragma unroll
;                 for (int qd = 0; qd < NQ; ++qd) {
;                     const int tq = tw0 + 4 * qd + (n >> 2);
;                     if (DBG == 3) continue;
;                     bool colsel = true;
.LBB0_1025:
	s_cmp_lt_i32 s37, 0
	s_cselect_b64 s[8:9], -1, 0
	s_cmp_gt_i32 s36, s10
	s_cselect_b64 s[10:11], -1, 0
	s_or_b32 s6, s36, 63
	s_cmp_lt_i32 s6, s7
	s_cselect_b64 s[6:7], -1, 0
	s_or_b64 s[6:7], s[8:9], s[6:7]
	s_or_b64 s[6:7], s[6:7], s[10:11]
	s_and_b64 vcc, exec, s[6:7]
	s_barrier
	s_waitcnt vmcnt(1)
	ds_write_b128 v146, v[208:211]
	s_waitcnt vmcnt(0)
	ds_write_b64 v147, v[212:213] offset:8192
	ds_write_b64 v148, v[214:215] offset:8192
	s_waitcnt lgkmcnt(0)
	s_barrier
	s_cbranch_vccnz .LBB0_1000
	v_add_u32_e32 v50, v136, v140
	ds_read_b128 v[82:85], v50
	v_add_u32_e32 v51, v136, v141
	ds_read_b128 v[86:89], v51
	ds_read_b128 v[90:93], v50 offset:2048
	ds_read_b128 v[94:97], v51 offset:2048
	ds_read_b128 v[98:101], v50 offset:4096
	ds_read_b128 v[102:105], v51 offset:4096
	ds_read_b128 v[106:109], v50 offset:6144
	ds_read_b128 v[110:113], v51 offset:6144
	ds_read_b128 v[78:81], v50 offset:8192
	ds_read_b128 v[74:77], v50 offset:10240
	ds_read_b128 v[70:73], v50 offset:12288
	ds_read_b128 v[66:69], v50 offset:14336
	ds_read_b128 v[62:65], v51 offset:8192
	ds_read_b128 v[58:61], v51 offset:10240
	ds_read_b128 v[54:57], v51 offset:12288
	ds_read_b128 v[50:53], v51 offset:14336
	s_waitcnt lgkmcnt(13)
	v_mfma_f32_16x16x32_bf16 v[118:121], v[90:93], v[42:45], 0
	s_waitcnt lgkmcnt(11)
	v_mfma_f32_16x16x32_bf16 v[154:157], v[98:101], v[42:45], 0
	v_mfma_f32_16x16x32_bf16 v[114:117], v[82:85], v[42:45], 0
	s_waitcnt lgkmcnt(9)
	v_mfma_f32_16x16x32_bf16 v[42:45], v[106:109], v[42:45], 0
	s_waitcnt lgkmcnt(8)
	v_mfma_f32_16x16x32_bf16 v[158:161], v[110:113], v[46:49], v[42:45]
	v_mfma_f32_16x16x32_bf16 v[114:117], v[86:89], v[46:49], v[114:117]
	s_nop 4
	v_sub_u32_e32 v42, s36, v130
	v_lshl_add_u32 v153, v42, 2, v143
	v_add_u32_e32 v42, 0xffc, v153
	ds_read2_b32 v[42:43], v42 offset1:1
	v_add_u32_e32 v44, 0x1004, v153
	v_mfma_f32_16x16x32_bf16 v[118:121], v[94:97], v[46:49], v[118:121]
	ds_read2_b32 v[44:45], v44 offset1:1
	v_mfma_f32_16x16x32_bf16 v[154:157], v[102:105], v[46:49], v[154:157]
	v_add_u32_e32 v46, 0x103c, v153
	ds_read2_b32 v[46:47], v46 offset1:1
	v_add_u32_e32 v48, 0x1044, v153
	ds_read2_b32 v[48:49], v48 offset1:1
	s_waitcnt lgkmcnt(3)
	v_add_f32_e32 v42, v114, v42
	v_add_u32_e32 v114, 0x107c, v153
	v_add_f32_e32 v43, v115, v43
	s_waitcnt lgkmcnt(2)
	v_add_f32_e32 v44, v116, v44
	ds_read2_b32 v[114:115], v114 offset1:1
	v_add_u32_e32 v116, 0x1084, v153
	v_add_f32_e32 v45, v117, v45
	s_waitcnt lgkmcnt(2)
	v_add_f32_e32 v46, v118, v46
	ds_read2_b32 v[116:117], v116 offset1:1
	v_add_u32_e32 v118, 0x10bc, v153
	v_add_f32_e32 v47, v119, v47
	s_waitcnt lgkmcnt(2)
	v_add_f32_e32 v48, v120, v48
	ds_read2_b32 v[118:119], v118 offset1:1
	v_add_u32_e32 v120, 0x10c4, v153
	v_max_f32_e32 v153, v42, v43
	v_add_f32_e32 v49, v121, v49
	ds_read2_b32 v[120:121], v120 offset1:1
	v_max3_f32 v153, v153, v44, v45
	v_max3_f32 v153, v153, v46, v47
	s_waitcnt lgkmcnt(3)
	v_add_f32_e32 v114, v154, v114
	v_add_f32_e32 v115, v155, v115
	v_max3_f32 v153, v153, v48, v49
	s_waitcnt lgkmcnt(2)
	v_add_f32_e32 v116, v156, v116
	v_add_f32_e32 v117, v157, v117
	v_max3_f32 v153, v153, v114, v115
	s_waitcnt lgkmcnt(1)
	v_add_f32_e32 v118, v158, v118
	v_add_f32_e32 v119, v159, v119
	v_max3_f32 v153, v153, v116, v117
	s_waitcnt lgkmcnt(0)
	v_add_f32_e32 v120, v160, v120
	v_add_f32_e32 v121, v161, v121
	v_max3_f32 v153, v153, v118, v119
	v_max3_f32 v153, v153, v120, v121
	v_add_f32_e32 v154, 0x40c00000, v150
	v_cmp_gt_f32_e32 vcc, v153, v154
	s_cbranch_vccz .LBB0_1028
	v_add_f32_e32 v153, 0, v153
	ds_bpermute_b32 v154, v137, v153
	s_waitcnt lgkmcnt(0)
	v_max_f32_e32 v154, v154, v154
	v_max_f32_e32 v153, v153, v154
	ds_bpermute_b32 v154, v138, v153
	s_waitcnt lgkmcnt(0)
	v_max3_f32 v153, v150, v153, v154
	v_sub_f32_e32 v150, v150, v153
	v_mul_f32_e32 v150, 0x3fb8aa3b, v150
	v_exp_f32_e32 v150, v150
	s_nop 0
	v_mul_f32_e32 v152, v152, v150
	v_mul_f32_e32 v32, v32, v150
	v_mul_f32_e32 v33, v33, v150
	v_mul_f32_e32 v30, v30, v150
	v_mul_f32_e32 v31, v31, v150
	v_mul_f32_e32 v20, v20, v150
	v_mul_f32_e32 v21, v21, v150
	v_mul_f32_e32 v18, v18, v150
	v_mul_f32_e32 v19, v19, v150
	v_mul_f32_e32 v16, v16, v150
	v_mul_f32_e32 v17, v17, v150
	v_mul_f32_e32 v14, v14, v150
	v_mul_f32_e32 v15, v15, v150
	v_mul_f32_e32 v12, v12, v150
	v_mul_f32_e32 v13, v13, v150
	v_mul_f32_e32 v10, v10, v150
	v_mul_f32_e32 v11, v11, v150
	v_mov_b32_e32 v150, v153
;     ...
;                         for (int kt = 0; kt < 4; ++kt) { sc[kt] = (f32x4){0.f, 0.f, 0.f, 0.f};
; #pragma unroll
;                             for (int ks = 0; ks < 2; ++ks) { const bf16x8 ak = (MODE != 3) ? akf[kt][ks] : akq[kt][ks];
;                                 sc[kt] = __builtin_amdgcn_mfma_f32_16x16x32_bf16(ak, Bq[qd][ks], sc[kt], 0, 0, 0); } }
;                         if (MODE == 3) {
; #pragma unroll
;                             for (int st = 0; st < 2; ++st)
; #pragma unroll
;                                 for (int dt = 0; dt < 4; ++dt) avq[st][dt] = *(const LAS bf16x8*)(L + LV + (16 * dt + n) * 128 + ((((4 * st + q) ^ n) & 7) << 4));
;                             __builtin_amdgcn_sched_barrier(0);
;                         }
;                         if (!far) {
;                             const LAS float* tp = (MODE == 2) ? biasd + hr * NT + (DOFF - tq + 31 + 16 * p0) + 64 * q : biasd + hr * NT + (DOFF - tq + p0) + 4 * q;
; #pragma unroll
;                             for (int kt = 0; kt < 4; ++kt)
; #pragma unroll
;                                 for (int r = 0; r < 4; ++r) sc[kt][r] += (MODE == 3) ? bia[kt][r] : ((MODE == 2) ? tp[256 * kt + 16 * r] : tp[16 * kt + r]);
;                         }
;                         const float bshift = far ? bfar : 0.f, boff = bshift * 1.4426950408889634f;
;                         float mx;
;                         { float m = fmaxf(fmaxf(sc[0][0], sc[0][1]), sc[0][2]);
;                           m = fmaxf(fmaxf(m, sc[0][3]), sc[1][0]); m = fmaxf(fmaxf(m, sc[1][1]), sc[1][2]); m = fmaxf(fmaxf(m, sc[1][3]), sc[2][0]);
;                           m = fmaxf(fmaxf(m, sc[2][1]), sc[2][2]); m = fmaxf(fmaxf(m, sc[2][3]), sc[3][0]); m = fmaxf(fmaxf(m, sc[3][1]), sc[3][2]); mx = fmaxf(m, sc[3][3]) + bshift; }
;                         if (MODE == 3 && !colsel) mx = -1e30f;
;                         float p[4][4];
;                         constexpr float L2E = 1.4426950408889634f;
;                         if (MODE == 2 && pass == 1) {
;                             const float negm1 = (mrun[qd] < -1e29f ? 0.f : -mrun[qd] * L2E) + boff + linv[qd];
; #pragma unroll
;                             for (int kt = 0; kt < 4; ++kt)
; #pragma unroll
;                                 for (int r = 0; r < 4; ++r) p[kt][r] = __builtin_amdgcn_exp2f(__builtin_fmaf(sc[kt][r], L2E, negm1));
.LBB0_1028:
	v_mfma_f32_16x16x32_bf16 v[82:85], v[82:85], v[2:5], 0
	v_fma_f32 v153, v150, s24, 0
	v_cmp_ngt_f32_e32 vcc, s30, v150
	v_mfma_f32_16x16x32_bf16 v[82:85], v[86:89], v[6:9], v[82:85]
	s_nop 0
	v_cndmask_b32_e32 v153, 0, v153, vcc
	v_fmamk_f32 v42, v42, 0x3fb8aa3b, v153
	v_fmamk_f32 v43, v43, 0x3fb8aa3b, v153
	v_mfma_f32_16x16x32_bf16 v[86:89], v[90:93], v[2:5], 0
	v_fmamk_f32 v44, v44, 0x3fb8aa3b, v153
	v_fmamk_f32 v45, v45, 0x3fb8aa3b, v153
	v_fmamk_f32 v46, v46, 0x3fb8aa3b, v153
	v_mfma_f32_16x16x32_bf16 v[90:93], v[98:101], v[2:5], 0
	v_fmamk_f32 v47, v47, 0x3fb8aa3b, v153
	v_fmamk_f32 v48, v48, 0x3fb8aa3b, v153
	v_fmamk_f32 v49, v49, 0x3fb8aa3b, v153
	v_mfma_f32_16x16x32_bf16 v[2:5], v[106:109], v[2:5], 0
	v_exp_f32_e32 v42, v42
	v_exp_f32_e32 v43, v43
	v_exp_f32_e32 v44, v44
	v_mfma_f32_16x16x32_bf16 v[86:89], v[94:97], v[6:9], v[86:89]
	v_exp_f32_e32 v45, v45
	v_exp_f32_e32 v46, v46
	v_exp_f32_e32 v47, v47
	v_mfma_f32_16x16x32_bf16 v[94:97], v[110:113], v[6:9], v[2:5]
	v_exp_f32_e32 v48, v48
	v_exp_f32_e32 v49, v49
	v_fmamk_f32 v114, v114, 0x3fb8aa3b, v153
	v_sub_u32_e32 v2, s36, v128
	v_lshl_add_u32 v98, v2, 2, v143
	v_add_u32_e32 v2, 0xffc, v98
	ds_read2_b32 v[4:5], v2 offset1:1
	v_mfma_f32_16x16x32_bf16 v[90:93], v[102:105], v[6:9], v[90:93]
	v_fmamk_f32 v115, v115, 0x3fb8aa3b, v153
	v_fmamk_f32 v116, v116, 0x3fb8aa3b, v153
	v_fmamk_f32 v117, v117, 0x3fb8aa3b, v153
	s_waitcnt lgkmcnt(0)
	v_add_f32_e32 v3, v82, v4
	v_add_u32_e32 v4, 0x1004, v98
	ds_read2_b32 v[6:7], v4 offset1:1
	v_add_f32_e32 v2, v83, v5
	v_fmamk_f32 v118, v118, 0x3fb8aa3b, v153
	v_fmamk_f32 v119, v119, 0x3fb8aa3b, v153
	v_fmamk_f32 v120, v120, 0x3fb8aa3b, v153
	s_waitcnt lgkmcnt(0)
	v_add_f32_e32 v5, v84, v6
	v_add_u32_e32 v6, 0x103c, v98
	ds_read2_b32 v[8:9], v6 offset1:1
	v_add_f32_e32 v4, v85, v7
	v_fmac_f32_e32 v153, 0x3fb8aa3b, v121
	v_exp_f32_e32 v114, v114
	v_exp_f32_e32 v115, v115
	s_waitcnt lgkmcnt(0)
	v_add_f32_e32 v7, v86, v8
	v_add_u32_e32 v8, 0x1044, v98
	v_add_f32_e32 v6, v87, v9
	ds_read2_b32 v[8:9], v8 offset1:1
	v_exp_f32_e32 v116, v116
	v_exp_f32_e32 v117, v117
	v_exp_f32_e32 v118, v118
	v_exp_f32_e32 v119, v119
	s_waitcnt lgkmcnt(0)
	v_add_f32_e32 v83, v88, v8
	v_add_u32_e32 v8, 0x107c, v98
	v_add_f32_e32 v82, v89, v9
	ds_read2_b32 v[8:9], v8 offset1:1
	v_exp_f32_e32 v120, v120
	v_exp_f32_e32 v121, v153
	v_cvt_pk_bf16_f32 v154, v42, v43
	v_cvt_pk_bf16_f32 v155, v44, v45
	s_waitcnt lgkmcnt(0)
	v_add_f32_e32 v85, v90, v8
	v_add_u32_e32 v8, 0x1084, v98
	v_add_f32_e32 v84, v91, v9
	ds_read2_b32 v[8:9], v8 offset1:1
	v_cvt_pk_bf16_f32 v156, v46, v47
	v_cvt_pk_bf16_f32 v157, v48, v49
	s_waitcnt lgkmcnt(0)
	v_add_f32_e32 v87, v92, v8
	v_add_u32_e32 v8, 0x10bc, v98
	ds_read2_b32 v[88:89], v8 offset1:1
	v_add_f32_e32 v86, v93, v9
	v_mfma_f32_16x16x32_bf16 v[30:33], v[78:81], v[154:157], v[30:33]
	s_waitcnt lgkmcnt(0)
	v_add_f32_e32 v9, v94, v88
	v_add_u32_e32 v88, 0x10c4, v98
	ds_read2_b32 v[90:91], v88 offset1:1
	v_add_f32_e32 v8, v95, v89
	v_mfma_f32_16x16x32_bf16 v[18:21], v[74:77], v[154:157], v[18:21]
	s_waitcnt lgkmcnt(0)
	v_add_f32_e32 v89, v96, v90
	v_max_f32_e32 v90, v3, v2
	v_mfma_f32_16x16x32_bf16 v[14:17], v[70:73], v[154:157], v[14:17]
	v_max3_f32 v90, v90, v5, v4
	v_max3_f32 v90, v90, v7, v6
	v_max3_f32 v90, v90, v83, v82
	v_mfma_f32_16x16x32_bf16 v[10:13], v[66:69], v[154:157], v[10:13]
	v_cvt_pk_bf16_f32 v154, v114, v115
	v_cvt_pk_bf16_f32 v155, v116, v117
	v_cvt_pk_bf16_f32 v156, v118, v119
	v_cvt_pk_bf16_f32 v157, v120, v121
	v_max3_f32 v90, v90, v85, v84
	v_max3_f32 v90, v90, v87, v86
	v_mfma_f32_16x16x32_bf16 v[30:33], v[62:65], v[154:157], v[30:33]
	v_add_f32_e32 v88, v97, v91
	v_max3_f32 v90, v90, v9, v8
	v_max3_f32 v90, v90, v89, v88
	v_mfma_f32_16x16x32_bf16 v[18:21], v[58:61], v[154:157], v[18:21]
	v_add_f32_e32 v91, 0x40c00000, v149
	v_cmp_gt_f32_e32 vcc, v90, v91
	v_mfma_f32_16x16x32_bf16 v[14:17], v[54:57], v[154:157], v[14:17]
	v_mfma_f32_16x16x32_bf16 v[10:13], v[50:53], v[154:157], v[10:13]
	s_cbranch_vccz .LBB0_999
	v_add_f32_e32 v90, 0, v90
	ds_bpermute_b32 v91, v137, v90
	s_waitcnt lgkmcnt(0)
	v_max_f32_e32 v91, v91, v91
	v_max_f32_e32 v90, v90, v91
	ds_bpermute_b32 v91, v138, v90
	s_waitcnt lgkmcnt(0)
	v_max3_f32 v91, v149, v90, v91
	v_sub_f32_e32 v90, v149, v91
	v_mul_f32_e32 v90, 0x3fb8aa3b, v90
	v_exp_f32_e32 v90, v90
	v_mov_b32_e32 v149, v91
	v_mul_f32_e32 v151, v151, v90
	v_mul_f32_e32 v40, v40, v90
	v_mul_f32_e32 v41, v41, v90
	v_mul_f32_e32 v38, v38, v90
	v_mul_f32_e32 v39, v39, v90
	v_mul_f32_e32 v36, v36, v90
	v_mul_f32_e32 v37, v37, v90
	v_mul_f32_e32 v34, v34, v90
	v_mul_f32_e32 v35, v35, v90
	v_mul_f32_e32 v28, v28, v90
	v_mul_f32_e32 v29, v29, v90
	v_mul_f32_e32 v26, v26, v90
	v_mul_f32_e32 v27, v27, v90
	v_mul_f32_e32 v24, v24, v90
	v_mul_f32_e32 v25, v25, v90
	v_mul_f32_e32 v22, v22, v90
	v_mul_f32_e32 v23, v23, v90
	s_branch .LBB0_999

; __device__ __forceinline__ float bf2f(unsigned v) { return __uint_as_float(v << 16); }
; __device__ __forceinline__ unsigned pk2(float lo, float hi) { const f32x2 f = {lo, hi}; const bf16n2 v = __builtin_convertvector(f, bf16n2); return __builtin_bit_cast(unsigned, v); }
; __device__ __forceinline__ float sigmoidf_(float x) { return __builtin_amdgcn_rcpf(1.0f + __expf(-x)); }
; __device__ __forceinline__ f32x4 unpack4(u32x2 z) { return (f32x4){__uint_as_float(z.x << 16), __uint_as_float(z.x & 0xffff0000u), __uint_as_float(z.y << 16), __uint_as_float(z.y & 0xffff0000u)}; }
;     ...
; #pragma unroll
;         for (int qd = 0; qd < NQ; ++qd) {
;             const int tq = tw0 + 4 * qd + (n >> 2), hh = g * 4 + hr;
;             f32x4 accp[4]; u32x2 winp[4];
;             if (MODE == 3) {
; #pragma unroll
;                 for (int dt = 0; dt < 4; ++dt) { const int col = hh * 64 + 16 * dt + 4 * q; accp[dt] = unpack4(*(const u32x2*)((const bf16_t*)nsaacc + (size_t)tq * 512 + col)); winp[dt] = *(const u32x2*)(oout + (size_t)tq * 512 + col); } }
;             float scale;
;             if (MODE == 2) scale = 1.0f;
;             else { float lt = lrun[qd]; lt += __shfl_xor(lt, 16); lt += __shfl_xor(lt, 32);
;                 if (MODE == 0) { const float sink = sinkv; const float mf = fmaxf(mrun[qd], sink), cr = __expf(mrun[qd] - mf); scale = cr / (lt * cr + __expf(sink - mf)); }
;                 else scale = lt > 0.f ? 1.0f / lt : 0.f; }
;             if (MODE != 0) scale *= sigmoidf_(bf2f(graw[qd]));
; #pragma unroll
;             for (int dt = 0; dt < 4; ++dt) { const f32x4 o = O[qd][dt] * scale; const int col = hh * 64 + 16 * dt + 4 * q;
;                 if (MODE == 0 || MODE == 1) { u32x2 w; w.x = pk2(o[0], o[1]); w.y = pk2(o[2], o[3]); *(u32x2*)(oout + (size_t)tq * 512 + col) = w; }
;                 else if (MODE == 2) { u32x2 w; w.x = pk2(o[0], o[1]); w.y = pk2(o[2], o[3]); *(u32x2*)((bf16_t*)nsaacc + (size_t)tq * 512 + col) = w; }
;                 else { const f32x4 t2 = (accp[dt] + unpack4(winp[dt])) + o; u32x2 w; w.x = pk2(t2[0], t2[1]); w.y = pk2(t2[2], t2[3]); *(u32x2*)(oout + (size_t)tq * 512 + col) = w; } }
;         }
.LBB0_1034:
	ds_bpermute_b32 v35, v144, v137
	ds_bpermute_b32 v34, v144, v136
	v_lshlrev_b32_e32 v37, 16, v156
	v_mul_f32_e32 v37, 0xbfb8aa3b, v37
	v_exp_f32_e32 v37, v37
	v_or_b32_e32 v36, s6, v122
	s_waitcnt lgkmcnt(0)
	v_add_f32_e32 v34, v136, v34
	v_add_f32_e32 v35, v137, v35
	ds_bpermute_b32 v39, v145, v35
	ds_bpermute_b32 v38, v145, v34
	v_lshl_or_b32 v36, v36, 6, v146
	v_add_f32_e32 v37, 1.0, v37
	v_rcp_f32_e32 v42, v37
	v_lshlrev_b64 v[40:41], 10, v[134:135]
	s_waitcnt lgkmcnt(0)
	v_add_f32_e32 v34, v34, v38
	v_add_f32_e32 v35, v35, v39
	v_ashrrev_i32_e32 v37, 31, v36
	v_div_scale_f32 v43, s[6:7], v35, v35, 1.0
	v_rcp_f32_e32 v44, v43
	v_lshl_add_u64 v[40:41], s[88:89], 0, v[40:41]
	v_lshlrev_b64 v[36:37], 1, v[36:37]
	v_lshl_add_u64 v[38:39], v[40:41], 0, v[36:37]
	v_fma_f32 v40, -v43, v44, 1.0
	v_fmac_f32_e32 v44, v40, v44
	v_div_scale_f32 v40, vcc, 1.0, v35, 1.0
	v_mul_f32_e32 v41, v40, v44
	v_fma_f32 v45, -v43, v41, v40
	v_fmac_f32_e32 v41, v45, v44
	v_fma_f32 v40, -v43, v41, v40
	v_div_fmas_f32 v40, v40, v44, v41
	v_div_fixup_f32 v40, v40, v35, 1.0
	v_cmp_lt_f32_e32 vcc, 0, v35
	s_add_i32 s22, s22, s74
	s_cmp_ge_i32 s22, s27
	v_cndmask_b32_e32 v35, 0, v40, vcc
	v_mul_f32_e32 v40, v42, v35
	v_mul_f32_e32 v24, v24, v40
	v_mul_f32_e32 v25, v25, v40
	v_mul_f32_e32 v22, v22, v40
	v_mul_f32_e32 v23, v23, v40
	v_mul_f32_e32 v20, v20, v40
	v_mul_f32_e32 v21, v21, v40
	v_cvt_pk_bf16_f32 v22, v22, v23
	v_cvt_pk_bf16_f32 v23, v24, v25
	global_store_dwordx2 v[38:39], v[22:23], off offset:64
	v_div_scale_f32 v22, s[6:7], v34, v34, 1.0
	v_rcp_f32_e32 v23, v22
	v_mul_f32_e32 v18, v18, v40
	v_mul_f32_e32 v19, v19, v40
	v_mul_f32_e32 v32, v32, v40
	v_mul_f32_e32 v33, v33, v40
	v_cvt_pk_bf16_f32 v18, v18, v19
	v_cvt_pk_bf16_f32 v19, v20, v21
	global_store_dwordx2 v[38:39], v[18:19], off offset:96
	v_fma_f32 v18, -v22, v23, 1.0
	v_fmac_f32_e32 v23, v18, v23
	v_div_scale_f32 v18, vcc, 1.0, v34, 1.0
	v_mul_f32_e32 v19, v18, v23
	v_fma_f32 v20, -v22, v19, v18
	v_fmac_f32_e32 v19, v20, v23
	v_lshlrev_b32_e32 v20, 16, v129
	v_mul_f32_e32 v20, 0xbfb8aa3b, v20
	v_exp_f32_e32 v20, v20
	v_fma_f32 v18, -v22, v19, v18
	v_div_fmas_f32 v18, v18, v23, v19
	v_div_fixup_f32 v18, v18, v34, 1.0
	v_add_f32_e32 v19, 1.0, v20
	v_rcp_f32_e32 v19, v19
	v_cmp_lt_f32_e32 vcc, 0, v34
	v_lshlrev_b64 v[20:21], 10, v[132:133]
	v_mul_f32_e32 v30, v30, v40
	v_mul_f32_e32 v31, v31, v40
	v_cndmask_b32_e32 v18, 0, v18, vcc
	v_mul_f32_e32 v18, v19, v18
	v_mul_f32_e32 v28, v28, v40
	v_mul_f32_e32 v29, v29, v40
	v_mul_f32_e32 v26, v26, v40
	v_mul_f32_e32 v27, v27, v40
	v_lshl_add_u64 v[20:21], s[88:89], 0, v[20:21]
	v_mul_f32_e32 v16, v16, v18
	v_mul_f32_e32 v17, v17, v18
	v_mul_f32_e32 v14, v14, v18
	v_mul_f32_e32 v15, v15, v18
	v_mul_f32_e32 v12, v12, v18
	v_mul_f32_e32 v13, v13, v18
	v_mul_f32_e32 v10, v10, v18
	v_mul_f32_e32 v11, v11, v18
	v_mul_f32_e32 v8, v8, v18
	v_mul_f32_e32 v9, v9, v18
	v_mul_f32_e32 v6, v6, v18
	v_mul_f32_e32 v7, v7, v18
	v_mul_f32_e32 v4, v4, v18
	v_mul_f32_e32 v5, v5, v18
	v_mul_f32_e32 v2, v2, v18
	v_mul_f32_e32 v3, v3, v18
	v_cvt_pk_bf16_f32 v30, v30, v31
	v_cvt_pk_bf16_f32 v31, v32, v33
	v_cvt_pk_bf16_f32 v26, v26, v27
	v_cvt_pk_bf16_f32 v27, v28, v29
	v_cvt_pk_bf16_f32 v14, v14, v15
	v_cvt_pk_bf16_f32 v15, v16, v17
	v_lshl_add_u64 v[16:17], v[20:21], 0, v[36:37]
	v_cvt_pk_bf16_f32 v10, v10, v11
	v_cvt_pk_bf16_f32 v11, v12, v13
	v_cvt_pk_bf16_f32 v6, v6, v7
	v_cvt_pk_bf16_f32 v7, v8, v9
	v_cvt_pk_bf16_f32 v2, v2, v3
	v_cvt_pk_bf16_f32 v3, v4, v5
	global_store_dwordx2 v[38:39], v[30:31], off
	global_store_dwordx2 v[38:39], v[26:27], off offset:32
	global_store_dwordx2 v[16:17], v[14:15], off
	global_store_dwordx2 v[16:17], v[10:11], off offset:32
	global_store_dwordx2 v[16:17], v[6:7], off offset:64
	global_store_dwordx2 v[16:17], v[2:3], off offset:96
	s_cbranch_scc1 .LBB0_987

;     ...
;             for (int rd = 0; rd < nrounds; ++rd) {
;                 int p0s[TS];
; #pragma unroll
;                 for (int i = 0; i < TS; ++i) p0s[i] = p0n[i];
;                 __syncthreads();
; #pragma unroll
;                 for (int i = 0; i < TS; ++i) {
;                     *(LAS u32x4*)(L + AT_K + i * AT_TS + st_k) = kreg[i];
;                     if (do_pv) { const u32x2 lo = {vreg[i].x, vreg[i].y}, hi = {vreg[i].z, vreg[i].w};
;                         *(LAS u32x2*)(L + AT_V + i * AT_TS + st_va) = lo; *(LAS u32x2*)(L + AT_V + i * AT_TS + (st_va ^ 16)) = hi; } }
;                 if (rd + 1 < nrounds) AT_ISSUE(rd + 1);
;                 __syncthreads();
; #pragma unroll
;               for (int ts = 0; ts < TS; ++ts) {
;                 const int p0 = p0s[ts]; const int LK = AT_K + ts * AT_TS, LV = AT_V + ts * AT_TS;
;                 if (p0 < 0) continue;
;                 if (MODE == 0) { if (p0 > tw0 + TW - 1 || p0 + 63 < tw0 - 127) continue; }
;                 if (MODE == 1) { if (p0 > tw0 + TW - 1 || p0 + 63 < tw0 - 511) continue; }
;                 if (MODE == 2) { if (16 * p0 + 31 > tw0 + TW - 1) continue; }
;                 if (MODE == 3) { if (p0 > tw0 + TW - 1) continue; }
;                 const bool far = (MODE == 2) ? (tw0 - (16 * (p0 + 63) + 31) >= 790) : ((MODE == 3) ? (tw0 - (p0 + 63) >= 790) : false);
;                 const int jblk = p0 >> 6;
;                 bf16x8 akf[4][2]; bf16x8 avf[2][4];
;                 if (MODE != 3) {
; #pragma unroll
;                     for (int kt = 0; kt < 4; ++kt)
; #pragma unroll
;                         for (int ks = 0; ks < 2; ++ks) akf[kt][ks] = *(const LAS bf16x8*)(L + LK + (16 * kt + n) * 128 + ((((4 * ks + q) ^ n) & 7) << 4));
;                     if (do_pv) {
; #pragma unroll
;                         for (int st = 0; st < 2; ++st)
; #pragma unroll
;                             for (int dt = 0; dt < 4; ++dt) avf[st][dt] = *(const LAS bf16x8*)(L + LV + (16 * dt + n) * 128 + ((((4 * st + q) ^ n) & 7) << 4)); }
;     ...
;                         for (int kt = 0; kt < 4; ++kt) { sc[kt] = (f32x4){0.f, 0.f, 0.f, 0.f};
; #pragma unroll
;                             for (int ks = 0; ks < 2; ++ks) { const bf16x8 ak = (MODE != 3) ? akf[kt][ks] : akq[kt][ks];
;                                 sc[kt] = __builtin_amdgcn_mfma_f32_16x16x32_bf16(ak, Bq[qd][ks], sc[kt], 0, 0, 0); } }
.LBB0_1047:
	s_mov_b32 s9, s7
	s_add_i32 s7, s7, 64
	s_add_i32 s42, s7, 64
	s_max_i32 s42, s42, 0
	s_lshl_b64 s[10:11], s[42:43], 13
	s_lshl_b32 s42, s42, 1
	s_waitcnt lgkmcnt(0)
	s_barrier
	s_waitcnt vmcnt(3)
	ds_write_b128 v153, v[54:57]
	s_waitcnt vmcnt(2)
	ds_write_b64 v154, v[50:51] offset:8192
	ds_write_b64 v155, v[52:53] offset:8192
	v_lshl_add_u64 v[50:51], v[138:139], 0, s[10:11]
	v_lshl_add_u64 v[52:53], v[140:141], 0, s[42:43]
	global_load_dwordx4 v[54:57], v[50:51], off
	s_nop 0
	global_load_dwordx4 v[50:53], v[52:53], off
	s_cmp_lt_i32 s9, 0
	s_cselect_b64 s[10:11], -1, 0
	s_cmp_gt_i32 s9, s13
	s_cselect_b64 s[14:15], -1, 0
	s_add_i32 s9, s9, 63
	s_cmp_lt_i32 s9, s12
	s_cselect_b64 s[16:17], -1, 0
	s_or_b64 s[10:11], s[10:11], s[16:17]
	s_or_b64 s[10:11], s[10:11], s[14:15]
	s_and_b64 vcc, exec, s[10:11]
	s_waitcnt lgkmcnt(0)
	s_barrier
	s_cbranch_vccnz .LBB0_1046
	v_add_u32_e32 v58, v143, v147
	ds_read_b128 v[90:93], v58
	v_add_u32_e32 v59, v143, v148
	ds_read_b128 v[94:97], v59
	ds_read_b128 v[98:101], v58 offset:2048
	ds_read_b128 v[102:105], v59 offset:2048
	ds_read_b128 v[106:109], v58 offset:4096
	ds_read_b128 v[110:113], v59 offset:4096
	ds_read_b128 v[114:117], v58 offset:6144
	ds_read_b128 v[118:121], v59 offset:6144
	ds_read_b128 v[86:89], v58 offset:8192
	ds_read_b128 v[82:85], v58 offset:10240
	ds_read_b128 v[78:81], v58 offset:12288
	ds_read_b128 v[74:77], v58 offset:14336
	ds_read_b128 v[70:73], v59 offset:8192
	ds_read_b128 v[66:69], v59 offset:10240
	ds_read_b128 v[62:65], v59 offset:12288
	ds_read_b128 v[58:61], v59 offset:14336
	s_waitcnt lgkmcnt(13)
	v_mfma_f32_16x16x32_bf16 v[164:167], v[98:101], v[42:45], 0
	s_waitcnt lgkmcnt(12)
	v_mfma_f32_16x16x32_bf16 v[164:167], v[102:105], v[46:49], v[164:167]
	v_mfma_f32_16x16x32_bf16 v[158:161], v[90:93], v[42:45], 0
	v_mfma_f32_16x16x32_bf16 v[160:163], v[94:97], v[46:49], v[158:161]
	s_waitcnt lgkmcnt(11)
	v_mfma_f32_16x16x32_bf16 v[168:171], v[106:109], v[42:45], 0
	s_nop 4
	v_add_u32_e32 v158, s8, v152
	v_add_u32_e32 v159, 0x207fc, v158
	ds_read2_b32 v[176:177], v159 offset1:1
	s_waitcnt lgkmcnt(11)
	v_mfma_f32_16x16x32_bf16 v[168:171], v[110:113], v[46:49], v[168:171]
	s_waitcnt lgkmcnt(0)
	v_add_f32_e32 v159, v160, v176
	v_add_f32_e32 v160, v161, v177
	v_add_u32_e32 v161, 0x20804, v158
	ds_read2_b32 v[176:177], v161 offset1:1
	v_mfma_f32_16x16x32_bf16 v[172:175], v[114:117], v[42:45], 0
	s_waitcnt lgkmcnt(0)
	v_add_f32_e32 v161, v162, v176
	v_add_f32_e32 v162, v163, v177
	v_add_u32_e32 v163, 0x2083c, v158
	ds_read2_b32 v[176:177], v163 offset1:1
	v_mfma_f32_16x16x32_bf16 v[172:175], v[118:121], v[46:49], v[172:175]
	s_waitcnt lgkmcnt(0)
	v_add_f32_e32 v163, v164, v176
	v_add_f32_e32 v164, v165, v177
	v_add_u32_e32 v165, 0x20844, v158
	ds_read2_b32 v[176:177], v165 offset1:1
	s_waitcnt lgkmcnt(0)
	v_add_f32_e32 v165, v166, v176
	v_add_f32_e32 v166, v167, v177
	v_add_u32_e32 v167, 0x2087c, v158
	ds_read2_b32 v[176:177], v167 offset1:1
	s_waitcnt lgkmcnt(0)
	v_add_f32_e32 v167, v168, v176
	v_add_f32_e32 v168, v169, v177
	v_add_u32_e32 v169, 0x20884, v158
	ds_read2_b32 v[176:177], v169 offset1:1
	s_waitcnt lgkmcnt(0)
	v_add_f32_e32 v169, v170, v176
	v_add_f32_e32 v170, v171, v177
	v_add_u32_e32 v171, 0x208bc, v158
	ds_read2_b32 v[176:177], v171 offset1:1
	s_waitcnt lgkmcnt(0)
	v_add_f32_e32 v171, v172, v176
	v_add_f32_e32 v172, v173, v177
	v_add_u32_e32 v173, 0x208c4, v158
	ds_read2_b32 v[176:177], v173 offset1:1
	s_waitcnt lgkmcnt(0)
	v_add_f32_e32 v173, v174, v176
	v_add_f32_e32 v174, v175, v177
	v_max_f32_e32 v175, v159, v160
	v_max3_f32 v175, v175, v161, v162
	v_max3_f32 v175, v175, v163, v164
	v_max3_f32 v175, v175, v165, v166
	v_max3_f32 v175, v175, v167, v168
	v_max3_f32 v175, v175, v169, v170
	v_max3_f32 v175, v175, v171, v172
	v_max3_f32 v175, v175, v173, v174
	v_add_f32_e32 v176, 0x40c00000, v157
	v_cmp_gt_f32_e32 vcc, v175, v176
	s_cbranch_vccz .LBB0_1050
	v_add_f32_e32 v175, 0, v175
	ds_bpermute_b32 v176, v144, v175
	s_waitcnt lgkmcnt(0)
	v_max_f32_e32 v176, v176, v176
	v_max_f32_e32 v175, v175, v176
	ds_bpermute_b32 v176, v145, v175
	s_waitcnt lgkmcnt(0)
	v_max3_f32 v175, v157, v175, v176
	v_sub_f32_e32 v157, v157, v175
	v_mul_f32_e32 v157, 0x3fb8aa3b, v157
	v_exp_f32_e32 v176, v157
	v_mov_b32_e32 v157, v175
	v_mul_f32_e32 v137, v137, v176
	v_mul_f32_e32 v32, v32, v176
	v_mul_f32_e32 v33, v33, v176
	v_mul_f32_e32 v30, v30, v176
	v_mul_f32_e32 v31, v31, v176
	v_mul_f32_e32 v28, v28, v176
	v_mul_f32_e32 v29, v29, v176
	v_mul_f32_e32 v26, v26, v176
	v_mul_f32_e32 v27, v27, v176
	v_mul_f32_e32 v24, v24, v176
	v_mul_f32_e32 v25, v25, v176
	v_mul_f32_e32 v22, v22, v176
	v_mul_f32_e32 v23, v23, v176
	v_mul_f32_e32 v20, v20, v176
	v_mul_f32_e32 v21, v21, v176
	v_mul_f32_e32 v18, v18, v176
	v_mul_f32_e32 v19, v19, v176
;     ...
;                         for (int kt = 0; kt < 4; ++kt) { sc[kt] = (f32x4){0.f, 0.f, 0.f, 0.f};
; #pragma unroll
;                             for (int ks = 0; ks < 2; ++ks) { const bf16x8 ak = (MODE != 3) ? akf[kt][ks] : akq[kt][ks];
;                                 sc[kt] = __builtin_amdgcn_mfma_f32_16x16x32_bf16(ak, Bq[qd][ks], sc[kt], 0, 0, 0); } }
;                         if (MODE == 3) {
; #pragma unroll
;                             for (int st = 0; st < 2; ++st)
; #pragma unroll
;                                 for (int dt = 0; dt < 4; ++dt) avq[st][dt] = *(const LAS bf16x8*)(L + LV + (16 * dt + n) * 128 + ((((4 * st + q) ^ n) & 7) << 4));
;                             __builtin_amdgcn_sched_barrier(0);
;                         }
;                         if (!far) {
;                             const LAS float* tp = (MODE == 2) ? biasd + hr * NT + (DOFF - tq + 31 + 16 * p0) + 64 * q : biasd + hr * NT + (DOFF - tq + p0) + 4 * q;
; #pragma unroll
;                             for (int kt = 0; kt < 4; ++kt)
; #pragma unroll
;                                 for (int r = 0; r < 4; ++r) sc[kt][r] += (MODE == 3) ? bia[kt][r] : ((MODE == 2) ? tp[256 * kt + 16 * r] : tp[16 * kt + r]);
;                         }
;                         const float bshift = far ? bfar : 0.f, boff = bshift * 1.4426950408889634f;
;                         float mx;
;                         { float m = fmaxf(fmaxf(sc[0][0], sc[0][1]), sc[0][2]);
;                           m = fmaxf(fmaxf(m, sc[0][3]), sc[1][0]); m = fmaxf(fmaxf(m, sc[1][1]), sc[1][2]); m = fmaxf(fmaxf(m, sc[1][3]), sc[2][0]);
;                           m = fmaxf(fmaxf(m, sc[2][1]), sc[2][2]); m = fmaxf(fmaxf(m, sc[2][3]), sc[3][0]); m = fmaxf(fmaxf(m, sc[3][1]), sc[3][2]); mx = fmaxf(m, sc[3][3]) + bshift; }
;                         if (MODE == 3 && !colsel) mx = -1e30f;
;                         float p[4][4];
;                         constexpr float L2E = 1.4426950408889634f;
;                         if (MODE == 2 && pass == 1) {
;                             const float negm1 = (mrun[qd] < -1e29f ? 0.f : -mrun[qd] * L2E) + boff + linv[qd];
; #pragma unroll
;                             for (int kt = 0; kt < 4; ++kt)
; #pragma unroll
;                                 for (int r = 0; r < 4; ++r) p[kt][r] = __builtin_amdgcn_exp2f(__builtin_fmaf(sc[kt][r], L2E, negm1));
.LBB0_1050:
	v_mfma_f32_16x16x32_bf16 v[90:93], v[90:93], v[34:37], 0
	v_fma_f32 v175, v157, s24, 0
	v_cmp_ngt_f32_e32 vcc, s30, v157
	v_mfma_f32_16x16x32_bf16 v[92:95], v[94:97], v[38:41], v[90:93]
	s_nop 0
	v_cndmask_b32_e32 v175, 0, v175, vcc
	v_fmamk_f32 v159, v159, 0x3fb8aa3b, v175
	v_fmamk_f32 v160, v160, 0x3fb8aa3b, v175
	v_mfma_f32_16x16x32_bf16 v[96:99], v[98:101], v[34:37], 0
	v_add_u32_e32 v90, 0x207ec, v158
	v_fmamk_f32 v161, v161, 0x3fb8aa3b, v175
	v_fmamk_f32 v162, v162, 0x3fb8aa3b, v175
	v_mfma_f32_16x16x32_bf16 v[98:101], v[102:105], v[38:41], v[96:99]
	v_fmamk_f32 v163, v163, 0x3fb8aa3b, v175
	v_fmamk_f32 v164, v164, 0x3fb8aa3b, v175
	v_fmamk_f32 v165, v165, 0x3fb8aa3b, v175
	s_nop 0
	ds_read2_b32 v[96:97], v90 offset1:1
	v_mfma_f32_16x16x32_bf16 v[102:105], v[106:109], v[34:37], 0
	v_fmamk_f32 v166, v166, 0x3fb8aa3b, v175
	v_exp_f32_e32 v159, v159
	v_exp_f32_e32 v160, v160
	s_waitcnt lgkmcnt(0)
	v_add_f32_e32 v91, v92, v96
	v_add_u32_e32 v92, 0x207f4, v158
	v_add_f32_e32 v90, v93, v97
	ds_read2_b32 v[96:97], v92 offset1:1
	v_mfma_f32_16x16x32_bf16 v[102:105], v[110:113], v[38:41], v[102:105]
	v_exp_f32_e32 v161, v161
	v_exp_f32_e32 v162, v162
	v_exp_f32_e32 v163, v163
	s_waitcnt lgkmcnt(0)
	v_add_f32_e32 v93, v94, v96
	v_add_u32_e32 v94, 0x2082c, v158
	v_add_f32_e32 v92, v95, v97
	ds_read2_b32 v[96:97], v94 offset1:1
	v_mfma_f32_16x16x32_bf16 v[106:109], v[114:117], v[34:37], 0
	v_exp_f32_e32 v164, v164
	v_exp_f32_e32 v165, v165
	v_exp_f32_e32 v166, v166
	s_waitcnt lgkmcnt(0)
	v_add_f32_e32 v95, v98, v96
	v_add_u32_e32 v96, 0x20834, v158
	v_add_f32_e32 v94, v99, v97
	ds_read2_b32 v[96:97], v96 offset1:1
	v_mfma_f32_16x16x32_bf16 v[106:109], v[118:121], v[38:41], v[106:109]
	v_fmamk_f32 v167, v167, 0x3fb8aa3b, v175
	v_fmamk_f32 v168, v168, 0x3fb8aa3b, v175
	v_fmamk_f32 v169, v169, 0x3fb8aa3b, v175
	s_waitcnt lgkmcnt(0)
	v_add_f32_e32 v99, v100, v96
	v_add_u32_e32 v96, 0x2086c, v158
	v_add_f32_e32 v98, v101, v97
	ds_read2_b32 v[96:97], v96 offset1:1
	v_fmamk_f32 v170, v170, 0x3fb8aa3b, v175
	v_fmamk_f32 v171, v171, 0x3fb8aa3b, v175
	v_fmamk_f32 v172, v172, 0x3fb8aa3b, v175
	v_fmamk_f32 v173, v173, 0x3fb8aa3b, v175
	s_waitcnt lgkmcnt(0)
	v_add_f32_e32 v101, v102, v96
	v_add_u32_e32 v96, 0x20874, v158
	v_add_f32_e32 v100, v103, v97
	ds_read2_b32 v[96:97], v96 offset1:1
	v_fmac_f32_e32 v175, 0x3fb8aa3b, v174
	v_exp_f32_e32 v167, v167
	v_exp_f32_e32 v168, v168
	v_exp_f32_e32 v169, v169
	s_waitcnt lgkmcnt(0)
	v_add_f32_e32 v103, v104, v96
	v_add_u32_e32 v96, 0x208ac, v158
	v_add_f32_e32 v102, v105, v97
	ds_read2_b32 v[104:105], v96 offset1:1
	v_exp_f32_e32 v170, v170
	v_exp_f32_e32 v171, v171
	v_exp_f32_e32 v172, v172
	v_exp_f32_e32 v173, v173
	s_waitcnt lgkmcnt(0)
	v_add_f32_e32 v97, v106, v104
	v_add_u32_e32 v104, 0x208b4, v158
	v_add_f32_e32 v96, v107, v105
	ds_read2_b32 v[106:107], v104 offset1:1
	v_exp_f32_e32 v174, v175
	v_cvt_pk_bf16_f32 v180, v159, v160
	v_cvt_pk_bf16_f32 v181, v161, v162
	v_cvt_pk_bf16_f32 v182, v163, v164
	v_cvt_pk_bf16_f32 v183, v165, v166
	s_waitcnt lgkmcnt(0)
	v_add_f32_e32 v105, v108, v106
	v_max_f32_e32 v106, v91, v90
	v_mfma_f32_16x16x32_bf16 v[30:33], v[86:89], v[180:183], v[30:33]
	v_max3_f32 v106, v106, v93, v92
	v_max3_f32 v106, v106, v95, v94
	v_max3_f32 v106, v106, v99, v98
	v_mfma_f32_16x16x32_bf16 v[26:29], v[82:85], v[180:183], v[26:29]
	v_max3_f32 v106, v106, v101, v100
	v_max3_f32 v106, v106, v103, v102
	v_add_f32_e32 v104, v109, v107
	v_mfma_f32_16x16x32_bf16 v[22:25], v[78:81], v[180:183], v[22:25]
	v_max3_f32 v106, v106, v97, v96
	v_max3_f32 v106, v106, v105, v104
	v_add_f32_e32 v107, 0x40c00000, v131
	v_mfma_f32_16x16x32_bf16 v[18:21], v[74:77], v[180:183], v[18:21]
	v_cvt_pk_bf16_f32 v180, v167, v168
	v_cvt_pk_bf16_f32 v181, v169, v170
	v_cvt_pk_bf16_f32 v182, v171, v172
	v_cvt_pk_bf16_f32 v183, v173, v174
	v_cmp_gt_f32_e32 vcc, v106, v107
	s_nop 0
	v_mfma_f32_16x16x32_bf16 v[30:33], v[70:73], v[180:183], v[30:33]
	v_mfma_f32_16x16x32_bf16 v[26:29], v[66:69], v[180:183], v[26:29]
	v_mfma_f32_16x16x32_bf16 v[22:25], v[62:65], v[180:183], v[22:25]
	v_mfma_f32_16x16x32_bf16 v[18:21], v[58:61], v[180:183], v[18:21]
	s_cbranch_vccz .LBB0_1045
	v_add_f32_e32 v106, 0, v106
	ds_bpermute_b32 v107, v144, v106
	s_waitcnt lgkmcnt(0)
	v_max_f32_e32 v107, v107, v107
	v_max_f32_e32 v106, v106, v107
	ds_bpermute_b32 v107, v145, v106
	s_waitcnt lgkmcnt(0)
	v_max3_f32 v107, v131, v106, v107
	v_sub_f32_e32 v106, v131, v107
	v_mul_f32_e32 v106, 0x3fb8aa3b, v106
	v_exp_f32_e32 v106, v106
	v_mov_b32_e32 v131, v107
	v_mul_f32_e32 v136, v136, v106
	v_mul_f32_e32 v16, v16, v106
	v_mul_f32_e32 v17, v17, v106
	v_mul_f32_e32 v14, v14, v106
	v_mul_f32_e32 v15, v15, v106
	v_mul_f32_e32 v12, v12, v106
	v_mul_f32_e32 v13, v13, v106
	v_mul_f32_e32 v10, v10, v106
	v_mul_f32_e32 v11, v11, v106
	v_mul_f32_e32 v8, v8, v106
	v_mul_f32_e32 v9, v9, v106
	v_mul_f32_e32 v6, v6, v106
	v_mul_f32_e32 v7, v7, v106
	v_mul_f32_e32 v4, v4, v106
	v_mul_f32_e32 v5, v5, v106
	v_mul_f32_e32 v2, v2, v106
	v_mul_f32_e32 v3, v3, v106
	s_branch .LBB0_1045

;     ...
;             for (int rd = 0; rd < nrounds; ++rd) {
;                 int p0s[TS];
; #pragma unroll
;                 for (int i = 0; i < TS; ++i) p0s[i] = p0n[i];
;                 __syncthreads();
; #pragma unroll
;                 for (int i = 0; i < TS; ++i) {
;                     *(LAS u32x4*)(L + AT_K + i * AT_TS + st_k) = kreg[i];
;                     if (do_pv) { const u32x2 lo = {vreg[i].x, vreg[i].y}, hi = {vreg[i].z, vreg[i].w};
;                         *(LAS u32x2*)(L + AT_V + i * AT_TS + st_va) = lo; *(LAS u32x2*)(L + AT_V + i * AT_TS + (st_va ^ 16)) = hi; } }
;                 if (rd + 1 < nrounds) AT_ISSUE(rd + 1);
;                 __syncthreads();
; #pragma unroll
;               for (int ts = 0; ts < TS; ++ts) {
;                 const int p0 = p0s[ts]; const int LK = AT_K + ts * AT_TS, LV = AT_V + ts * AT_TS;
;                 if (p0 < 0) continue;
;                 if (MODE == 0) { if (p0 > tw0 + TW - 1 || p0 + 63 < tw0 - 127) continue; }
;                 if (MODE == 1) { if (p0 > tw0 + TW - 1 || p0 + 63 < tw0 - 511) continue; }
;                 if (MODE == 2) { if (16 * p0 + 31 > tw0 + TW - 1) continue; }
;                 if (MODE == 3) { if (p0 > tw0 + TW - 1) continue; }
;                 const bool far = (MODE == 2) ? (tw0 - (16 * (p0 + 63) + 31) >= 790) : ((MODE == 3) ? (tw0 - (p0 + 63) >= 790) : false);
;                 const int jblk = p0 >> 6;
;                 bf16x8 akf[4][2]; bf16x8 avf[2][4];
;                 if (MODE != 3) {
; #pragma unroll
;                     for (int kt = 0; kt < 4; ++kt)
; #pragma unroll
;                         for (int ks = 0; ks < 2; ++ks) akf[kt][ks] = *(const LAS bf16x8*)(L + LK + (16 * kt + n) * 128 + ((((4 * ks + q) ^ n) & 7) << 4));
;                     if (do_pv) {
; #pragma unroll
;                         for (int st = 0; st < 2; ++st)
; #pragma unroll
;                             for (int dt = 0; dt < 4; ++dt) avf[st][dt] = *(const LAS bf16x8*)(L + LV + (16 * dt + n) * 128 + ((((4 * st + q) ^ n) & 7) << 4)); }
;     ...
;                         for (int kt = 0; kt < 4; ++kt) { sc[kt] = (f32x4){0.f, 0.f, 0.f, 0.f};
; #pragma unroll
;                             for (int ks = 0; ks < 2; ++ks) { const bf16x8 ak = (MODE != 3) ? akf[kt][ks] : akq[kt][ks];
;                                 sc[kt] = __builtin_amdgcn_mfma_f32_16x16x32_bf16(ak, Bq[qd][ks], sc[kt], 0, 0, 0); } }
.Lw2_1047:
	s_mov_b32 s9, s7
	s_add_i32 s7, s7, 64
	s_cmpk_eq_i32 s8, 0x700
	s_cselect_b32 s10, 0, 64
	s_add_i32 s42, s7, s10
	s_max_i32 s42, s42, 0
	s_lshl_b64 s[10:11], s[42:43], 13
	s_lshl_b32 s42, s42, 1
	s_waitcnt lgkmcnt(0)
	s_barrier
	s_waitcnt vmcnt(3)
	ds_write_b128 v153, v[204:207]
	s_waitcnt vmcnt(2)
	ds_write_b64 v154, v[200:201] offset:8192
	ds_write_b64 v155, v[202:203] offset:8192
	v_lshl_add_u64 v[200:201], v[138:139], 0, s[10:11]
	v_lshl_add_u64 v[202:203], v[140:141], 0, s[42:43]
	global_load_dwordx4 v[204:207], v[200:201], off
	s_nop 0
	global_load_dwordx4 v[200:203], v[202:203], off
	s_cmp_lt_i32 s9, 0
	s_cselect_b64 s[10:11], -1, 0
	s_cmp_gt_i32 s9, s13
	s_cselect_b64 s[14:15], -1, 0
	s_add_i32 s9, s9, 63
	s_cmp_lt_i32 s9, s12
	s_cselect_b64 s[16:17], -1, 0
	s_or_b64 s[10:11], s[10:11], s[16:17]
	s_or_b64 s[10:11], s[10:11], s[14:15]
	s_and_b64 vcc, exec, s[10:11]
	s_waitcnt lgkmcnt(0)
	s_barrier
	s_cbranch_vccnz .Lw2_1046
	v_add_u32_e32 v58, v143, v147
	ds_read_b128 v[90:93], v58
	v_add_u32_e32 v59, v143, v148
	ds_read_b128 v[94:97], v59
	ds_read_b128 v[98:101], v58 offset:2048
	ds_read_b128 v[102:105], v59 offset:2048
	ds_read_b128 v[106:109], v58 offset:4096
	ds_read_b128 v[110:113], v59 offset:4096
	ds_read_b128 v[114:117], v58 offset:6144
	ds_read_b128 v[118:121], v59 offset:6144
	ds_read_b128 v[86:89], v58 offset:8192
	ds_read_b128 v[82:85], v58 offset:10240
	ds_read_b128 v[78:81], v58 offset:12288
	ds_read_b128 v[74:77], v58 offset:14336
	ds_read_b128 v[70:73], v59 offset:8192
	ds_read_b128 v[66:69], v59 offset:10240
	ds_read_b128 v[62:65], v59 offset:12288
	ds_read_b128 v[58:61], v59 offset:14336
	s_waitcnt lgkmcnt(13)
	v_mfma_f32_16x16x32_bf16 v[164:167], v[98:101], v[42:45], 0
	s_waitcnt lgkmcnt(12)
	v_mfma_f32_16x16x32_bf16 v[164:167], v[102:105], v[46:49], v[164:167]
	v_mfma_f32_16x16x32_bf16 v[158:161], v[90:93], v[42:45], 0
	v_mfma_f32_16x16x32_bf16 v[160:163], v[94:97], v[46:49], v[158:161]
	s_waitcnt lgkmcnt(11)
	v_mfma_f32_16x16x32_bf16 v[168:171], v[106:109], v[42:45], 0
	s_nop 4
	v_add_u32_e32 v158, s8, v152
	v_add_u32_e32 v159, 0x207fc, v158
	ds_read2_b32 v[176:177], v159 offset1:1
	s_waitcnt lgkmcnt(11)
	v_mfma_f32_16x16x32_bf16 v[168:171], v[110:113], v[46:49], v[168:171]
	s_waitcnt lgkmcnt(0)
	v_add_f32_e32 v159, v160, v176
	v_add_f32_e32 v160, v161, v177
	v_add_u32_e32 v161, 0x20804, v158
	ds_read2_b32 v[176:177], v161 offset1:1
	v_mfma_f32_16x16x32_bf16 v[172:175], v[114:117], v[42:45], 0
	s_waitcnt lgkmcnt(0)
	v_add_f32_e32 v161, v162, v176
	v_add_f32_e32 v162, v163, v177
	v_add_u32_e32 v163, 0x2083c, v158
	ds_read2_b32 v[176:177], v163 offset1:1
	v_mfma_f32_16x16x32_bf16 v[172:175], v[118:121], v[46:49], v[172:175]
	s_waitcnt lgkmcnt(0)
	v_add_f32_e32 v163, v164, v176
	v_add_f32_e32 v164, v165, v177
	v_add_u32_e32 v165, 0x20844, v158
	ds_read2_b32 v[176:177], v165 offset1:1
	s_waitcnt lgkmcnt(0)
	v_add_f32_e32 v165, v166, v176
	v_add_f32_e32 v166, v167, v177
	v_add_u32_e32 v167, 0x2087c, v158
	ds_read2_b32 v[176:177], v167 offset1:1
	s_waitcnt lgkmcnt(0)
	v_add_f32_e32 v167, v168, v176
	v_add_f32_e32 v168, v169, v177
	v_add_u32_e32 v169, 0x20884, v158
	ds_read2_b32 v[176:177], v169 offset1:1
	s_waitcnt lgkmcnt(0)
	v_add_f32_e32 v169, v170, v176
	v_add_f32_e32 v170, v171, v177
	v_add_u32_e32 v171, 0x208bc, v158
	ds_read2_b32 v[176:177], v171 offset1:1
	s_waitcnt lgkmcnt(0)
	v_add_f32_e32 v171, v172, v176
	v_add_f32_e32 v172, v173, v177
	v_add_u32_e32 v173, 0x208c4, v158
	ds_read2_b32 v[176:177], v173 offset1:1
	s_waitcnt lgkmcnt(0)
	v_add_f32_e32 v173, v174, v176
	v_add_f32_e32 v174, v175, v177
	v_max_f32_e32 v175, v159, v160
	v_max3_f32 v175, v175, v161, v162
	v_max3_f32 v175, v175, v163, v164
	v_max3_f32 v175, v175, v165, v166
	v_max3_f32 v175, v175, v167, v168
	v_max3_f32 v175, v175, v169, v170
	v_max3_f32 v175, v175, v171, v172
	v_max3_f32 v175, v175, v173, v174
	v_add_f32_e32 v176, 0x40c00000, v157
	v_cmp_gt_f32_e32 vcc, v175, v176
	s_cbranch_vccz .Lw2_1050
	v_add_f32_e32 v175, 0, v175
	ds_bpermute_b32 v176, v144, v175
	s_waitcnt lgkmcnt(0)
	v_max_f32_e32 v176, v176, v176
	v_max_f32_e32 v175, v175, v176
	ds_bpermute_b32 v176, v145, v175
	s_waitcnt lgkmcnt(0)
	v_max3_f32 v175, v157, v175, v176
	v_sub_f32_e32 v157, v157, v175
	v_mul_f32_e32 v157, 0x3fb8aa3b, v157
	v_exp_f32_e32 v176, v157
	v_mov_b32_e32 v157, v175
	v_mul_f32_e32 v137, v137, v176
	v_mul_f32_e32 v32, v32, v176
	v_mul_f32_e32 v33, v33, v176
	v_mul_f32_e32 v30, v30, v176
	v_mul_f32_e32 v31, v31, v176
	v_mul_f32_e32 v28, v28, v176
	v_mul_f32_e32 v29, v29, v176
	v_mul_f32_e32 v26, v26, v176
	v_mul_f32_e32 v27, v27, v176
	v_mul_f32_e32 v24, v24, v176
	v_mul_f32_e32 v25, v25, v176
	v_mul_f32_e32 v22, v22, v176
	v_mul_f32_e32 v23, v23, v176
	v_mul_f32_e32 v20, v20, v176
	v_mul_f32_e32 v21, v21, v176
	v_mul_f32_e32 v18, v18, v176
	v_mul_f32_e32 v19, v19, v176

; #define LAS __attribute__((address_space(3)))
;     ...
;                 __syncthreads();
; #pragma unroll
;                 for (int i = 0; i < TS; ++i) {
;                     *(LAS u32x4*)(L + AT_K + i * AT_TS + st_k) = kreg[i];
;                     if (do_pv) { const u32x2 lo = {vreg[i].x, vreg[i].y}, hi = {vreg[i].z, vreg[i].w};
;                         *(LAS u32x2*)(L + AT_V + i * AT_TS + st_va) = lo; *(LAS u32x2*)(L + AT_V + i * AT_TS + (st_va ^ 16)) = hi; } }
;                 if (rd + 1 < nrounds) AT_ISSUE(rd + 1);
;                 __syncthreads();
; #pragma unroll
;               for (int ts = 0; ts < TS; ++ts) {
;                 const int p0 = p0s[ts]; const int LK = AT_K + ts * AT_TS, LV = AT_V + ts * AT_TS;
;                 if (p0 < 0) continue;
;                 if (MODE == 0) { if (p0 > tw0 + TW - 1 || p0 + 63 < tw0 - 127) continue; }
;                 if (MODE == 1) { if (p0 > tw0 + TW - 1 || p0 + 63 < tw0 - 511) continue; }
;                 if (MODE == 2) { if (16 * p0 + 31 > tw0 + TW - 1) continue; }
;                 if (MODE == 3) { if (p0 > tw0 + TW - 1) continue; }
;                 const bool far = (MODE == 2) ? (tw0 - (16 * (p0 + 63) + 31) >= 790) : ((MODE == 3) ? (tw0 - (p0 + 63) >= 790) : false);
;                 const int jblk = p0 >> 6;
;                 bf16x8 akf[4][2]; bf16x8 avf[2][4];
;                 if (MODE != 3) {
; #pragma unroll
;                     for (int kt = 0; kt < 4; ++kt)
; #pragma unroll
;                         for (int ks = 0; ks < 2; ++ks) akf[kt][ks] = *(const LAS bf16x8*)(L + LK + (16 * kt + n) * 128 + ((((4 * ks + q) ^ n) & 7) << 4));
;                     if (do_pv) {
; #pragma unroll
;                         for (int st = 0; st < 2; ++st)
; #pragma unroll
;                             for (int dt = 0; dt < 4; ++dt) avf[st][dt] = *(const LAS bf16x8*)(L + LV + (16 * dt + n) * 128 + ((((4 * st + q) ^ n) & 7) << 4)); }
;                 }
;                 unsigned tokmask = 0u;
;                 if (MODE == 3) { tokmask = (unsigned)__ballot(lane < TW && ((selm[(wave * TW + (lane & (TW - 1))) * 8 + (jblk >> 5)] >> (jblk & 31)) & 1u)); if (tokmask == 0u) continue; }
; #pragma unroll
;                 for (int qd = 0; qd < NQ; ++qd) {
;                     const int tq = tw0 + 4 * qd + (n >> 2);
;                     if (DBG == 3) continue;
;                     bool colsel = true;
.LBB0_1052:
	s_cmp_lt_i32 s7, 0
	s_cselect_b64 s[8:9], -1, 0
	s_cmp_gt_i32 s7, s13
	s_cselect_b64 s[10:11], -1, 0
	s_or_b32 s13, s7, 63
	s_cmp_lt_i32 s13, s12
	s_cselect_b64 s[12:13], -1, 0
	s_or_b64 s[8:9], s[8:9], s[12:13]
	s_or_b64 s[8:9], s[8:9], s[10:11]
	s_and_b64 vcc, exec, s[8:9]
	s_barrier
	s_waitcnt vmcnt(3)
	ds_write_b128 v153, v[54:57]
	s_waitcnt vmcnt(2)
	ds_write_b64 v154, v[50:51] offset:8192
	ds_write_b64 v155, v[52:53] offset:8192
	s_waitcnt lgkmcnt(0)
	s_barrier
	s_cbranch_vccnz .LBB0_1034
	v_add_u32_e32 v50, v143, v147
	ds_read_b128 v[82:85], v50
	v_add_u32_e32 v51, v143, v148
	ds_read_b128 v[86:89], v51
	ds_read_b128 v[90:93], v50 offset:2048
	ds_read_b128 v[94:97], v51 offset:2048
	ds_read_b128 v[98:101], v50 offset:4096
	ds_read_b128 v[102:105], v51 offset:4096
	ds_read_b128 v[106:109], v50 offset:6144
	ds_read_b128 v[110:113], v51 offset:6144
	ds_read_b128 v[78:81], v50 offset:8192
	ds_read_b128 v[74:77], v50 offset:10240
	ds_read_b128 v[70:73], v50 offset:12288
	ds_read_b128 v[66:69], v50 offset:14336
	ds_read_b128 v[62:65], v51 offset:8192
	ds_read_b128 v[58:61], v51 offset:10240
	ds_read_b128 v[54:57], v51 offset:12288
	ds_read_b128 v[50:53], v51 offset:14336
	s_waitcnt lgkmcnt(13)
	v_mfma_f32_16x16x32_bf16 v[118:121], v[90:93], v[42:45], 0
	s_waitcnt lgkmcnt(11)
	v_mfma_f32_16x16x32_bf16 v[138:141], v[98:101], v[42:45], 0
	v_mfma_f32_16x16x32_bf16 v[114:117], v[82:85], v[42:45], 0
	s_waitcnt lgkmcnt(9)
	v_mfma_f32_16x16x32_bf16 v[42:45], v[106:109], v[42:45], 0
	s_waitcnt lgkmcnt(8)
	v_mfma_f32_16x16x32_bf16 v[158:161], v[110:113], v[46:49], v[42:45]
	v_mfma_f32_16x16x32_bf16 v[114:117], v[86:89], v[46:49], v[114:117]
	s_nop 4
	v_sub_u32_e32 v42, s7, v134
	v_lshl_add_u32 v162, v42, 2, v149
	v_add_u32_e32 v42, 0xffc, v162
	ds_read2_b32 v[42:43], v42 offset1:1
	v_add_u32_e32 v44, 0x1004, v162
	v_mfma_f32_16x16x32_bf16 v[118:121], v[94:97], v[46:49], v[118:121]
	ds_read2_b32 v[44:45], v44 offset1:1
	v_mfma_f32_16x16x32_bf16 v[138:141], v[102:105], v[46:49], v[138:141]
	v_add_u32_e32 v46, 0x103c, v162
	v_add_u32_e32 v48, 0x1044, v162
	ds_read2_b32 v[46:47], v46 offset1:1
	ds_read2_b32 v[48:49], v48 offset1:1
	s_waitcnt lgkmcnt(3)
	v_add_f32_e32 v42, v114, v42
	v_add_u32_e32 v114, 0x107c, v162
	v_add_f32_e32 v43, v115, v43
	ds_read2_b32 v[114:115], v114 offset1:1
	s_waitcnt lgkmcnt(3)
	v_add_f32_e32 v44, v116, v44
	v_add_u32_e32 v116, 0x1084, v162
	v_add_f32_e32 v45, v117, v45
	s_waitcnt lgkmcnt(2)
	v_add_f32_e32 v46, v118, v46
	s_waitcnt lgkmcnt(1)
	v_add_f32_e32 v48, v120, v48
	ds_read2_b32 v[116:117], v116 offset1:1
	v_add_u32_e32 v118, 0x10bc, v162
	v_add_u32_e32 v120, 0x10c4, v162
	v_add_f32_e32 v47, v119, v47
	v_add_f32_e32 v49, v121, v49
	ds_read2_b32 v[118:119], v118 offset1:1
	ds_read2_b32 v[120:121], v120 offset1:1
	s_waitcnt lgkmcnt(3)
	v_add_f32_e32 v114, v138, v114
	v_max_f32_e32 v138, v42, v43
	v_max3_f32 v138, v138, v44, v45
	v_max3_f32 v138, v138, v46, v47
	v_add_f32_e32 v115, v139, v115
	v_max3_f32 v138, v138, v48, v49
	s_waitcnt lgkmcnt(2)
	v_add_f32_e32 v116, v140, v116
	v_add_f32_e32 v117, v141, v117
	v_max3_f32 v138, v138, v114, v115
	s_waitcnt lgkmcnt(1)
	v_add_f32_e32 v118, v158, v118
	v_add_f32_e32 v119, v159, v119
	v_max3_f32 v138, v138, v116, v117
	s_waitcnt lgkmcnt(0)
	v_add_f32_e32 v120, v160, v120
	v_add_f32_e32 v121, v161, v121
	v_max3_f32 v138, v138, v118, v119
	v_max3_f32 v138, v138, v120, v121
	v_add_f32_e32 v139, 0x40c00000, v157
	v_cmp_gt_f32_e32 vcc, v138, v139
	s_cbranch_vccz .LBB0_1055
	v_add_f32_e32 v138, 0, v138
	ds_bpermute_b32 v139, v144, v138
	s_waitcnt lgkmcnt(0)
	v_max_f32_e32 v139, v139, v139
	v_max_f32_e32 v138, v138, v139
	ds_bpermute_b32 v139, v145, v138
	s_waitcnt lgkmcnt(0)
	v_max3_f32 v139, v157, v138, v139
	v_sub_f32_e32 v138, v157, v139
	v_mul_f32_e32 v138, 0x3fb8aa3b, v138
	v_exp_f32_e32 v138, v138
	v_mov_b32_e32 v157, v139
	v_mul_f32_e32 v137, v137, v138
	v_mul_f32_e32 v32, v32, v138
	v_mul_f32_e32 v33, v33, v138
	v_mul_f32_e32 v30, v30, v138
	v_mul_f32_e32 v31, v31, v138
	v_mul_f32_e32 v28, v28, v138
	v_mul_f32_e32 v29, v29, v138
	v_mul_f32_e32 v26, v26, v138
	v_mul_f32_e32 v27, v27, v138
	v_mul_f32_e32 v24, v24, v138
	v_mul_f32_e32 v25, v25, v138
	v_mul_f32_e32 v22, v22, v138
	v_mul_f32_e32 v23, v23, v138
	v_mul_f32_e32 v20, v20, v138
	v_mul_f32_e32 v21, v21, v138
	v_mul_f32_e32 v18, v18, v138
	v_mul_f32_e32 v19, v19, v138
;     ...
;                         for (int kt = 0; kt < 4; ++kt) { sc[kt] = (f32x4){0.f, 0.f, 0.f, 0.f};
; #pragma unroll
;                             for (int ks = 0; ks < 2; ++ks) { const bf16x8 ak = (MODE != 3) ? akf[kt][ks] : akq[kt][ks];
;                                 sc[kt] = __builtin_amdgcn_mfma_f32_16x16x32_bf16(ak, Bq[qd][ks], sc[kt], 0, 0, 0); } }
;                         if (MODE == 3) {
; #pragma unroll
;                             for (int st = 0; st < 2; ++st)
; #pragma unroll
;                                 for (int dt = 0; dt < 4; ++dt) avq[st][dt] = *(const LAS bf16x8*)(L + LV + (16 * dt + n) * 128 + ((((4 * st + q) ^ n) & 7) << 4));
;                             __builtin_amdgcn_sched_barrier(0);
;                         }
;                         if (!far) {
;                             const LAS float* tp = (MODE == 2) ? biasd + hr * NT + (DOFF - tq + 31 + 16 * p0) + 64 * q : biasd + hr * NT + (DOFF - tq + p0) + 4 * q;
; #pragma unroll
;                             for (int kt = 0; kt < 4; ++kt)
; #pragma unroll
;                                 for (int r = 0; r < 4; ++r) sc[kt][r] += (MODE == 3) ? bia[kt][r] : ((MODE == 2) ? tp[256 * kt + 16 * r] : tp[16 * kt + r]);
;                         }
;                         const float bshift = far ? bfar : 0.f, boff = bshift * 1.4426950408889634f;
;                         float mx;
;                         { float m = fmaxf(fmaxf(sc[0][0], sc[0][1]), sc[0][2]);
;                           m = fmaxf(fmaxf(m, sc[0][3]), sc[1][0]); m = fmaxf(fmaxf(m, sc[1][1]), sc[1][2]); m = fmaxf(fmaxf(m, sc[1][3]), sc[2][0]);
;                           m = fmaxf(fmaxf(m, sc[2][1]), sc[2][2]); m = fmaxf(fmaxf(m, sc[2][3]), sc[3][0]); m = fmaxf(fmaxf(m, sc[3][1]), sc[3][2]); mx = fmaxf(m, sc[3][3]) + bshift; }
;                         if (MODE == 3 && !colsel) mx = -1e30f;
;                         float p[4][4];
;                         constexpr float L2E = 1.4426950408889634f;
;                         if (MODE == 2 && pass == 1) {
;                             const float negm1 = (mrun[qd] < -1e29f ? 0.f : -mrun[qd] * L2E) + boff + linv[qd];
; #pragma unroll
;                             for (int kt = 0; kt < 4; ++kt)
; #pragma unroll
;                                 for (int r = 0; r < 4; ++r) p[kt][r] = __builtin_amdgcn_exp2f(__builtin_fmaf(sc[kt][r], L2E, negm1));
.LBB0_1055:
	v_mfma_f32_16x16x32_bf16 v[82:85], v[82:85], v[34:37], 0
	v_fma_f32 v138, v157, s24, 0
	v_cmp_ngt_f32_e32 vcc, s30, v157
	v_mfma_f32_16x16x32_bf16 v[82:85], v[86:89], v[38:41], v[82:85]
	s_nop 0
	v_cndmask_b32_e32 v138, 0, v138, vcc
	v_fmamk_f32 v42, v42, 0x3fb8aa3b, v138
	v_fmamk_f32 v43, v43, 0x3fb8aa3b, v138
	v_mfma_f32_16x16x32_bf16 v[86:89], v[90:93], v[34:37], 0
	v_fmamk_f32 v44, v44, 0x3fb8aa3b, v138
	v_fmamk_f32 v45, v45, 0x3fb8aa3b, v138
	v_fmamk_f32 v46, v46, 0x3fb8aa3b, v138
	v_mfma_f32_16x16x32_bf16 v[90:93], v[98:101], v[34:37], 0
	v_fmamk_f32 v47, v47, 0x3fb8aa3b, v138
	v_fmamk_f32 v48, v48, 0x3fb8aa3b, v138
	v_fmamk_f32 v49, v49, 0x3fb8aa3b, v138
	v_mfma_f32_16x16x32_bf16 v[34:37], v[106:109], v[34:37], 0
	v_exp_f32_e32 v42, v42
	v_exp_f32_e32 v43, v43
	v_exp_f32_e32 v44, v44
	v_mfma_f32_16x16x32_bf16 v[86:89], v[94:97], v[38:41], v[86:89]
	v_exp_f32_e32 v45, v45
	v_exp_f32_e32 v46, v46
	v_exp_f32_e32 v47, v47
	v_mfma_f32_16x16x32_bf16 v[94:97], v[110:113], v[38:41], v[34:37]
	v_exp_f32_e32 v48, v48
	v_exp_f32_e32 v49, v49
	v_fmamk_f32 v114, v114, 0x3fb8aa3b, v138
	v_sub_u32_e32 v34, s7, v132
	v_lshl_add_u32 v98, v34, 2, v149
	v_add_u32_e32 v34, 0xffc, v98
	ds_read2_b32 v[36:37], v34 offset1:1
	v_mfma_f32_16x16x32_bf16 v[90:93], v[102:105], v[38:41], v[90:93]
	v_fmamk_f32 v115, v115, 0x3fb8aa3b, v138
	v_fmamk_f32 v116, v116, 0x3fb8aa3b, v138
	v_fmamk_f32 v117, v117, 0x3fb8aa3b, v138
	s_waitcnt lgkmcnt(0)
	v_add_f32_e32 v35, v82, v36
	v_add_u32_e32 v36, 0x1004, v98
	ds_read2_b32 v[38:39], v36 offset1:1
	v_add_f32_e32 v34, v83, v37
	v_fmamk_f32 v118, v118, 0x3fb8aa3b, v138
	v_fmamk_f32 v119, v119, 0x3fb8aa3b, v138
	v_fmamk_f32 v120, v120, 0x3fb8aa3b, v138
	s_waitcnt lgkmcnt(0)
	v_add_f32_e32 v37, v84, v38
	v_add_u32_e32 v38, 0x103c, v98
	ds_read2_b32 v[40:41], v38 offset1:1
	v_add_f32_e32 v36, v85, v39
	v_fmac_f32_e32 v138, 0x3fb8aa3b, v121
	v_exp_f32_e32 v114, v114
	v_exp_f32_e32 v115, v115
	s_waitcnt lgkmcnt(0)
	v_add_f32_e32 v39, v86, v40
	v_add_u32_e32 v40, 0x1044, v98
	v_add_f32_e32 v38, v87, v41
	ds_read2_b32 v[40:41], v40 offset1:1
	v_exp_f32_e32 v116, v116
	v_exp_f32_e32 v117, v117
	v_exp_f32_e32 v118, v118
	v_exp_f32_e32 v119, v119
	s_waitcnt lgkmcnt(0)
	v_add_f32_e32 v83, v88, v40
	v_add_u32_e32 v40, 0x107c, v98
	v_add_f32_e32 v82, v89, v41
	ds_read2_b32 v[40:41], v40 offset1:1
	v_exp_f32_e32 v120, v120
	v_exp_f32_e32 v121, v138
	v_cvt_pk_bf16_f32 v138, v42, v43
	v_cvt_pk_bf16_f32 v139, v44, v45
	s_waitcnt lgkmcnt(0)
	v_add_f32_e32 v85, v90, v40
	v_add_u32_e32 v40, 0x1084, v98
	v_add_f32_e32 v84, v91, v41
	ds_read2_b32 v[40:41], v40 offset1:1
	v_cvt_pk_bf16_f32 v140, v46, v47
	v_cvt_pk_bf16_f32 v141, v48, v49
	s_waitcnt lgkmcnt(0)
	v_add_f32_e32 v87, v92, v40
	v_add_u32_e32 v40, 0x10bc, v98
	ds_read2_b32 v[88:89], v40 offset1:1
	v_add_f32_e32 v86, v93, v41
	v_mfma_f32_16x16x32_bf16 v[30:33], v[78:81], v[138:141], v[30:33]
	s_waitcnt lgkmcnt(0)
	v_add_f32_e32 v41, v94, v88
	v_add_u32_e32 v88, 0x10c4, v98
	ds_read2_b32 v[90:91], v88 offset1:1
	v_add_f32_e32 v40, v95, v89
	v_mfma_f32_16x16x32_bf16 v[26:29], v[74:77], v[138:141], v[26:29]
	s_waitcnt lgkmcnt(0)
	v_add_f32_e32 v89, v96, v90
	v_max_f32_e32 v90, v35, v34
	v_mfma_f32_16x16x32_bf16 v[22:25], v[70:73], v[138:141], v[22:25]
	v_max3_f32 v90, v90, v37, v36
	v_max3_f32 v90, v90, v39, v38
	v_max3_f32 v90, v90, v83, v82
	v_mfma_f32_16x16x32_bf16 v[18:21], v[66:69], v[138:141], v[18:21]
	v_cvt_pk_bf16_f32 v138, v114, v115
	v_cvt_pk_bf16_f32 v139, v116, v117
	v_cvt_pk_bf16_f32 v140, v118, v119
	v_cvt_pk_bf16_f32 v141, v120, v121
	v_max3_f32 v90, v90, v85, v84
	v_max3_f32 v90, v90, v87, v86
	v_mfma_f32_16x16x32_bf16 v[30:33], v[62:65], v[138:141], v[30:33]
	v_add_f32_e32 v88, v97, v91
	v_max3_f32 v90, v90, v41, v40
	v_max3_f32 v90, v90, v89, v88
	v_mfma_f32_16x16x32_bf16 v[26:29], v[58:61], v[138:141], v[26:29]
	v_add_f32_e32 v91, 0x40c00000, v131
	v_cmp_gt_f32_e32 vcc, v90, v91
	v_mfma_f32_16x16x32_bf16 v[22:25], v[54:57], v[138:141], v[22:25]
	v_mfma_f32_16x16x32_bf16 v[18:21], v[50:53], v[138:141], v[18:21]
	s_cbranch_vccz .LBB0_1033
	v_add_f32_e32 v90, 0, v90
	ds_bpermute_b32 v91, v144, v90
	s_waitcnt lgkmcnt(0)
	v_max_f32_e32 v91, v91, v91
	v_max_f32_e32 v90, v90, v91
	ds_bpermute_b32 v91, v145, v90
	s_waitcnt lgkmcnt(0)
	v_max3_f32 v91, v131, v90, v91
	v_sub_f32_e32 v90, v131, v91
	v_mul_f32_e32 v90, 0x3fb8aa3b, v90
	v_exp_f32_e32 v90, v90
	v_mov_b32_e32 v131, v91
	v_mul_f32_e32 v136, v136, v90
	v_mul_f32_e32 v16, v16, v90
	v_mul_f32_e32 v17, v17, v90
	v_mul_f32_e32 v14, v14, v90
	v_mul_f32_e32 v15, v15, v90
	v_mul_f32_e32 v12, v12, v90
	v_mul_f32_e32 v13, v13, v90
	v_mul_f32_e32 v10, v10, v90
	v_mul_f32_e32 v11, v11, v90
	v_mul_f32_e32 v8, v8, v90
	v_mul_f32_e32 v9, v9, v90
	v_mul_f32_e32 v6, v6, v90
	v_mul_f32_e32 v7, v7, v90
	v_mul_f32_e32 v4, v4, v90
	v_mul_f32_e32 v5, v5, v90
	v_mul_f32_e32 v2, v2, v90
	v_mul_f32_e32 v3, v3, v90
	s_branch .LBB0_1033

; __device__ __forceinline__ float bf2f(unsigned v) { return __uint_as_float(v << 16); }
; __device__ __forceinline__ unsigned f2bf(float f) { return pk2(f, 0.f) & 0xffffu; }
; __device__ __forceinline__ void phase_rwkv_out(const Ctx& c, const Args& a, int layer, const bf16_t* proj, const bf16_t* rwu, const bf16_t* rws, const float* bonusg, bf16_t* orwkv) {
;     ...
; #pragma unroll
;             for (int r = 0; r < 4; ++r) { const int t = t0 + 16 * ta + 4 * q + r;
;                 float sm = row16_sum(y[0][r] + y[1][r] + y[2][r] + y[3][r]);
;                 const float mean = sm * (1.0f / 64.0f); float d[4], vs = 0.f;
; #pragma unroll
;                 for (int cq = 0; cq < 4; ++cq) { d[cq] = y[cq][r] - mean; vs += d[cq] * d[cq]; }
;                 vs = row16_sum(vs);
;                 const float rstd = rsqrtf(vs * (1.0f / 64.0f) + 64e-5f); const float bon = bonv[r];
; #pragma unroll
;                 for (int cq = 0; cq < 4; ++cq) { const int col = h * 64 + 16 * cq + m; const float vc = bf2f(vcur[r][cq]); const float vp = t > 0 ? bf2f(vprv[r][cq]) : 0.f; const float v = vc + (vp - vc) * muv[cq];
;                     orwkv[(size_t)t * 512 + col] = (bf16_t)f2bf((d[cq] * rstd * lnw[cq] + lnb[cq] + bon * v) * bf2f(graw[r][cq])); } }
;         }
.LBB0_1114:
	s_or_b64 exec, exec, s[0:1]
	v_add_f32_e32 v38, v38, v42
	v_fmamk_f32 v38, v38, 0x3c800000, v186
	v_mul_f32_e32 v42, 0x4b800000, v38
	v_cmp_gt_f32_e64 s[0:1], s33, v38
	s_waitcnt vmcnt(0)
	v_lshlrev_b32_e32 v0, 16, v0
	s_add_i32 s3, s3, 16
	v_cndmask_b32_e64 v38, v38, v42, s[0:1]
	v_rsq_f32_e32 v38, v38
	v_lshlrev_b32_e32 v42, 16, v117
	v_sub_f32_e32 v34, v34, v42
	v_fmac_f32_e32 v42, v82, v34
	v_mul_f32_e32 v46, 0x45800000, v38
	v_cndmask_b32_e64 v38, v38, v46, s[0:1]
	v_mul_f32_e32 v34, v80, v38
	v_fma_f32 v34, v59, v34, v87
	v_fmac_f32_e32 v34, v95, v42
	v_lshlrev_b32_e32 v42, 16, v114
	v_mul_f32_e32 v34, v34, v42
	v_cvt_pk_bf16_f32 v34, v34, s0
	v_lshlrev_b32_e32 v42, 16, v111
	global_store_short v[68:69], v34, off
	v_lshlrev_b32_e32 v34, 16, v110
	v_cndmask_b32_e32 v42, 0, v42, vcc
	v_sub_f32_e32 v42, v42, v34
	v_fmac_f32_e32 v34, v83, v42
	v_mul_f32_e32 v42, v81, v38
	v_fma_f32 v42, v88, v42, v89
	v_fmac_f32_e32 v42, v95, v34
	v_lshlrev_b32_e32 v34, 16, v108
	v_mul_f32_e32 v34, v42, v34
	v_cvt_pk_bf16_f32 v34, v34, s0
	v_lshlrev_b32_e32 v42, 16, v105
	global_store_short v[68:69], v34, off offset:32
	v_lshlrev_b32_e32 v34, 16, v104
	v_cndmask_b32_e32 v42, 0, v42, vcc
	v_sub_f32_e32 v42, v42, v34
	v_fmac_f32_e32 v34, v84, v42
	v_mul_f32_e32 v42, v79, v38
	v_fma_f32 v42, v90, v42, v91
	v_fmac_f32_e32 v42, v95, v34
	v_lshlrev_b32_e32 v34, 16, v102
	v_mul_f32_e32 v34, v42, v34
	v_cvt_pk_bf16_f32 v34, v34, s0
	v_lshlrev_b32_e32 v42, 16, v99
	global_store_short v[68:69], v34, off offset:64
	v_lshlrev_b32_e32 v34, 16, v98
	v_cndmask_b32_e32 v42, 0, v42, vcc
	v_sub_f32_e32 v42, v42, v34
	v_mul_f32_e32 v38, v78, v38
	v_fmac_f32_e32 v34, v85, v42
	s_waitcnt lgkmcnt(0)
	v_fma_f32 v46, v92, v38, v93
	v_fmac_f32_e32 v46, v95, v34
	v_add_f32_e32 v34, v35, v39
	v_add_f32_e32 v34, v34, v43
	v_add_f32_e32 v34, v34, v47
	v_mov_b32_e32 v38, v35
	v_mov_b32_e32 v42, v47
	v_add_f32_dpp v34, v34, v34 quad_perm:[1,0,3,2] row_mask:0xf bank_mask:0xf bound_ctrl:1
	v_lshlrev_b32_e32 v78, 16, v96
	s_cmp_eq_u32 s3, 64
	v_add_f32_dpp v34, v34, v34 quad_perm:[2,3,0,1] row_mask:0xf bank_mask:0xf bound_ctrl:1
	s_nop 1
	v_add_f32_dpp v34, v34, v34 row_half_mirror row_mask:0xf bank_mask:0xf bound_ctrl:1
	s_nop 1
	v_add_f32_dpp v34, v34, v34 row_mirror row_mask:0xf bank_mask:0xf bound_ctrl:1
	v_mul_f32_e32 v34, 0x3c800000, v34
	v_pk_add_f32 v[38:39], v[38:39], v[34:35] op_sel_hi:[1,0] neg_lo:[0,1] neg_hi:[0,1]
	v_pk_add_f32 v[34:35], v[42:43], v[34:35] op_sel_hi:[1,0] neg_lo:[0,1] neg_hi:[0,1]
	v_mul_f32_e32 v72, v38, v38
	v_mul_f32_e32 v73, v39, v39
	v_mul_f32_e32 v42, v34, v34
	v_mul_f32_e32 v43, v35, v35
	v_add_f32_e32 v47, v72, v73
	v_add_f32_e32 v43, v43, v47
	v_add_f32_e32 v42, v42, v43
	v_lshlrev_b32_e32 v72, 16, v138
	v_mov_b32_e32 v47, v44
	v_add_f32_dpp v42, v42, v42 quad_perm:[1,0,3,2] row_mask:0xf bank_mask:0xf bound_ctrl:1
	v_lshlrev_b32_e32 v73, 16, v134
	s_nop 0
	v_add_f32_dpp v42, v42, v42 quad_perm:[2,3,0,1] row_mask:0xf bank_mask:0xf bound_ctrl:1
	s_nop 1
	v_add_f32_dpp v42, v42, v42 row_half_mirror row_mask:0xf bank_mask:0xf bound_ctrl:1
	s_nop 1
	v_add_f32_dpp v42, v42, v42 row_mirror row_mask:0xf bank_mask:0xf bound_ctrl:1
	v_fmamk_f32 v42, v42, 0x3c800000, v186
	v_mul_f32_e32 v43, 0x4b800000, v42
	v_cmp_gt_f32_e32 vcc, s33, v42
	s_nop 1
	v_cndmask_b32_e32 v42, v42, v43, vcc
	v_rsq_f32_e32 v42, v42
	v_mul_f32_e32 v43, v46, v78
	v_cvt_pk_bf16_f32 v43, v43, s0
	global_store_short v[68:69], v43, off offset:96
	v_mul_f32_e32 v43, 0x45800000, v42
	v_cndmask_b32_e32 v42, v42, v43, vcc
	v_lshlrev_b32_e32 v46, 16, v119
	v_cmp_lt_i32_e32 vcc, -1, v66
	v_lshlrev_b32_e32 v43, 16, v118
	v_mul_f32_e32 v38, v38, v42
	v_cndmask_b32_e32 v46, 0, v46, vcc
	v_sub_f32_e32 v46, v46, v43
	v_fmac_f32_e32 v43, v82, v46
	v_fma_f32 v38, v59, v38, v87
	v_fmac_f32_e32 v38, v67, v43
	v_lshlrev_b32_e32 v43, 16, v115
	v_mul_f32_e32 v38, v38, v43
	v_cvt_pk_bf16_f32 v38, v38, s0
	v_lshlrev_b32_e32 v43, 16, v113
	global_store_short v[70:71], v38, off
	v_lshlrev_b32_e32 v38, 16, v112
	v_cndmask_b32_e32 v43, 0, v43, vcc
	v_sub_f32_e32 v43, v43, v38
	v_mul_f32_e32 v39, v39, v42
	v_fmac_f32_e32 v38, v83, v43
	v_fma_f32 v39, v88, v39, v89
	v_fmac_f32_e32 v39, v67, v38
	v_lshlrev_b32_e32 v38, 16, v109
	v_mul_f32_e32 v38, v39, v38
	v_cvt_pk_bf16_f32 v38, v38, s0
	v_lshlrev_b32_e32 v39, 16, v107
	global_store_short v[70:71], v38, off offset:32
	v_lshlrev_b32_e32 v38, 16, v106
	v_cndmask_b32_e32 v39, 0, v39, vcc
	v_sub_f32_e32 v39, v39, v38
	v_mul_f32_e32 v35, v35, v42
	v_fmac_f32_e32 v38, v84, v39
	v_fma_f32 v35, v90, v35, v91
	v_fmac_f32_e32 v35, v67, v38
	v_lshlrev_b32_e32 v38, 16, v103
	v_mul_f32_e32 v35, v35, v38
	v_cvt_pk_bf16_f32 v35, v35, s0
	v_lshlrev_b32_e32 v38, 16, v101
	global_store_short v[70:71], v35, off offset:64
	v_lshlrev_b32_e32 v35, 16, v100
	v_cndmask_b32_e32 v38, 0, v38, vcc
	v_sub_f32_e32 v38, v38, v35
	v_mul_f32_e32 v34, v34, v42
	v_fmac_f32_e32 v35, v85, v38
	v_fma_f32 v34, v92, v34, v93
	v_fmac_f32_e32 v34, v67, v35
	v_lshlrev_b32_e32 v35, 16, v97
	v_mul_f32_e32 v34, v34, v35
	v_cvt_pk_bf16_f32 v34, v34, s0
	global_store_short v[70:71], v34, off offset:96
	v_add_f32_e32 v34, v36, v40
	v_mov_b32_e32 v38, v36
	v_lshlrev_b32_e32 v36, 16, v140
	v_lshlrev_b32_e32 v68, 16, v133
	v_cndmask_b32_e32 v36, 0, v36, vcc
	v_sub_f32_e32 v36, v36, v68
	v_fmac_f32_e32 v68, v82, v36
	v_lshlrev_b32_e32 v36, 16, v143
	v_lshlrev_b32_e32 v70, 16, v142
	v_cndmask_b32_e32 v36, 0, v36, vcc
	v_sub_f32_e32 v36, v36, v70
	v_fmac_f32_e32 v70, v83, v36
	v_lshlrev_b32_e32 v36, 16, v139
	v_cndmask_b32_e32 v36, 0, v36, vcc
	v_sub_f32_e32 v36, v36, v72
	v_fmac_f32_e32 v72, v84, v36
; __device__ __forceinline__ float bf2f(unsigned v) { return __uint_as_float(v << 16); }
; __device__ __forceinline__ unsigned f2bf(float f) { return pk2(f, 0.f) & 0xffffu; }
; __device__ __forceinline__ void phase_rwkv_out(const Ctx& c, const Args& a, int layer, const bf16_t* proj, const bf16_t* rwu, const bf16_t* rws, const float* bonusg, bf16_t* orwkv) {
;     ...
; #pragma unroll
;             for (int r = 0; r < 4; ++r) { const int t = t0 + 16 * ta + 4 * q + r;
;                 float sm = row16_sum(y[0][r] + y[1][r] + y[2][r] + y[3][r]);
;                 const float mean = sm * (1.0f / 64.0f); float d[4], vs = 0.f;
; #pragma unroll
;                 for (int cq = 0; cq < 4; ++cq) { d[cq] = y[cq][r] - mean; vs += d[cq] * d[cq]; }
;                 vs = row16_sum(vs);
;                 const float rstd = rsqrtf(vs * (1.0f / 64.0f) + 64e-5f); const float bon = bonv[r];
; #pragma unroll
;                 for (int cq = 0; cq < 4; ++cq) { const int col = h * 64 + 16 * cq + m; const float vc = bf2f(vcur[r][cq]); const float vp = t > 0 ? bf2f(vprv[r][cq]) : 0.f; const float v = vc + (vp - vc) * muv[cq];
;                     orwkv[(size_t)t * 512 + col] = (bf16_t)f2bf((d[cq] * rstd * lnw[cq] + lnb[cq] + bon * v) * bf2f(graw[r][cq])); } }
;         }
	v_lshlrev_b32_e32 v36, 16, v136
	v_cndmask_b32_e32 v79, 0, v36, vcc
	v_add_f32_e32 v36, v37, v41
	v_add_f32_e32 v34, v34, v44
	v_add_f32_e32 v36, v36, v45
	v_add_f32_e32 v34, v34, v48
	v_add_f32_e32 v36, v36, v49
	v_mov_b32_e32 v39, v40
	v_add_f32_dpp v34, v34, v34 quad_perm:[1,0,3,2] row_mask:0xf bank_mask:0xf bound_ctrl:1
	v_add_f32_dpp v36, v36, v36 quad_perm:[1,0,3,2] row_mask:0xf bank_mask:0xf bound_ctrl:1
	v_mov_b32_e32 v40, v37
	v_add_f32_dpp v34, v34, v34 quad_perm:[2,3,0,1] row_mask:0xf bank_mask:0xf bound_ctrl:1
	v_add_f32_dpp v36, v36, v36 quad_perm:[2,3,0,1] row_mask:0xf bank_mask:0xf bound_ctrl:1
	v_mov_b32_e32 v46, v48
	v_add_f32_dpp v34, v34, v34 row_half_mirror row_mask:0xf bank_mask:0xf bound_ctrl:1
	v_add_f32_dpp v36, v36, v36 row_half_mirror row_mask:0xf bank_mask:0xf bound_ctrl:1
	v_mov_b32_e32 v44, v49
	v_add_f32_dpp v34, v34, v34 row_mirror row_mask:0xf bank_mask:0xf bound_ctrl:1
	v_add_f32_dpp v36, v36, v36 row_mirror row_mask:0xf bank_mask:0xf bound_ctrl:1
	v_mul_f32_e32 v34, 0x3c800000, v34
	v_mul_f32_e32 v36, 0x3c800000, v36
	v_pk_add_f32 v[38:39], v[38:39], v[34:35] op_sel_hi:[1,0] neg_lo:[0,1] neg_hi:[0,1]
	v_pk_add_f32 v[40:41], v[40:41], v[36:37] op_sel_hi:[1,0] neg_lo:[0,1] neg_hi:[0,1]
	v_mul_f32_e32 v42, v38, v38
	v_mul_f32_e32 v43, v39, v39
	v_pk_add_f32 v[34:35], v[46:47], v[34:35] op_sel_hi:[1,0] neg_lo:[0,1] neg_hi:[0,1]
	v_mul_f32_e32 v66, v40, v40
	v_mul_f32_e32 v67, v41, v41
	v_pk_add_f32 v[36:37], v[44:45], v[36:37] op_sel_hi:[1,0] neg_lo:[0,1] neg_hi:[0,1]
	v_mul_f32_e32 v46, v34, v34
	v_mul_f32_e32 v47, v35, v35
	v_mul_f32_e32 v44, v36, v36
	v_mul_f32_e32 v45, v37, v37
	v_mov_b32_e32 v48, v66
	v_mov_b32_e32 v49, v42
	v_mov_b32_e32 v42, v67
	v_add_f32_e32 v42, v48, v42
	v_add_f32_e32 v43, v49, v43
	v_mov_b32_e32 v48, v45
	v_mov_b32_e32 v49, v47
	v_add_f32_e32 v42, v48, v42
	v_add_f32_e32 v43, v49, v43
	v_mov_b32_e32 v45, v46
	v_add_f32_e32 v42, v44, v42
	v_add_f32_e32 v43, v45, v43
	v_mov_b32_e32 v45, v1
	v_mov_b32_e32 v44, v1
	s_mov_b32 s0, 0x3c800000
	v_mov_b32_dpp v45, v43 quad_perm:[1,0,3,2] row_mask:0xf bank_mask:0xf
	v_mov_b32_dpp v44, v42 quad_perm:[1,0,3,2] row_mask:0xf bank_mask:0xf
	v_add_f32_e32 v42, v42, v44
	v_add_f32_e32 v43, v43, v45
	v_mov_b32_e32 v45, v1
	v_mov_b32_e32 v44, v1
	v_lshlrev_b32_e32 v69, 16, v141
	v_mov_b32_dpp v45, v43 quad_perm:[2,3,0,1] row_mask:0xf bank_mask:0xf
	v_mov_b32_dpp v44, v42 quad_perm:[2,3,0,1] row_mask:0xf bank_mask:0xf
	v_add_f32_e32 v42, v42, v44
	v_add_f32_e32 v43, v43, v45
	v_mov_b32_e32 v45, v1
	v_mov_b32_e32 v44, v1
	v_lshlrev_b32_e32 v71, 16, v137
	v_mov_b32_dpp v45, v43 row_half_mirror row_mask:0xf bank_mask:0xf
	v_mov_b32_dpp v44, v42 row_half_mirror row_mask:0xf bank_mask:0xf
	v_add_f32_e32 v42, v42, v44
	v_add_f32_e32 v43, v43, v45
	v_mov_b32_e32 v45, v1
	v_mov_b32_e32 v44, v1
	v_lshlrev_b32_e32 v78, 16, v135
	v_mov_b32_dpp v45, v43 row_mirror row_mask:0xf bank_mask:0xf
	v_mov_b32_dpp v44, v42 row_mirror row_mask:0xf bank_mask:0xf
	v_add_f32_e32 v42, v42, v44
	v_add_f32_e32 v43, v43, v45
	s_nop 0
	v_fma_f32 v42, v42, s0, v186
	v_fma_f32 v43, v43, s0, v186
	s_nop 0
	v_mul_f32_e32 v44, 0x4b800000, v43
	v_cmp_gt_f32_e64 s[0:1], s33, v43
	s_nop 1
	v_cndmask_b32_e64 v43, v43, v44, s[0:1]
	v_rsq_f32_e32 v43, v43
	v_sub_f32_e32 v44, v79, v78
	v_fmac_f32_e32 v78, v85, v44
	v_lshlrev_b32_e32 v44, 16, v121
	v_mul_f32_e32 v45, 0x45800000, v43
	v_cndmask_b32_e64 v43, v43, v45, s[0:1]
	v_mul_f32_e32 v38, v38, v43
	v_fma_f32 v38, v59, v38, v87
	v_fmac_f32_e32 v38, v116, v68
	v_mul_f32_e32 v38, v38, v69
	v_cvt_pk_bf16_f32 v38, v38, s0
	v_mul_f32_e32 v35, v35, v43
	global_store_short v[74:75], v38, off
	v_mul_f32_e32 v38, v39, v43
	v_fma_f32 v35, v90, v35, v91
	v_fma_f32 v38, v88, v38, v89
	v_fmac_f32_e32 v35, v116, v72
	v_fmac_f32_e32 v38, v116, v70
	v_mul_f32_e32 v35, v35, v73
	v_mul_f32_e32 v38, v38, v71
	v_cvt_pk_bf16_f32 v35, v35, s0
	v_cvt_pk_bf16_f32 v38, v38, s0
	global_store_short v[74:75], v35, off offset:64
	v_mul_f32_e32 v35, 0x4b800000, v42
	v_cmp_gt_f32_e64 s[0:1], s33, v42
	v_mul_f32_e32 v34, v34, v43
	v_fma_f32 v34, v92, v34, v93
	v_cndmask_b32_e64 v35, v42, v35, s[0:1]
	v_rsq_f32_e32 v35, v35
	v_fmac_f32_e32 v34, v116, v78
	v_mul_f32_e32 v34, v34, v44
	v_cvt_pk_bf16_f32 v34, v34, s0
	global_store_short v[74:75], v34, off offset:96
	v_mul_f32_e32 v34, 0x45800000, v35
	v_cndmask_b32_e64 v34, v35, v34, s[0:1]
	v_lshlrev_b32_e32 v35, 16, v122
	v_cndmask_b32_e32 v35, 0, v35, vcc
	v_sub_f32_e32 v35, v35, v0
	v_fmac_f32_e32 v0, v82, v35
	v_mul_f32_e32 v35, v40, v34
	v_fma_f32 v35, v59, v35, v87
	v_fmac_f32_e32 v35, v120, v0
	v_lshlrev_b32_e32 v0, 16, v130
	v_mul_f32_e32 v0, v35, v0
	v_cvt_pk_bf16_f32 v0, v0, s0
	v_lshlrev_b32_e32 v35, 16, v132
	global_store_short v[76:77], v0, off
	v_lshlrev_b32_e32 v0, 16, v131
	v_cndmask_b32_e32 v35, 0, v35, vcc
	v_sub_f32_e32 v35, v35, v0
	v_fmac_f32_e32 v0, v83, v35
	v_mul_f32_e32 v35, v41, v34
	v_fma_f32 v35, v88, v35, v89
	v_fmac_f32_e32 v35, v120, v0
	v_lshlrev_b32_e32 v0, 16, v127
	v_mul_f32_e32 v0, v35, v0
	v_cvt_pk_bf16_f32 v0, v0, s0
	v_lshlrev_b32_e32 v35, 16, v129
	global_store_short v[76:77], v0, off offset:32
	v_lshlrev_b32_e32 v0, 16, v128
	v_cndmask_b32_e32 v35, 0, v35, vcc
	v_sub_f32_e32 v35, v35, v0
	v_fmac_f32_e32 v0, v84, v35
	v_mul_f32_e32 v35, v37, v34
	v_fma_f32 v35, v90, v35, v91
	v_fmac_f32_e32 v35, v120, v0
	v_lshlrev_b32_e32 v0, 16, v124
	v_mul_f32_e32 v0, v35, v0
	v_cvt_pk_bf16_f32 v0, v0, s0
	v_lshlrev_b32_e32 v35, 16, v125
	global_store_short v[76:77], v0, off offset:64
	v_lshlrev_b32_e32 v0, 16, v123
	v_cndmask_b32_e32 v35, 0, v35, vcc
	v_sub_f32_e32 v35, v35, v0
	v_mul_f32_e32 v34, v36, v34
	v_fmac_f32_e32 v0, v85, v35
	v_fma_f32 v34, v92, v34, v93
	v_fmac_f32_e32 v34, v120, v0
	v_lshlrev_b32_e32 v0, 16, v126
	v_mul_f32_e32 v0, v34, v0
	v_cvt_pk_bf16_f32 v0, v0, s0
	s_mov_b64 s[0:1], 0x800
	v_lshl_add_u64 v[64:65], v[64:65], 0, s[0:1]
	s_mov_b64 s[0:1], 0x200
	v_lshl_add_u64 v[62:63], v[62:63], 0, s[0:1]
	global_store_short v[74:75], v38, off offset:32
	global_store_short v[76:77], v0, off offset:96
	s_cbranch_scc1 .LBB0_1112
; __device__ __forceinline__ void phase_rwkv_out(const Ctx& c, const Args& a, int layer, const bf16_t* proj, const bf16_t* rwu, const bf16_t* rws, const float* bonusg, bf16_t* orwkv) {
;     ...
;         for (int ta = 0; ta < 4; ++ta) {
;             const bf16x8 A0 = *(const bf16x8*)(ug + 8192 + ((ta * 2) * 64 + lane) * 8), A1 = *(const bf16x8*)(ug + 8192 + ((ta * 2 + 1) * 64 + lane) * 8);
;             f32x4 y[4];
; #pragma unroll
;             for (int cq = 0; cq < 4; ++cq) { const u32x2 z = *(const u32x2*)(ug + 12288 + ((cq * 4 + ta) * 64 + lane) * 4);
;                 y[cq] = (f32x4){__uint_as_float(z.x << 16), __uint_as_float(z.x & 0xffff0000u), __uint_as_float(z.y << 16), __uint_as_float(z.y & 0xffff0000u)};
;                 y[cq] = __builtin_amdgcn_mfma_f32_16x16x32_bf16(A0, Bf[cq][0], y[cq], 0, 0, 0); y[cq] = __builtin_amdgcn_mfma_f32_16x16x32_bf16(A1, Bf[cq][1], y[cq], 0, 0, 0); }
.LBB0_1115:
	v_lshl_add_u64 v[34:35], v[64:65], 0, s[6:7]
	v_add_co_u32_e32 v34, vcc, 0x15f04000, v34
	v_lshl_add_u64 v[42:43], v[62:63], 0, s[6:7]
	s_nop 0
	v_addc_co_u32_e32 v35, vcc, 0, v35, vcc
	v_add_co_u32_e32 v38, vcc, 0x15f06000, v42
	s_mov_b32 s0, 0x15f07000
	s_nop 0
	v_addc_co_u32_e32 v39, vcc, 0, v43, vcc
	v_add_co_u32_e32 v70, vcc, s0, v42
	global_load_dwordx4 v[46:49], v[34:35], off
	global_load_dwordx4 v[66:69], v[34:35], off offset:1024
	v_addc_co_u32_e32 v71, vcc, 0, v43, vcc
	global_load_dwordx2 v[36:37], v[38:39], off
	global_load_dwordx2 v[40:41], v[38:39], off offset:2048
	global_load_dwordx2 v[44:45], v[70:71], off
	global_load_dwordx2 v[72:73], v[70:71], off offset:2048
	s_waitcnt vmcnt(0)
; __device__ __forceinline__ void phase_rwkv_out(const Ctx& c, const Args& a, int layer, const bf16_t* proj, const bf16_t* rwu, const bf16_t* rws, const float* bonusg, bf16_t* orwkv) {
;     ...
;             for (int cq = 0; cq < 4; ++cq) { const u32x2 z = *(const u32x2*)(ug + 12288 + ((cq * 4 + ta) * 64 + lane) * 4);
;                 y[cq] = (f32x4){__uint_as_float(z.x << 16), __uint_as_float(z.x & 0xffff0000u), __uint_as_float(z.y << 16), __uint_as_float(z.y & 0xffff0000u)};
;                 y[cq] = __builtin_amdgcn_mfma_f32_16x16x32_bf16(A0, Bf[cq][0], y[cq], 0, 0, 0); y[cq] = __builtin_amdgcn_mfma_f32_16x16x32_bf16(A1, Bf[cq][1], y[cq], 0, 0, 0); }
;             bf16_t vcur[4][4], vprv[4][4], graw[4][4]; float bonv[4];
; #pragma unroll
;             for (int r = 0; r < 4; ++r) { const int t = t0 + 16 * ta + 4 * q + r; bonv[r] = bonusg[(size_t)t * 8 + h];
; #pragma unroll
;                 for (int cq = 0; cq < 4; ++cq) { const int col = h * 64 + 16 * cq + m; vcur[r][cq] = proj[(size_t)t * PLD + PC_V + col];
;                     vprv[r][cq] = proj[(size_t)(t > 0 ? t - 1 : 0) * PLD + PC_V + col]; graw[r][cq] = orwkv[(size_t)t * 512 + col]; } }
; #pragma unroll
;             for (int r = 0; r < 4; ++r) { const int t = t0 + 16 * ta + 4 * q + r;
;                 float sm = row16_sum(y[0][r] + y[1][r] + y[2][r] + y[3][r]);
;                 const float mean = sm * (1.0f / 64.0f); float d[4], vs = 0.f;
; #pragma unroll
;                 for (int cq = 0; cq < 4; ++cq) { d[cq] = y[cq][r] - mean; vs += d[cq] * d[cq]; }
;                 vs = row16_sum(vs);
;                 const float rstd = rsqrtf(vs * (1.0f / 64.0f) + 64e-5f); const float bon = bonv[r];
	v_lshlrev_b32_e32 v34, 16, v36
	v_and_b32_e32 v35, 0xffff0000, v36
	v_lshlrev_b32_e32 v36, 16, v37
	v_and_b32_e32 v37, 0xffff0000, v37
	v_lshlrev_b32_e32 v38, 16, v40
	v_and_b32_e32 v39, 0xffff0000, v40
	v_lshlrev_b32_e32 v40, 16, v41
	v_and_b32_e32 v41, 0xffff0000, v41
	v_lshlrev_b32_e32 v42, 16, v44
	v_and_b32_e32 v43, 0xffff0000, v44
	v_lshlrev_b32_e32 v44, 16, v45
	v_and_b32_e32 v45, 0xffff0000, v45
	v_lshlrev_b32_e32 v70, 16, v72
	v_and_b32_e32 v71, 0xffff0000, v72
	v_lshlrev_b32_e32 v72, 16, v73
	v_and_b32_e32 v73, 0xffff0000, v73
	v_mfma_f32_16x16x32_bf16 v[34:37], v[46:49], v[2:5], v[34:37]
	v_mfma_f32_16x16x32_bf16 v[38:41], v[46:49], v[10:13], v[38:41]
	v_mfma_f32_16x16x32_bf16 v[42:45], v[46:49], v[18:21], v[42:45]
	v_mfma_f32_16x16x32_bf16 v[46:49], v[46:49], v[26:29], v[70:73]
	v_mfma_f32_16x16x32_bf16 v[34:37], v[66:69], v[6:9], v[34:37]
	v_mfma_f32_16x16x32_bf16 v[38:41], v[66:69], v[14:17], v[38:41]
	v_mfma_f32_16x16x32_bf16 v[42:45], v[66:69], v[22:25], v[42:45]
	v_mfma_f32_16x16x32_bf16 v[46:49], v[66:69], v[30:33], v[46:49]
	v_add_u32_e32 v66, s3, v94
	v_ashrrev_i32_e32 v67, 31, v66
	v_lshlrev_b64 v[68:69], 5, v[66:67]
	v_max_i32_e32 v0, 1, v66
	v_lshl_add_u64 v[68:69], s[4:5], 0, v[68:69]
	v_add_u32_e32 v0, -1, v0
	global_load_dword v95, v[68:69], off
	v_lshlrev_b64 v[68:69], 13, v[66:67]
	v_lshlrev_b64 v[70:71], 13, v[0:1]
	v_lshlrev_b64 v[72:73], 10, v[66:67]
	v_lshl_add_u64 v[74:75], v[50:51], 0, v[68:69]
	v_lshl_add_u64 v[68:69], v[52:53], 0, v[72:73]
	v_lshl_add_u64 v[72:73], v[50:51], 0, v[70:71]
	v_add_u32_e32 v70, 1, v66
	v_max_i32_e32 v0, 1, v70
	v_ashrrev_i32_e32 v71, 31, v70
	v_add_u32_e32 v0, -1, v0
	global_load_ushort v117, v[74:75], off offset:2048
	global_load_ushort v114, v[68:69], off
	global_load_ushort v110, v[74:75], off offset:2080
	global_load_ushort v111, v[72:73], off offset:2080
	global_load_ushort v108, v[68:69], off offset:32
	global_load_ushort v104, v[74:75], off offset:2112
	global_load_ushort v105, v[72:73], off offset:2112
	global_load_ushort v102, v[68:69], off offset:64
	global_load_ushort v98, v[74:75], off offset:2144
	global_load_ushort v99, v[72:73], off offset:2144
	global_load_ushort v96, v[68:69], off offset:96
	v_lshlrev_b64 v[74:75], 5, v[70:71]
	v_lshlrev_b64 v[76:77], 13, v[0:1]
	v_lshl_add_u64 v[74:75], s[4:5], 0, v[74:75]
	v_lshl_add_u64 v[76:77], v[50:51], 0, v[76:77]
	global_load_dword v67, v[74:75], off
	global_load_ushort v119, v[76:77], off offset:2048
	v_lshlrev_b64 v[74:75], 13, v[70:71]
	v_lshlrev_b64 v[70:71], 10, v[70:71]
	v_lshl_add_u64 v[74:75], v[50:51], 0, v[74:75]
	v_lshl_add_u64 v[70:71], v[52:53], 0, v[70:71]
	global_load_ushort v118, v[74:75], off offset:2048
	global_load_ushort v115, v[70:71], off
	global_load_ushort v112, v[74:75], off offset:2080
	global_load_ushort v113, v[76:77], off offset:2080
	global_load_ushort v109, v[70:71], off offset:32
	global_load_ushort v106, v[74:75], off offset:2112
	global_load_ushort v107, v[76:77], off offset:2112
	global_load_ushort v103, v[70:71], off offset:64
	global_load_ushort v100, v[74:75], off offset:2144
	global_load_ushort v101, v[76:77], off offset:2144
	global_load_ushort v97, v[70:71], off offset:96
	v_add_u32_e32 v74, 2, v66
	v_max_i32_e32 v0, 1, v74
	v_ashrrev_i32_e32 v75, 31, v74
	v_add_u32_e32 v0, -1, v0
	v_lshlrev_b64 v[76:77], 5, v[74:75]
	v_lshlrev_b64 v[78:79], 13, v[0:1]
	v_lshl_add_u64 v[76:77], s[4:5], 0, v[76:77]
	v_lshl_add_u64 v[78:79], v[50:51], 0, v[78:79]
	global_load_dword v116, v[76:77], off
	global_load_ushort v140, v[78:79], off offset:2048
	v_lshlrev_b64 v[76:77], 13, v[74:75]
	v_lshlrev_b64 v[74:75], 10, v[74:75]
	v_lshl_add_u64 v[76:77], v[50:51], 0, v[76:77]
	v_lshl_add_u64 v[74:75], v[52:53], 0, v[74:75]
	global_load_ushort v133, v[76:77], off offset:2048
	global_load_ushort v141, v[74:75], off
	global_load_ushort v142, v[76:77], off offset:2080
	global_load_ushort v143, v[78:79], off offset:2080
	global_load_ushort v137, v[74:75], off offset:32
	global_load_ushort v138, v[76:77], off offset:2112
	global_load_ushort v139, v[78:79], off offset:2112
	global_load_ushort v134, v[74:75], off offset:64
	global_load_ushort v135, v[76:77], off offset:2144
	global_load_ushort v136, v[78:79], off offset:2144
	global_load_ushort v121, v[74:75], off offset:96
	v_add_u32_e32 v76, 3, v66
	v_max_i32_e32 v0, 1, v76
	v_ashrrev_i32_e32 v77, 31, v76
	v_add_u32_e32 v0, -1, v0
	v_lshlrev_b64 v[78:79], 5, v[76:77]
	v_lshlrev_b64 v[80:81], 13, v[0:1]
	v_lshl_add_u64 v[78:79], s[4:5], 0, v[78:79]
	v_lshl_add_u64 v[80:81], v[50:51], 0, v[80:81]
	global_load_dword v120, v[78:79], off
	global_load_ushort v122, v[80:81], off offset:2048
	v_lshlrev_b64 v[78:79], 13, v[76:77]
	v_lshlrev_b64 v[76:77], 10, v[76:77]
	v_lshl_add_u64 v[78:79], v[50:51], 0, v[78:79]
	v_lshl_add_u64 v[76:77], v[52:53], 0, v[76:77]
	global_load_ushort v0, v[78:79], off offset:2048
	global_load_ushort v130, v[76:77], off
	global_load_ushort v131, v[78:79], off offset:2080
	global_load_ushort v132, v[80:81], off offset:2080
	global_load_ushort v127, v[76:77], off offset:32
	global_load_ushort v128, v[78:79], off offset:2112
	global_load_ushort v129, v[80:81], off offset:2112
	global_load_ushort v124, v[76:77], off offset:64
	global_load_ushort v123, v[78:79], off offset:2144
	global_load_ushort v125, v[80:81], off offset:2144
	global_load_ushort v126, v[76:77], off offset:96
	v_add_f32_e32 v78, v34, v38
	v_add_f32_e32 v78, v78, v42
	v_add_f32_e32 v78, v78, v46
	v_mov_b32_e32 v80, v34
	v_mov_b32_e32 v81, v38
	v_add_f32_dpp v78, v78, v78 quad_perm:[1,0,3,2] row_mask:0xf bank_mask:0xf bound_ctrl:1
	v_mov_b32_e32 v146, v46
	v_mov_b32_e32 v147, v42
	v_add_f32_dpp v78, v78, v78 quad_perm:[2,3,0,1] row_mask:0xf bank_mask:0xf bound_ctrl:1
	v_mov_b32_e32 v42, 0
	v_cmp_lt_i32_e32 vcc, 0, v66
	v_add_f32_dpp v78, v78, v78 row_half_mirror row_mask:0xf bank_mask:0xf bound_ctrl:1
	s_nop 1
	v_add_f32_dpp v78, v78, v78 row_mirror row_mask:0xf bank_mask:0xf bound_ctrl:1
	v_mul_f32_e32 v78, 0x3c800000, v78
	v_pk_add_f32 v[80:81], v[80:81], v[78:79] op_sel_hi:[1,0] neg_lo:[0,1] neg_hi:[0,1]
	v_pk_add_f32 v[78:79], v[146:147], v[78:79] op_sel_hi:[1,0] neg_lo:[0,1] neg_hi:[0,1]
	v_mul_f32_e32 v144, v80, v80
	v_mul_f32_e32 v145, v81, v81
	v_mul_f32_e32 v146, v78, v78
	v_mul_f32_e32 v147, v79, v79
	v_add_f32_e32 v34, v144, v145
	v_add_f32_e32 v34, v147, v34
	v_add_f32_e32 v34, v146, v34
	s_nop 1
	v_add_f32_dpp v34, v34, v34 quad_perm:[1,0,3,2] row_mask:0xf bank_mask:0xf bound_ctrl:1
	s_nop 1
	v_add_f32_dpp v34, v34, v34 quad_perm:[2,3,0,1] row_mask:0xf bank_mask:0xf bound_ctrl:1
	s_nop 1
	v_add_f32_dpp v38, v34, v34 row_half_mirror row_mask:0xf bank_mask:0xf bound_ctrl:1
	v_mov_b32_e32 v34, 0
	s_nop 0
	v_mov_b32_dpp v42, v38 row_mirror row_mask:0xf bank_mask:0xf
	s_and_saveexec_b64 s[0:1], vcc
	s_cbranch_execz .LBB0_1114
	global_load_ushort v34, v[72:73], off offset:2048
	s_waitcnt vmcnt(0)
	v_lshlrev_b32_e32 v34, 16, v34
	s_branch .LBB0_1114

; __device__ __forceinline__ float bf2f(unsigned v) { return __uint_as_float(v << 16); }
; __device__ __forceinline__ unsigned pk2(float lo, float hi) { const f32x2 f = {lo, hi}; const bf16n2 v = __builtin_convertvector(f, bf16n2); return __builtin_bit_cast(unsigned, v); }
; __device__ __forceinline__ float sigmoidf_(float x) { return __builtin_amdgcn_rcpf(1.0f + __expf(-x)); }
; __device__ __forceinline__ f32x4 unpack4(u32x2 z) { return (f32x4){__uint_as_float(z.x << 16), __uint_as_float(z.x & 0xffff0000u), __uint_as_float(z.y << 16), __uint_as_float(z.y & 0xffff0000u)}; }
;     ...
;         for (int qd = 0; qd < NQ; ++qd) {
;             const int tq = tw0 + 4 * qd + (n >> 2), hh = g * 4 + hr;
;             f32x4 accp[4]; u32x2 winp[4];
;             if (MODE == 3) {
; #pragma unroll
;                 for (int dt = 0; dt < 4; ++dt) { const int col = hh * 64 + 16 * dt + 4 * q; accp[dt] = unpack4(*(const u32x2*)((const bf16_t*)nsaacc + (size_t)tq * 512 + col)); winp[dt] = *(const u32x2*)(oout + (size_t)tq * 512 + col); } }
;             float scale;
;             if (MODE == 2) scale = 1.0f;
;             else { float lt = lrun[qd]; lt += __shfl_xor(lt, 16); lt += __shfl_xor(lt, 32);
;                 if (MODE == 0) { const float sink = sinkv; const float mf = fmaxf(mrun[qd], sink), cr = __expf(mrun[qd] - mf); scale = cr / (lt * cr + __expf(sink - mf)); }
;                 else scale = lt > 0.f ? 1.0f / lt : 0.f; }
;             if (MODE != 0) scale *= sigmoidf_(bf2f(graw[qd]));
; #pragma unroll
;             for (int dt = 0; dt < 4; ++dt) { const f32x4 o = O[qd][dt] * scale; const int col = hh * 64 + 16 * dt + 4 * q;
;                 if (MODE == 0 || MODE == 1) { u32x2 w; w.x = pk2(o[0], o[1]); w.y = pk2(o[2], o[3]); *(u32x2*)(oout + (size_t)tq * 512 + col) = w; }
;                 else if (MODE == 2) { u32x2 w; w.x = pk2(o[0], o[1]); w.y = pk2(o[2], o[3]); *(u32x2*)((bf16_t*)nsaacc + (size_t)tq * 512 + col) = w; }
;                 else { const f32x4 t2 = (accp[dt] + unpack4(winp[dt])) + o; u32x2 w; w.x = pk2(t2[0], t2[1]); w.y = pk2(t2[2], t2[3]); *(u32x2*)(oout + (size_t)tq * 512 + col) = w; } }
.LBB0_1120:
	v_readlane_b32 s0, v254, 29
	v_readlane_b32 s1, v254, 27
	v_readlane_b32 s2, v252, 29
	v_readlane_b32 s3, v252, 30
	s_lshl_b32 s0, s0, 4
	s_or_b32 s0, s0, s1
	s_lshl_b32 s0, s0, 2
	s_add_u32 s2, s2, s0
	s_addc_u32 s3, s3, 0
	s_and_saveexec_b64 s[4:5], s[8:9]
	v_mov_b32_e32 v250, 1
	global_atomic_add v188, v1, v250, s[2:3] offset:512 sc0
	s_or_b64 exec, exec, s[4:5]
	v_or_b32_e32 v58, s12, v156
	v_lshl_or_b32 v58, v58, 6, v189
	v_readlane_b32 s0, v252, 25
	v_lshlrev_b64 v[62:63], 10, v[196:197]
	v_readlane_b32 s1, v252, 26
	v_ashrrev_i32_e32 v59, 31, v58
	v_lshlrev_b64 v[60:61], 1, v[58:59]
	v_lshl_add_u64 v[64:65], s[0:1], 0, v[62:63]
	v_lshl_add_u64 v[58:59], v[64:65], 0, v[60:61]
	global_load_dwordx2 v[66:67], v[58:59], off
	global_load_dwordx2 v[68:69], v[58:59], off offset:32
	global_load_dwordx2 v[70:71], v[58:59], off offset:64
	global_load_dwordx2 v[110:111], v[58:59], off offset:96
	v_lshl_add_u64 v[58:59], s[88:89], 0, v[62:63]
	v_lshl_add_u64 v[58:59], v[58:59], 0, v[60:61]
	v_lshlrev_b64 v[62:63], 10, v[184:185]
	global_load_dwordx2 v[108:109], v[58:59], off
	global_load_dwordx2 v[106:107], v[58:59], off offset:32
	global_load_dwordx2 v[72:73], v[58:59], off offset:64
	global_load_dwordx2 v[112:113], v[58:59], off offset:96
	v_lshl_add_u64 v[64:65], s[0:1], 0, v[62:63]
	v_lshl_add_u64 v[64:65], v[64:65], 0, v[60:61]
	global_load_dwordx2 v[118:119], v[64:65], off
	global_load_dwordx2 v[120:121], v[64:65], off offset:32
	global_load_dwordx2 v[114:115], v[64:65], off offset:64
	global_load_dwordx2 v[116:117], v[64:65], off offset:96
	ds_bpermute_b32 v123, v230, v203
	ds_bpermute_b32 v122, v230, v202
	v_lshlrev_b32_e32 v64, 16, v235
	v_lshl_add_u64 v[62:63], s[88:89], 0, v[62:63]
	v_mul_f32_e32 v64, 0xbfb8aa3b, v64
	v_lshl_add_u64 v[60:61], v[62:63], 0, v[60:61]
	v_exp_f32_e32 v124, v64
	global_load_dwordx2 v[64:65], v[60:61], off
	global_load_dwordx2 v[62:63], v[60:61], off offset:32
	s_waitcnt lgkmcnt(0)
	v_add_f32_e32 v122, v202, v122
	v_add_f32_e32 v123, v203, v123
	v_add_f32_e32 v124, 1.0, v124
	v_rcp_f32_e32 v152, v124
	s_waitcnt vmcnt(13)
	v_lshlrev_b32_e32 v126, 16, v67
	v_and_b32_e32 v127, 0xffff0000, v67
	s_waitcnt vmcnt(12)
	v_lshlrev_b32_e32 v130, 16, v69
	v_and_b32_e32 v131, 0xffff0000, v69
	s_waitcnt vmcnt(11)
	v_lshlrev_b32_e32 v134, 16, v71
	v_and_b32_e32 v135, 0xffff0000, v71
	s_waitcnt vmcnt(9)
	v_lshlrev_b32_e32 v140, 16, v109
	v_and_b32_e32 v141, 0xffff0000, v109
	s_waitcnt vmcnt(8)
	v_lshlrev_b32_e32 v144, 16, v107
	v_and_b32_e32 v145, 0xffff0000, v107
	s_waitcnt vmcnt(7)
	v_lshlrev_b32_e32 v148, 16, v73
	v_and_b32_e32 v149, 0xffff0000, v73
	v_lshlrev_b32_e32 v132, 16, v70
	v_and_b32_e32 v133, 0xffff0000, v70
	v_lshlrev_b32_e32 v146, 16, v72
	v_and_b32_e32 v147, 0xffff0000, v72
	s_waitcnt vmcnt(4)
	v_lshlrev_b32_e32 v72, 16, v120
	v_and_b32_e32 v73, 0xffff0000, v120
	v_lshlrev_b32_e32 v70, 16, v121
	v_and_b32_e32 v71, 0xffff0000, v121
	v_add_f32_e32 v120, v126, v140
	v_add_f32_e32 v121, v127, v141
	v_add_f32_e32 v126, v130, v144
	v_add_f32_e32 v127, v131, v145
	v_add_f32_e32 v130, v134, v148
	v_add_f32_e32 v131, v135, v149
	ds_bpermute_b32 v135, v231, v123
	ds_bpermute_b32 v134, v231, v122
	v_lshlrev_b32_e32 v136, 16, v110
	v_and_b32_e32 v137, 0xffff0000, v110
	v_lshlrev_b32_e32 v110, 16, v111
	v_and_b32_e32 v111, 0xffff0000, v111
	v_lshlrev_b32_e32 v150, 16, v112
	v_and_b32_e32 v151, 0xffff0000, v112
	v_lshlrev_b32_e32 v112, 16, v113
	v_and_b32_e32 v113, 0xffff0000, v113
	v_lshlrev_b32_e32 v124, 16, v66
	v_and_b32_e32 v125, 0xffff0000, v66
	v_lshlrev_b32_e32 v128, 16, v68
	v_and_b32_e32 v129, 0xffff0000, v68
	s_waitcnt vmcnt(3)
	v_lshlrev_b32_e32 v68, 16, v114
	v_and_b32_e32 v69, 0xffff0000, v114
	v_lshlrev_b32_e32 v66, 16, v115
	v_add_f32_e32 v112, v110, v112
	v_add_f32_e32 v113, v111, v113
	v_and_b32_e32 v67, 0xffff0000, v115
	s_waitcnt vmcnt(2)
	v_lshlrev_b32_e32 v114, 16, v116
	v_and_b32_e32 v115, 0xffff0000, v116
	v_lshlrev_b32_e32 v110, 16, v117
	s_waitcnt lgkmcnt(0)
; __device__ __forceinline__ float bf2f(unsigned v) { return __uint_as_float(v << 16); }
; __device__ __forceinline__ unsigned pk2(float lo, float hi) { const f32x2 f = {lo, hi}; const bf16n2 v = __builtin_convertvector(f, bf16n2); return __builtin_bit_cast(unsigned, v); }
; __device__ __forceinline__ float sigmoidf_(float x) { return __builtin_amdgcn_rcpf(1.0f + __expf(-x)); }
; __device__ __forceinline__ f32x4 unpack4(u32x2 z) { return (f32x4){__uint_as_float(z.x << 16), __uint_as_float(z.x & 0xffff0000u), __uint_as_float(z.y << 16), __uint_as_float(z.y & 0xffff0000u)}; }
;     ...
;         for (int qd = 0; qd < NQ; ++qd) {
;             const int tq = tw0 + 4 * qd + (n >> 2), hh = g * 4 + hr;
;             f32x4 accp[4]; u32x2 winp[4];
;             if (MODE == 3) {
; #pragma unroll
;                 for (int dt = 0; dt < 4; ++dt) { const int col = hh * 64 + 16 * dt + 4 * q; accp[dt] = unpack4(*(const u32x2*)((const bf16_t*)nsaacc + (size_t)tq * 512 + col)); winp[dt] = *(const u32x2*)(oout + (size_t)tq * 512 + col); } }
;             float scale;
;             if (MODE == 2) scale = 1.0f;
;             else { float lt = lrun[qd]; lt += __shfl_xor(lt, 16); lt += __shfl_xor(lt, 32);
;                 if (MODE == 0) { const float sink = sinkv; const float mf = fmaxf(mrun[qd], sink), cr = __expf(mrun[qd] - mf); scale = cr / (lt * cr + __expf(sink - mf)); }
;                 else scale = lt > 0.f ? 1.0f / lt : 0.f; }
;             if (MODE != 0) scale *= sigmoidf_(bf2f(graw[qd]));
; #pragma unroll
;             for (int dt = 0; dt < 4; ++dt) { const f32x4 o = O[qd][dt] * scale; const int col = hh * 64 + 16 * dt + 4 * q;
;                 if (MODE == 0 || MODE == 1) { u32x2 w; w.x = pk2(o[0], o[1]); w.y = pk2(o[2], o[3]); *(u32x2*)(oout + (size_t)tq * 512 + col) = w; }
;                 else if (MODE == 2) { u32x2 w; w.x = pk2(o[0], o[1]); w.y = pk2(o[2], o[3]); *(u32x2*)((bf16_t*)nsaacc + (size_t)tq * 512 + col) = w; }
;                 else { const f32x4 t2 = (accp[dt] + unpack4(winp[dt])) + o; u32x2 w; w.x = pk2(t2[0], t2[1]); w.y = pk2(t2[2], t2[3]); *(u32x2*)(oout + (size_t)tq * 512 + col) = w; } }
	v_add_f32_e32 v122, v122, v134
	v_add_f32_e32 v123, v123, v135
	v_and_b32_e32 v111, 0xffff0000, v117
	global_load_dwordx2 v[116:117], v[60:61], off offset:64
	global_load_dwordx2 v[134:135], v[60:61], off offset:96
	v_lshlrev_b32_e32 v138, 16, v108
	v_and_b32_e32 v139, 0xffff0000, v108
	v_lshlrev_b32_e32 v142, 16, v106
	v_and_b32_e32 v143, 0xffff0000, v106
	v_lshlrev_b32_e32 v108, 16, v118
	v_and_b32_e32 v109, 0xffff0000, v118
	v_lshlrev_b32_e32 v106, 16, v119
	v_and_b32_e32 v107, 0xffff0000, v119
	v_add_f32_e32 v118, v124, v138
	v_add_f32_e32 v119, v125, v139
	v_add_f32_e32 v124, v128, v142
	v_add_f32_e32 v125, v129, v143
	v_add_f32_e32 v128, v132, v146
	v_add_f32_e32 v129, v133, v147
	v_add_f32_e32 v132, v136, v150
	v_add_f32_e32 v133, v137, v151
	v_div_scale_f32 v136, s[0:1], v123, v123, 1.0
	v_rcp_f32_e32 v137, v136
	s_nop 0
	v_fma_f32 v138, -v136, v137, 1.0
	v_fmac_f32_e32 v137, v138, v137
	v_div_scale_f32 v138, vcc, 1.0, v123, 1.0
	v_mul_f32_e32 v139, v138, v137
	v_fma_f32 v140, -v136, v139, v138
	v_fmac_f32_e32 v139, v140, v137
	v_fma_f32 v136, -v136, v139, v138
	v_div_fmas_f32 v136, v136, v137, v139
	v_div_fixup_f32 v136, v136, v123, 1.0
	v_cmp_lt_f32_e32 vcc, 0, v123
	s_nop 1
	v_cndmask_b32_e32 v123, 0, v136, vcc
	v_mul_f32_e32 v136, v152, v123
	v_fma_f32 v96, v96, v136, v130
	v_fma_f32 v97, v97, v136, v131
	v_fma_f32 v94, v94, v136, v128
	v_fma_f32 v95, v95, v136, v129
	v_fma_f32 v104, v104, v136, v120
	v_fma_f32 v105, v105, v136, v121
	v_cvt_pk_bf16_f32 v94, v94, v95
	v_cvt_pk_bf16_f32 v95, v96, v97
	global_store_dwordx2 v[58:59], v[94:95], off offset:64
	v_div_scale_f32 v94, s[0:1], v122, v122, 1.0
	v_rcp_f32_e32 v95, v94
	v_fma_f32 v102, v102, v136, v118
	v_fma_f32 v103, v103, v136, v119
	v_fma_f32 v100, v100, v136, v126
	v_fma_f32 v101, v101, v136, v127
	v_fma_f32 v98, v98, v136, v124
	v_fma_f32 v99, v99, v136, v125
	v_fma_f32 v92, v92, v136, v112
	v_fma_f32 v93, v93, v136, v113
	v_fma_f32 v90, v90, v136, v132
	v_fma_f32 v91, v91, v136, v133
	v_cvt_pk_bf16_f32 v102, v102, v103
	v_cvt_pk_bf16_f32 v103, v104, v105
	v_cvt_pk_bf16_f32 v98, v98, v99
	v_cvt_pk_bf16_f32 v99, v100, v101
	v_cvt_pk_bf16_f32 v90, v90, v91
	v_cvt_pk_bf16_f32 v91, v92, v93
	global_store_dwordx2 v[58:59], v[102:103], off
	global_store_dwordx2 v[58:59], v[98:99], off offset:32
	global_store_dwordx2 v[58:59], v[90:91], off offset:96
	v_fma_f32 v58, -v94, v95, 1.0
	v_fmac_f32_e32 v95, v58, v95
	v_div_scale_f32 v58, vcc, 1.0, v122, 1.0
	v_mul_f32_e32 v59, v58, v95
	v_fma_f32 v90, -v94, v59, v58
	v_fmac_f32_e32 v59, v90, v95
	v_lshlrev_b32_e32 v90, 16, v163
	v_mul_f32_e32 v90, 0xbfb8aa3b, v90
	v_exp_f32_e32 v90, v90
	v_fma_f32 v58, -v94, v59, v58
	v_div_fmas_f32 v58, v58, v95, v59
	v_div_fixup_f32 v58, v58, v122, 1.0
	v_add_f32_e32 v59, 1.0, v90
	v_rcp_f32_e32 v59, v59
	v_cmp_lt_f32_e32 vcc, 0, v122
	s_waitcnt vmcnt(7)
	v_lshlrev_b32_e32 v90, 16, v64
	v_and_b32_e32 v91, 0xffff0000, v64
	v_cndmask_b32_e32 v58, 0, v58, vcc
	v_lshlrev_b32_e32 v64, 16, v65
	v_and_b32_e32 v65, 0xffff0000, v65
	v_mul_f32_e32 v58, v59, v58
	v_add_f32_e32 v90, v108, v90
	v_add_f32_e32 v91, v109, v91
	v_add_f32_e32 v64, v106, v64
	v_add_f32_e32 v65, v107, v65
	v_fma_f32 v86, v86, v58, v90
	v_fma_f32 v87, v87, v58, v91
	v_fmac_f32_e32 v64, v88, v58
	v_fmac_f32_e32 v65, v89, v58
	v_cvt_pk_bf16_f32 v86, v86, v87
	v_cvt_pk_bf16_f32 v87, v64, v65
	s_waitcnt vmcnt(6)
	v_lshlrev_b32_e32 v64, 16, v62
	v_and_b32_e32 v65, 0xffff0000, v62
	v_lshlrev_b32_e32 v62, 16, v63
	v_and_b32_e32 v63, 0xffff0000, v63
	v_add_f32_e32 v64, v72, v64
	v_add_f32_e32 v65, v73, v65
	v_add_f32_e32 v62, v70, v62
	v_add_f32_e32 v63, v71, v63
	v_fmac_f32_e32 v64, v82, v58
	v_fmac_f32_e32 v65, v83, v58
	v_fmac_f32_e32 v62, v84, v58
	v_fmac_f32_e32 v63, v85, v58
	v_cvt_pk_bf16_f32 v64, v64, v65
	v_cvt_pk_bf16_f32 v65, v62, v63
	global_store_dwordx2 v[60:61], v[64:65], off offset:32
	s_waitcnt vmcnt(6)
	v_lshlrev_b32_e32 v62, 16, v116
	v_and_b32_e32 v63, 0xffff0000, v116
	v_lshlrev_b32_e32 v64, 16, v117
	v_and_b32_e32 v65, 0xffff0000, v117
	v_add_f32_e32 v62, v68, v62
	v_add_f32_e32 v63, v69, v63
	v_add_f32_e32 v64, v66, v64
	v_add_f32_e32 v65, v67, v65
	v_fmac_f32_e32 v62, v78, v58
	v_fmac_f32_e32 v63, v79, v58
	v_fmac_f32_e32 v64, v80, v58
	v_fmac_f32_e32 v65, v81, v58
	v_cvt_pk_bf16_f32 v62, v62, v63
	v_cvt_pk_bf16_f32 v63, v64, v65
	global_store_dwordx2 v[60:61], v[62:63], off offset:64
	s_waitcnt vmcnt(6)
	v_lshlrev_b32_e32 v62, 16, v134
	v_and_b32_e32 v63, 0xffff0000, v134
	v_lshlrev_b32_e32 v64, 16, v135
	v_and_b32_e32 v65, 0xffff0000, v135
	v_add_f32_e32 v62, v114, v62
	v_add_f32_e32 v63, v115, v63
	v_add_f32_e32 v64, v110, v64
	v_add_f32_e32 v65, v111, v65
	global_store_dwordx2 v[60:61], v[86:87], off
	v_fmac_f32_e32 v64, v76, v58
	v_fmac_f32_e32 v65, v77, v58
	v_fma_f32 v59, v75, v58, v63
	v_fma_f32 v58, v74, v58, v62
	s_nop 0
	v_cvt_pk_bf16_f32 v58, v58, v59
	v_cvt_pk_bf16_f32 v59, v64, v65
	global_store_dwordx2 v[60:61], v[58:59], off offset:96
	s_and_saveexec_b64 s[0:1], s[8:9]
	v_add_u32_e32 v250, 0x100, v188
	v_mov_b32_e32 v186, 0x26400
	ds_write_b32 v186, v250
	s_or_b64 exec, exec, s[0:1]
	s_waitcnt lgkmcnt(0)
	s_barrier
	v_mov_b32_e32 v186, 0x26400
	ds_read_b32 v250, v186
	s_waitcnt lgkmcnt(0)
	v_readfirstlane_b32 s20, v250
	s_cmpk_gt_i32 s20, 0x1ff
	s_cbranch_scc1 .LBB0_1310

; #define LAS __attribute__((address_space(3)))
;     ...
; #pragma unroll
;                         for (int kt = 0; kt < 4; ++kt) { sc[kt] = (f32x4){0.f, 0.f, 0.f, 0.f};
; #pragma unroll
;                             for (int ks = 0; ks < 2; ++ks) { const bf16x8 ak = (MODE != 3) ? akf[kt][ks] : akq[kt][ks];
;                                 sc[kt] = __builtin_amdgcn_mfma_f32_16x16x32_bf16(ak, Bq[qd][ks], sc[kt], 0, 0, 0); } }
;                         if (MODE == 3) {
; #pragma unroll
;                             for (int st = 0; st < 2; ++st)
; #pragma unroll
;                                 for (int dt = 0; dt < 4; ++dt) avq[st][dt] = *(const LAS bf16x8*)(L + LV + (16 * dt + n) * 128 + ((((4 * st + q) ^ n) & 7) << 4));
;                             __builtin_amdgcn_sched_barrier(0);
;                         }
;                         if (!far) {
;                             const LAS float* tp = (MODE == 2) ? biasd + hr * NT + (DOFF - tq + 31 + 16 * p0) + 64 * q : biasd + hr * NT + (DOFF - tq + p0) + 4 * q;
; #pragma unroll
;                             for (int kt = 0; kt < 4; ++kt)
; #pragma unroll
;                                 for (int r = 0; r < 4; ++r) sc[kt][r] += (MODE == 3) ? bia[kt][r] : ((MODE == 2) ? tp[256 * kt + 16 * r] : tp[16 * kt + r]);
;                         }
.LBB0_1160:
	s_waitcnt lgkmcnt(7)
	v_mfma_f32_16x16x32_bf16 v[106:109], v[106:109], v[58:61], 0
	s_waitcnt lgkmcnt(5)
	v_mfma_f32_16x16x32_bf16 v[150:153], v[126:129], v[62:65], v[106:109]
	v_mfma_f32_16x16x32_bf16 v[106:109], v[110:113], v[58:61], 0
	s_waitcnt lgkmcnt(4)
	v_mfma_f32_16x16x32_bf16 v[146:149], v[114:117], v[62:65], v[106:109]
	s_waitcnt lgkmcnt(3)
	v_mfma_f32_16x16x32_bf16 v[106:109], v[118:121], v[58:61], 0
	s_waitcnt lgkmcnt(1)
	v_mfma_f32_16x16x32_bf16 v[142:145], v[134:137], v[62:65], v[106:109]
	v_mfma_f32_16x16x32_bf16 v[106:109], v[122:125], v[58:61], 0
	s_waitcnt lgkmcnt(0)
	v_mfma_f32_16x16x32_bf16 v[110:113], v[130:133], v[62:65], v[106:109]
	ds_read_b128 v[138:141], v238 offset:8192
	ds_read_b128 v[134:137], v238 offset:10240
	ds_read_b128 v[130:133], v238 offset:12288
	ds_read_b128 v[126:129], v238 offset:14336
	ds_read_b128 v[122:125], v237 offset:8192
	ds_read_b128 v[118:121], v237 offset:10240
	ds_read_b128 v[114:117], v237 offset:12288
	ds_read_b128 v[106:109], v237 offset:14336
	s_and_b64 vcc, exec, s[2:3]
	s_cbranch_vccnz .LBB0_1162
	v_add_f32_e32 v152, v170, v152
	v_add_f32_e32 v153, v171, v153
	v_add_f32_e32 v150, v168, v150
	v_add_f32_e32 v151, v169, v151
	v_add_f32_e32 v148, v174, v148
	v_add_f32_e32 v149, v175, v149
	v_add_f32_e32 v146, v172, v146
	v_add_f32_e32 v147, v173, v147
	v_add_f32_e32 v144, v178, v144
	v_add_f32_e32 v145, v179, v145
	v_add_f32_e32 v142, v176, v142
	v_add_f32_e32 v143, v177, v143
	v_add_f32_e32 v112, v182, v112
	v_add_f32_e32 v113, v183, v113
	v_add_f32_e32 v110, v180, v110
	v_add_f32_e32 v111, v181, v111
	v_mov_b32_e32 v237, 0
	s_branch .LBB0_1163

;     ...
;                         const float bshift = far ? bfar : 0.f, boff = bshift * 1.4426950408889634f;
;                         float mx;
;                         { float m = fmaxf(fmaxf(sc[0][0], sc[0][1]), sc[0][2]);
;                           m = fmaxf(fmaxf(m, sc[0][3]), sc[1][0]); m = fmaxf(fmaxf(m, sc[1][1]), sc[1][2]); m = fmaxf(fmaxf(m, sc[1][3]), sc[2][0]);
;                           m = fmaxf(fmaxf(m, sc[2][1]), sc[2][2]); m = fmaxf(fmaxf(m, sc[2][3]), sc[3][0]); m = fmaxf(fmaxf(m, sc[3][1]), sc[3][2]); mx = fmaxf(m, sc[3][3]) + bshift; }
;                         if (MODE == 3 && !colsel) mx = -1e30f;
;                         float p[4][4];
;                         constexpr float L2E = 1.4426950408889634f;
;                         if (MODE == 2 && pass == 1) {
;                             const float negm1 = (mrun[qd] < -1e29f ? 0.f : -mrun[qd] * L2E) + boff + linv[qd];
; #pragma unroll
;                             for (int kt = 0; kt < 4; ++kt)
; #pragma unroll
;                                 for (int r = 0; r < 4; ++r) p[kt][r] = __builtin_amdgcn_exp2f(__builtin_fmaf(sc[kt][r], L2E, negm1));
;                         } else if (MODE == 2) {
;                             const float mn = fmaxf(mrun[qd], mx), corr = __expf(mrun[qd] - mn); mrun[qd] = mn; float ps = 0.f;
;                             const float negm0 = (mn < -1e29f ? 0.f : -mn * L2E) + boff;
; #pragma unroll
;                             for (int kt = 0; kt < 4; ++kt)
; #pragma unroll
;                                 for (int r = 0; r < 4; ++r) ps += __builtin_amdgcn_exp2f(__builtin_fmaf(sc[kt][r], L2E, negm0));
;                             lrun[qd] = lrun[qd] * corr + ps;
;                         } else {
;                             if (__any(mx > mrun[qd] + 6.0f)) {
;                                 mx = fmaxf(mx, __shfl_xor(mx, 16)); mx = fmaxf(mx, __shfl_xor(mx, 32));
;                                 const float mn = fmaxf(mrun[qd], mx), corr = __expf(mrun[qd] - mn); mrun[qd] = mn;
;                                 lrun[qd] *= corr;
; #pragma unroll
;                                 for (int dt = 0; dt < 4; ++dt) O[qd][dt] = O[qd][dt] * corr;
;                             }
;                             float negm = (mrun[qd] < -1e29f ? 0.f : -mrun[qd] * L2E) + boff; float ps = 0.f;
.LBB0_1163:
	v_and_b32_e32 v192, s0, v191
	v_cmp_eq_u32_e64 s[4:5], 0, v192
	v_max3_f32 v192, v150, v151, v152
	v_max3_f32 v192, v192, v153, v146
	v_max3_f32 v192, v192, v147, v148
	v_max3_f32 v192, v192, v149, v142
	v_max3_f32 v192, v192, v143, v144
	v_max3_f32 v192, v192, v145, v110
	v_max3_f32 v192, v192, v111, v112
	v_max_f32_e32 v192, v192, v113
	v_add_f32_e32 v192, v237, v192
	v_cndmask_b32_e64 v192, v192, v190, s[4:5]
	v_cmp_gt_f32_e32 vcc, v192, v188
	s_cbranch_vccz .LBB0_1165
	ds_bpermute_b32 v193, v230, v192
	v_max_f32_e32 v192, v192, v192
	s_waitcnt lgkmcnt(0)
	v_max_f32_e32 v193, v193, v193
	v_max_f32_e32 v192, v192, v193
	ds_bpermute_b32 v193, v231, v192
	s_waitcnt lgkmcnt(0)
	v_max3_f32 v193, v167, v192, v193
	v_sub_f32_e32 v167, v167, v193
	v_mul_f32_e32 v167, 0x3fb8aa3b, v167
	v_exp_f32_e32 v192, v167
	v_mov_b32_e32 v167, v193
	v_mul_f32_e32 v203, v203, v192
	v_mul_f32_e32 v104, v104, v192
	v_mul_f32_e32 v105, v105, v192
	v_mul_f32_e32 v102, v102, v192
	v_mul_f32_e32 v103, v103, v192
	v_mul_f32_e32 v100, v100, v192
	v_mul_f32_e32 v101, v101, v192
	v_mul_f32_e32 v98, v98, v192
	v_mul_f32_e32 v99, v99, v192
	v_mul_f32_e32 v96, v96, v192
	v_mul_f32_e32 v97, v97, v192
	v_mul_f32_e32 v94, v94, v192
	v_mul_f32_e32 v95, v95, v192
	v_mul_f32_e32 v92, v92, v192
	v_mul_f32_e32 v93, v93, v192
	v_mul_f32_e32 v90, v90, v192
	v_mul_f32_e32 v91, v91, v192
	v_add_f32_e32 v188, 0x40c00000, v193
	v_mul_f32_e32 v186, 0xbfb8aa3b, v193
	v_cmp_ngt_f32_e32 vcc, s30, v193
	s_nop 1
	v_cndmask_b32_e32 v186, 0, v186, vcc

; #define LAS __attribute__((address_space(3)))
;     ...
; #pragma unroll
;                         for (int kt = 0; kt < 4; ++kt) { sc[kt] = (f32x4){0.f, 0.f, 0.f, 0.f};
; #pragma unroll
;                             for (int ks = 0; ks < 2; ++ks) { const bf16x8 ak = (MODE != 3) ? akf[kt][ks] : akq[kt][ks];
;                                 sc[kt] = __builtin_amdgcn_mfma_f32_16x16x32_bf16(ak, Bq[qd][ks], sc[kt], 0, 0, 0); } }
;                         if (MODE == 3) {
; #pragma unroll
;                             for (int st = 0; st < 2; ++st)
; #pragma unroll
;                                 for (int dt = 0; dt < 4; ++dt) avq[st][dt] = *(const LAS bf16x8*)(L + LV + (16 * dt + n) * 128 + ((((4 * st + q) ^ n) & 7) << 4));
;                             __builtin_amdgcn_sched_barrier(0);
;                         }
;                         if (!far) {
;                             const LAS float* tp = (MODE == 2) ? biasd + hr * NT + (DOFF - tq + 31 + 16 * p0) + 64 * q : biasd + hr * NT + (DOFF - tq + p0) + 4 * q;
; #pragma unroll
;                             for (int kt = 0; kt < 4; ++kt)
; #pragma unroll
;                                 for (int r = 0; r < 4; ++r) sc[kt][r] += (MODE == 3) ? bia[kt][r] : ((MODE == 2) ? tp[256 * kt + 16 * r] : tp[16 * kt + r]);
;                         }
.LBB0_1169:
	s_waitcnt lgkmcnt(7)
	v_mfma_f32_16x16x32_bf16 v[106:109], v[106:109], v[66:69], 0
	s_waitcnt lgkmcnt(5)
	v_mfma_f32_16x16x32_bf16 v[150:153], v[126:129], v[70:73], v[106:109]
	v_mfma_f32_16x16x32_bf16 v[106:109], v[110:113], v[66:69], 0
	s_waitcnt lgkmcnt(4)
	v_mfma_f32_16x16x32_bf16 v[146:149], v[114:117], v[70:73], v[106:109]
	s_waitcnt lgkmcnt(3)
	v_mfma_f32_16x16x32_bf16 v[106:109], v[118:121], v[66:69], 0
	s_waitcnt lgkmcnt(1)
	v_mfma_f32_16x16x32_bf16 v[142:145], v[134:137], v[70:73], v[106:109]
	v_mfma_f32_16x16x32_bf16 v[106:109], v[122:125], v[66:69], 0
	s_waitcnt lgkmcnt(0)
	v_mfma_f32_16x16x32_bf16 v[110:113], v[130:133], v[70:73], v[106:109]
	ds_read_b128 v[138:141], v238 offset:8192
	ds_read_b128 v[134:137], v238 offset:10240
	ds_read_b128 v[130:133], v238 offset:12288
	ds_read_b128 v[126:129], v238 offset:14336
	ds_read_b128 v[122:125], v237 offset:8192
	ds_read_b128 v[118:121], v237 offset:10240
	ds_read_b128 v[114:117], v237 offset:12288
	ds_read_b128 v[106:109], v237 offset:14336
	s_and_b64 vcc, exec, s[2:3]
	s_cbranch_vccnz .LBB0_1171
	v_add_f32_e32 v152, v170, v152
	v_add_f32_e32 v153, v171, v153
	v_add_f32_e32 v150, v168, v150
	v_add_f32_e32 v151, v169, v151
	v_add_f32_e32 v148, v174, v148
	v_add_f32_e32 v149, v175, v149
	v_add_f32_e32 v146, v172, v146
	v_add_f32_e32 v147, v173, v147
	v_add_f32_e32 v144, v178, v144
	v_add_f32_e32 v145, v179, v145
	v_add_f32_e32 v142, v176, v142
	v_add_f32_e32 v143, v177, v143
	v_add_f32_e32 v112, v182, v112
	v_add_f32_e32 v113, v183, v113
	v_add_f32_e32 v110, v180, v110
	v_add_f32_e32 v111, v181, v111
	v_mov_b32_e32 v237, 0
	s_branch .LBB0_1172

;     ...
;                         const float bshift = far ? bfar : 0.f, boff = bshift * 1.4426950408889634f;
;                         float mx;
;                         { float m = fmaxf(fmaxf(sc[0][0], sc[0][1]), sc[0][2]);
;                           m = fmaxf(fmaxf(m, sc[0][3]), sc[1][0]); m = fmaxf(fmaxf(m, sc[1][1]), sc[1][2]); m = fmaxf(fmaxf(m, sc[1][3]), sc[2][0]);
;                           m = fmaxf(fmaxf(m, sc[2][1]), sc[2][2]); m = fmaxf(fmaxf(m, sc[2][3]), sc[3][0]); m = fmaxf(fmaxf(m, sc[3][1]), sc[3][2]); mx = fmaxf(m, sc[3][3]) + bshift; }
;                         if (MODE == 3 && !colsel) mx = -1e30f;
;                         float p[4][4];
;                         constexpr float L2E = 1.4426950408889634f;
;                         if (MODE == 2 && pass == 1) {
;                             const float negm1 = (mrun[qd] < -1e29f ? 0.f : -mrun[qd] * L2E) + boff + linv[qd];
; #pragma unroll
;                             for (int kt = 0; kt < 4; ++kt)
; #pragma unroll
;                                 for (int r = 0; r < 4; ++r) p[kt][r] = __builtin_amdgcn_exp2f(__builtin_fmaf(sc[kt][r], L2E, negm1));
;                         } else if (MODE == 2) {
;                             const float mn = fmaxf(mrun[qd], mx), corr = __expf(mrun[qd] - mn); mrun[qd] = mn; float ps = 0.f;
;                             const float negm0 = (mn < -1e29f ? 0.f : -mn * L2E) + boff;
; #pragma unroll
;                             for (int kt = 0; kt < 4; ++kt)
; #pragma unroll
;                                 for (int r = 0; r < 4; ++r) ps += __builtin_amdgcn_exp2f(__builtin_fmaf(sc[kt][r], L2E, negm0));
;                             lrun[qd] = lrun[qd] * corr + ps;
;                         } else {
;                             if (__any(mx > mrun[qd] + 6.0f)) {
;                                 mx = fmaxf(mx, __shfl_xor(mx, 16)); mx = fmaxf(mx, __shfl_xor(mx, 32));
;                                 const float mn = fmaxf(mrun[qd], mx), corr = __expf(mrun[qd] - mn); mrun[qd] = mn;
;                                 lrun[qd] *= corr;
; #pragma unroll
;                                 for (int dt = 0; dt < 4; ++dt) O[qd][dt] = O[qd][dt] * corr;
;                             }
;                             float negm = (mrun[qd] < -1e29f ? 0.f : -mrun[qd] * L2E) + boff; float ps = 0.f;
.LBB0_1172:
	v_and_b32_e32 v192, s0, v205
	v_cmp_eq_u32_e64 s[0:1], 0, v192
	v_max3_f32 v192, v150, v151, v152
	v_max3_f32 v192, v192, v153, v146
	v_max3_f32 v192, v192, v147, v148
	v_max3_f32 v192, v192, v149, v142
	v_max3_f32 v192, v192, v143, v144
	v_max3_f32 v192, v192, v145, v110
	v_max3_f32 v192, v192, v111, v112
	v_max_f32_e32 v192, v192, v113
	v_add_f32_e32 v192, v237, v192
	v_cndmask_b32_e64 v192, v192, v190, s[0:1]
	v_add_f32_e32 v193, 0x40c00000, v236
	v_cmp_gt_f32_e32 vcc, v192, v193
	s_cbranch_vccz .LBB0_1174
	ds_bpermute_b32 v193, v230, v192
	v_max_f32_e32 v192, v192, v192
	s_waitcnt lgkmcnt(0)
	v_max_f32_e32 v193, v193, v193
	v_max_f32_e32 v192, v192, v193
	ds_bpermute_b32 v193, v231, v192
	s_waitcnt lgkmcnt(0)
	v_max3_f32 v193, v236, v192, v193
	v_sub_f32_e32 v192, v236, v193
	v_mul_f32_e32 v192, 0x3fb8aa3b, v192
	v_exp_f32_e32 v192, v192
	v_mov_b32_e32 v236, v193
	v_mul_f32_e32 v202, v202, v192
	v_mul_f32_e32 v88, v88, v192
	v_mul_f32_e32 v89, v89, v192
	v_mul_f32_e32 v86, v86, v192
	v_mul_f32_e32 v87, v87, v192
	v_mul_f32_e32 v84, v84, v192
	v_mul_f32_e32 v85, v85, v192
	v_mul_f32_e32 v82, v82, v192
	v_mul_f32_e32 v83, v83, v192
	v_mul_f32_e32 v80, v80, v192
	v_mul_f32_e32 v81, v81, v192
	v_mul_f32_e32 v78, v78, v192
	v_mul_f32_e32 v79, v79, v192
	v_mul_f32_e32 v76, v76, v192
	v_mul_f32_e32 v77, v77, v192
	v_mul_f32_e32 v74, v74, v192
	v_mul_f32_e32 v75, v75, v192
	v_mul_f32_e32 v250, 0xbfb8aa3b, v193
	v_cmp_ngt_f32_e32 vcc, s30, v193
	s_nop 1
	v_cndmask_b32_e32 v250, 0, v250, vcc

; #define LAS __attribute__((address_space(3)))
;     ...
; #pragma unroll
;                         for (int kt = 0; kt < 4; ++kt) { sc[kt] = (f32x4){0.f, 0.f, 0.f, 0.f};
; #pragma unroll
;                             for (int ks = 0; ks < 2; ++ks) { const bf16x8 ak = (MODE != 3) ? akf[kt][ks] : akq[kt][ks];
;                                 sc[kt] = __builtin_amdgcn_mfma_f32_16x16x32_bf16(ak, Bq[qd][ks], sc[kt], 0, 0, 0); } }
;                         if (MODE == 3) {
; #pragma unroll
;                             for (int st = 0; st < 2; ++st)
; #pragma unroll
;                                 for (int dt = 0; dt < 4; ++dt) avq[st][dt] = *(const LAS bf16x8*)(L + LV + (16 * dt + n) * 128 + ((((4 * st + q) ^ n) & 7) << 4));
;                             __builtin_amdgcn_sched_barrier(0);
;                         }
;                         if (!far) {
;                             const LAS float* tp = (MODE == 2) ? biasd + hr * NT + (DOFF - tq + 31 + 16 * p0) + 64 * q : biasd + hr * NT + (DOFF - tq + p0) + 4 * q;
; #pragma unroll
;                             for (int kt = 0; kt < 4; ++kt)
; #pragma unroll
;                                 for (int r = 0; r < 4; ++r) sc[kt][r] += (MODE == 3) ? bia[kt][r] : ((MODE == 2) ? tp[256 * kt + 16 * r] : tp[16 * kt + r]);
;                         }
.LBB0_1182:
	s_waitcnt lgkmcnt(7)
	v_mfma_f32_16x16x32_bf16 v[106:109], v[106:109], v[58:61], 0
	s_waitcnt lgkmcnt(5)
	v_mfma_f32_16x16x32_bf16 v[150:153], v[126:129], v[62:65], v[106:109]
	v_mfma_f32_16x16x32_bf16 v[106:109], v[110:113], v[58:61], 0
	s_waitcnt lgkmcnt(4)
	v_mfma_f32_16x16x32_bf16 v[146:149], v[114:117], v[62:65], v[106:109]
	s_waitcnt lgkmcnt(3)
	v_mfma_f32_16x16x32_bf16 v[106:109], v[118:121], v[58:61], 0
	s_waitcnt lgkmcnt(1)
	v_mfma_f32_16x16x32_bf16 v[142:145], v[134:137], v[62:65], v[106:109]
	v_mfma_f32_16x16x32_bf16 v[106:109], v[122:125], v[58:61], 0
	s_waitcnt lgkmcnt(0)
	v_mfma_f32_16x16x32_bf16 v[110:113], v[130:133], v[62:65], v[106:109]
	ds_read_b128 v[138:141], v238 offset:24576
	ds_read_b128 v[134:137], v238 offset:26624
	ds_read_b128 v[130:133], v238 offset:28672
	ds_read_b128 v[126:129], v238 offset:30720
	ds_read_b128 v[122:125], v237 offset:24576
	ds_read_b128 v[118:121], v237 offset:26624
	ds_read_b128 v[114:117], v237 offset:28672
	ds_read_b128 v[106:109], v237 offset:30720
	s_and_b64 vcc, exec, s[2:3]
	s_cbranch_vccnz .LBB0_1184
	v_add_f32_e32 v152, v170, v152
	v_add_f32_e32 v153, v171, v153
	v_add_f32_e32 v150, v168, v150
	v_add_f32_e32 v151, v169, v151
	v_add_f32_e32 v148, v174, v148
	v_add_f32_e32 v149, v175, v149
	v_add_f32_e32 v146, v172, v146
	v_add_f32_e32 v147, v173, v147
	v_add_f32_e32 v144, v178, v144
	v_add_f32_e32 v145, v179, v145
	v_add_f32_e32 v142, v176, v142
	v_add_f32_e32 v143, v177, v143
	v_add_f32_e32 v112, v182, v112
	v_add_f32_e32 v113, v183, v113
	v_add_f32_e32 v110, v180, v110
	v_add_f32_e32 v111, v181, v111
	v_mov_b32_e32 v237, 0
	s_branch .LBB0_1185

; #define LAS __attribute__((address_space(3)))
;     ...
; #pragma unroll
;                         for (int kt = 0; kt < 4; ++kt) { sc[kt] = (f32x4){0.f, 0.f, 0.f, 0.f};
; #pragma unroll
;                             for (int ks = 0; ks < 2; ++ks) { const bf16x8 ak = (MODE != 3) ? akf[kt][ks] : akq[kt][ks];
;                                 sc[kt] = __builtin_amdgcn_mfma_f32_16x16x32_bf16(ak, Bq[qd][ks], sc[kt], 0, 0, 0); } }
;                         if (MODE == 3) {
; #pragma unroll
;                             for (int st = 0; st < 2; ++st)
; #pragma unroll
;                                 for (int dt = 0; dt < 4; ++dt) avq[st][dt] = *(const LAS bf16x8*)(L + LV + (16 * dt + n) * 128 + ((((4 * st + q) ^ n) & 7) << 4));
;                             __builtin_amdgcn_sched_barrier(0);
;                         }
;                         if (!far) {
;                             const LAS float* tp = (MODE == 2) ? biasd + hr * NT + (DOFF - tq + 31 + 16 * p0) + 64 * q : biasd + hr * NT + (DOFF - tq + p0) + 4 * q;
; #pragma unroll
;                             for (int kt = 0; kt < 4; ++kt)
; #pragma unroll
;                                 for (int r = 0; r < 4; ++r) sc[kt][r] += (MODE == 3) ? bia[kt][r] : ((MODE == 2) ? tp[256 * kt + 16 * r] : tp[16 * kt + r]);
;                         }
.LBB0_1191:
	s_waitcnt lgkmcnt(7)
	v_mfma_f32_16x16x32_bf16 v[106:109], v[106:109], v[66:69], 0
	s_waitcnt lgkmcnt(5)
	v_mfma_f32_16x16x32_bf16 v[150:153], v[126:129], v[70:73], v[106:109]
	v_mfma_f32_16x16x32_bf16 v[106:109], v[110:113], v[66:69], 0
	s_waitcnt lgkmcnt(4)
	v_mfma_f32_16x16x32_bf16 v[146:149], v[114:117], v[70:73], v[106:109]
	s_waitcnt lgkmcnt(3)
	v_mfma_f32_16x16x32_bf16 v[106:109], v[118:121], v[66:69], 0
	s_waitcnt lgkmcnt(1)
	v_mfma_f32_16x16x32_bf16 v[142:145], v[134:137], v[70:73], v[106:109]
	v_mfma_f32_16x16x32_bf16 v[106:109], v[122:125], v[66:69], 0
	s_waitcnt lgkmcnt(0)
	v_mfma_f32_16x16x32_bf16 v[110:113], v[130:133], v[70:73], v[106:109]
	ds_read_b128 v[138:141], v238 offset:24576
	ds_read_b128 v[134:137], v238 offset:26624
	ds_read_b128 v[130:133], v238 offset:28672
	ds_read_b128 v[126:129], v238 offset:30720
	ds_read_b128 v[122:125], v237 offset:24576
	ds_read_b128 v[118:121], v237 offset:26624
	ds_read_b128 v[114:117], v237 offset:28672
	ds_read_b128 v[106:109], v237 offset:30720
	s_and_b64 vcc, exec, s[2:3]
	s_cbranch_vccnz .LBB0_1193
	v_add_f32_e32 v152, v170, v152
	v_add_f32_e32 v153, v171, v153
	v_add_f32_e32 v150, v168, v150
	v_add_f32_e32 v151, v169, v151
	v_add_f32_e32 v148, v174, v148
	v_add_f32_e32 v149, v175, v149
	v_add_f32_e32 v146, v172, v146
	v_add_f32_e32 v147, v173, v147
	v_add_f32_e32 v144, v178, v144
	v_add_f32_e32 v145, v179, v145
	v_add_f32_e32 v142, v176, v142
	v_add_f32_e32 v143, v177, v143
	v_add_f32_e32 v112, v182, v112
	v_add_f32_e32 v113, v183, v113
	v_add_f32_e32 v110, v180, v110
	v_add_f32_e32 v111, v181, v111
	v_mov_b32_e32 v237, 0
	s_branch .LBB0_1194

; #define LAS __attribute__((address_space(3)))
;     ...
; #pragma unroll
;                         for (int kt = 0; kt < 4; ++kt) { sc[kt] = (f32x4){0.f, 0.f, 0.f, 0.f};
; #pragma unroll
;                             for (int ks = 0; ks < 2; ++ks) { const bf16x8 ak = (MODE != 3) ? akf[kt][ks] : akq[kt][ks];
;                                 sc[kt] = __builtin_amdgcn_mfma_f32_16x16x32_bf16(ak, Bq[qd][ks], sc[kt], 0, 0, 0); } }
;                         if (MODE == 3) {
; #pragma unroll
;                             for (int st = 0; st < 2; ++st)
; #pragma unroll
;                                 for (int dt = 0; dt < 4; ++dt) avq[st][dt] = *(const LAS bf16x8*)(L + LV + (16 * dt + n) * 128 + ((((4 * st + q) ^ n) & 7) << 4));
;                             __builtin_amdgcn_sched_barrier(0);
;                         }
;                         if (!far) {
;                             const LAS float* tp = (MODE == 2) ? biasd + hr * NT + (DOFF - tq + 31 + 16 * p0) + 64 * q : biasd + hr * NT + (DOFF - tq + p0) + 4 * q;
; #pragma unroll
;                             for (int kt = 0; kt < 4; ++kt)
; #pragma unroll
;                                 for (int r = 0; r < 4; ++r) sc[kt][r] += (MODE == 3) ? bia[kt][r] : ((MODE == 2) ? tp[256 * kt + 16 * r] : tp[16 * kt + r]);
;                         }
.LBB0_1204:
	s_waitcnt lgkmcnt(7)
	v_mfma_f32_16x16x32_bf16 v[106:109], v[106:109], v[58:61], 0
	s_waitcnt lgkmcnt(5)
	v_mfma_f32_16x16x32_bf16 v[150:153], v[126:129], v[62:65], v[106:109]
	v_mfma_f32_16x16x32_bf16 v[106:109], v[110:113], v[58:61], 0
	s_waitcnt lgkmcnt(4)
	v_mfma_f32_16x16x32_bf16 v[146:149], v[114:117], v[62:65], v[106:109]
	s_waitcnt lgkmcnt(3)
	v_mfma_f32_16x16x32_bf16 v[106:109], v[118:121], v[58:61], 0
	s_waitcnt lgkmcnt(1)
	v_mfma_f32_16x16x32_bf16 v[142:145], v[134:137], v[62:65], v[106:109]
	v_mfma_f32_16x16x32_bf16 v[106:109], v[122:125], v[58:61], 0
	s_waitcnt lgkmcnt(0)
	v_mfma_f32_16x16x32_bf16 v[110:113], v[130:133], v[62:65], v[106:109]
	ds_read_b128 v[138:141], v238 offset:40960
	ds_read_b128 v[134:137], v238 offset:43008
	ds_read_b128 v[130:133], v238 offset:45056
	ds_read_b128 v[126:129], v238 offset:47104
	ds_read_b128 v[122:125], v237 offset:40960
	ds_read_b128 v[118:121], v237 offset:43008
	ds_read_b128 v[114:117], v237 offset:45056
	ds_read_b128 v[106:109], v237 offset:47104
	s_and_b64 vcc, exec, s[2:3]
	s_cbranch_vccnz .LBB0_1206
	v_add_f32_e32 v152, v170, v152
	v_add_f32_e32 v153, v171, v153
	v_add_f32_e32 v150, v168, v150
	v_add_f32_e32 v151, v169, v151
	v_add_f32_e32 v148, v174, v148
	v_add_f32_e32 v149, v175, v149
	v_add_f32_e32 v146, v172, v146
	v_add_f32_e32 v147, v173, v147
	v_add_f32_e32 v144, v178, v144
	v_add_f32_e32 v145, v179, v145
	v_add_f32_e32 v142, v176, v142
	v_add_f32_e32 v143, v177, v143
	v_add_f32_e32 v112, v182, v112
	v_add_f32_e32 v113, v183, v113
	v_add_f32_e32 v110, v180, v110
	v_add_f32_e32 v111, v181, v111
	v_mov_b32_e32 v237, 0
	s_branch .LBB0_1207

; #define LAS __attribute__((address_space(3)))
;     ...
; #pragma unroll
;                         for (int kt = 0; kt < 4; ++kt) { sc[kt] = (f32x4){0.f, 0.f, 0.f, 0.f};
; #pragma unroll
;                             for (int ks = 0; ks < 2; ++ks) { const bf16x8 ak = (MODE != 3) ? akf[kt][ks] : akq[kt][ks];
;                                 sc[kt] = __builtin_amdgcn_mfma_f32_16x16x32_bf16(ak, Bq[qd][ks], sc[kt], 0, 0, 0); } }
;                         if (MODE == 3) {
; #pragma unroll
;                             for (int st = 0; st < 2; ++st)
; #pragma unroll
;                                 for (int dt = 0; dt < 4; ++dt) avq[st][dt] = *(const LAS bf16x8*)(L + LV + (16 * dt + n) * 128 + ((((4 * st + q) ^ n) & 7) << 4));
;                             __builtin_amdgcn_sched_barrier(0);
;                         }
;                         if (!far) {
;                             const LAS float* tp = (MODE == 2) ? biasd + hr * NT + (DOFF - tq + 31 + 16 * p0) + 64 * q : biasd + hr * NT + (DOFF - tq + p0) + 4 * q;
; #pragma unroll
;                             for (int kt = 0; kt < 4; ++kt)
; #pragma unroll
;                                 for (int r = 0; r < 4; ++r) sc[kt][r] += (MODE == 3) ? bia[kt][r] : ((MODE == 2) ? tp[256 * kt + 16 * r] : tp[16 * kt + r]);
;                         }
.LBB0_1213:
	s_waitcnt lgkmcnt(7)
	v_mfma_f32_16x16x32_bf16 v[106:109], v[106:109], v[66:69], 0
	s_waitcnt lgkmcnt(5)
	v_mfma_f32_16x16x32_bf16 v[150:153], v[126:129], v[70:73], v[106:109]
	v_mfma_f32_16x16x32_bf16 v[106:109], v[110:113], v[66:69], 0
	s_waitcnt lgkmcnt(4)
	v_mfma_f32_16x16x32_bf16 v[146:149], v[114:117], v[70:73], v[106:109]
	s_waitcnt lgkmcnt(3)
	v_mfma_f32_16x16x32_bf16 v[106:109], v[118:121], v[66:69], 0
	s_waitcnt lgkmcnt(1)
	v_mfma_f32_16x16x32_bf16 v[142:145], v[134:137], v[70:73], v[106:109]
	v_mfma_f32_16x16x32_bf16 v[106:109], v[122:125], v[66:69], 0
	s_waitcnt lgkmcnt(0)
	v_mfma_f32_16x16x32_bf16 v[110:113], v[130:133], v[70:73], v[106:109]
	ds_read_b128 v[138:141], v238 offset:40960
	ds_read_b128 v[134:137], v238 offset:43008
	ds_read_b128 v[130:133], v238 offset:45056
	ds_read_b128 v[126:129], v238 offset:47104
	ds_read_b128 v[122:125], v237 offset:40960
	ds_read_b128 v[118:121], v237 offset:43008
	ds_read_b128 v[114:117], v237 offset:45056
	ds_read_b128 v[106:109], v237 offset:47104
	s_and_b64 vcc, exec, s[2:3]
	s_cbranch_vccnz .LBB0_1215
	v_add_f32_e32 v152, v170, v152
	v_add_f32_e32 v153, v171, v153
	v_add_f32_e32 v150, v168, v150
	v_add_f32_e32 v151, v169, v151
	v_add_f32_e32 v148, v174, v148
	v_add_f32_e32 v149, v175, v149
	v_add_f32_e32 v146, v172, v146
	v_add_f32_e32 v147, v173, v147
	v_add_f32_e32 v144, v178, v144
	v_add_f32_e32 v145, v179, v145
	v_add_f32_e32 v142, v176, v142
	v_add_f32_e32 v143, v177, v143
	v_add_f32_e32 v112, v182, v112
	v_add_f32_e32 v113, v183, v113
	v_add_f32_e32 v110, v180, v110
	v_add_f32_e32 v111, v181, v111
	v_mov_b32_e32 v237, 0
	s_branch .LBB0_1216

; #define LAS __attribute__((address_space(3)))
;     ...
; #pragma unroll
;                         for (int kt = 0; kt < 4; ++kt) { sc[kt] = (f32x4){0.f, 0.f, 0.f, 0.f};
; #pragma unroll
;                             for (int ks = 0; ks < 2; ++ks) { const bf16x8 ak = (MODE != 3) ? akf[kt][ks] : akq[kt][ks];
;                                 sc[kt] = __builtin_amdgcn_mfma_f32_16x16x32_bf16(ak, Bq[qd][ks], sc[kt], 0, 0, 0); } }
;                         if (MODE == 3) {
; #pragma unroll
;                             for (int st = 0; st < 2; ++st)
; #pragma unroll
;                                 for (int dt = 0; dt < 4; ++dt) avq[st][dt] = *(const LAS bf16x8*)(L + LV + (16 * dt + n) * 128 + ((((4 * st + q) ^ n) & 7) << 4));
;                             __builtin_amdgcn_sched_barrier(0);
;                         }
;                         if (!far) {
;                             const LAS float* tp = (MODE == 2) ? biasd + hr * NT + (DOFF - tq + 31 + 16 * p0) + 64 * q : biasd + hr * NT + (DOFF - tq + p0) + 4 * q;
; #pragma unroll
;                             for (int kt = 0; kt < 4; ++kt)
; #pragma unroll
;                                 for (int r = 0; r < 4; ++r) sc[kt][r] += (MODE == 3) ? bia[kt][r] : ((MODE == 2) ? tp[256 * kt + 16 * r] : tp[16 * kt + r]);
;                         }
.LBB0_1226:
	s_waitcnt lgkmcnt(7)
	v_mfma_f32_16x16x32_bf16 v[106:109], v[106:109], v[58:61], 0
	s_waitcnt lgkmcnt(5)
	v_mfma_f32_16x16x32_bf16 v[150:153], v[126:129], v[62:65], v[106:109]
	v_mfma_f32_16x16x32_bf16 v[106:109], v[110:113], v[58:61], 0
	s_waitcnt lgkmcnt(4)
	v_mfma_f32_16x16x32_bf16 v[146:149], v[114:117], v[62:65], v[106:109]
	s_waitcnt lgkmcnt(3)
	v_mfma_f32_16x16x32_bf16 v[106:109], v[118:121], v[58:61], 0
	s_waitcnt lgkmcnt(1)
	v_mfma_f32_16x16x32_bf16 v[142:145], v[134:137], v[62:65], v[106:109]
	v_mfma_f32_16x16x32_bf16 v[106:109], v[122:125], v[58:61], 0
	s_waitcnt lgkmcnt(0)
	v_mfma_f32_16x16x32_bf16 v[110:113], v[130:133], v[62:65], v[106:109]
	ds_read_b128 v[138:141], v238 offset:57344
	ds_read_b128 v[134:137], v238 offset:59392
	ds_read_b128 v[130:133], v238 offset:61440
	ds_read_b128 v[126:129], v238 offset:63488
	ds_read_b128 v[122:125], v237 offset:57344
	ds_read_b128 v[118:121], v237 offset:59392
	ds_read_b128 v[114:117], v237 offset:61440
	ds_read_b128 v[106:109], v237 offset:63488
	s_and_b64 vcc, exec, s[2:3]
	s_cbranch_vccnz .LBB0_1228
	v_add_f32_e32 v152, v170, v152
	v_add_f32_e32 v153, v171, v153
	v_add_f32_e32 v150, v168, v150
	v_add_f32_e32 v151, v169, v151
	v_add_f32_e32 v148, v174, v148
	v_add_f32_e32 v149, v175, v149
	v_add_f32_e32 v146, v172, v146
	v_add_f32_e32 v147, v173, v147
	v_add_f32_e32 v144, v178, v144
	v_add_f32_e32 v145, v179, v145
	v_add_f32_e32 v142, v176, v142
	v_add_f32_e32 v143, v177, v143
	v_add_f32_e32 v112, v182, v112
	v_add_f32_e32 v113, v183, v113
	v_add_f32_e32 v110, v180, v110
	v_add_f32_e32 v111, v181, v111
	v_mov_b32_e32 v239, 0
	s_branch .LBB0_1229

;     ...
;                         const float bshift = far ? bfar : 0.f, boff = bshift * 1.4426950408889634f;
;                         float mx;
;                         { float m = fmaxf(fmaxf(sc[0][0], sc[0][1]), sc[0][2]);
;                           m = fmaxf(fmaxf(m, sc[0][3]), sc[1][0]); m = fmaxf(fmaxf(m, sc[1][1]), sc[1][2]); m = fmaxf(fmaxf(m, sc[1][3]), sc[2][0]);
;                           m = fmaxf(fmaxf(m, sc[2][1]), sc[2][2]); m = fmaxf(fmaxf(m, sc[2][3]), sc[3][0]); m = fmaxf(fmaxf(m, sc[3][1]), sc[3][2]); mx = fmaxf(m, sc[3][3]) + bshift; }
;                         if (MODE == 3 && !colsel) mx = -1e30f;
;                         float p[4][4];
;                         constexpr float L2E = 1.4426950408889634f;
;                         if (MODE == 2 && pass == 1) {
;                             const float negm1 = (mrun[qd] < -1e29f ? 0.f : -mrun[qd] * L2E) + boff + linv[qd];
; #pragma unroll
;                             for (int kt = 0; kt < 4; ++kt)
; #pragma unroll
;                                 for (int r = 0; r < 4; ++r) p[kt][r] = __builtin_amdgcn_exp2f(__builtin_fmaf(sc[kt][r], L2E, negm1));
;                         } else if (MODE == 2) {
;                             const float mn = fmaxf(mrun[qd], mx), corr = __expf(mrun[qd] - mn); mrun[qd] = mn; float ps = 0.f;
;                             const float negm0 = (mn < -1e29f ? 0.f : -mn * L2E) + boff;
; #pragma unroll
;                             for (int kt = 0; kt < 4; ++kt)
; #pragma unroll
;                                 for (int r = 0; r < 4; ++r) ps += __builtin_amdgcn_exp2f(__builtin_fmaf(sc[kt][r], L2E, negm0));
;                             lrun[qd] = lrun[qd] * corr + ps;
;                         } else {
;                             if (__any(mx > mrun[qd] + 6.0f)) {
;                                 mx = fmaxf(mx, __shfl_xor(mx, 16)); mx = fmaxf(mx, __shfl_xor(mx, 32));
;                                 const float mn = fmaxf(mrun[qd], mx), corr = __expf(mrun[qd] - mn); mrun[qd] = mn;
;                                 lrun[qd] *= corr;
; #pragma unroll
;                                 for (int dt = 0; dt < 4; ++dt) O[qd][dt] = O[qd][dt] * corr;
;                             }
;                             float negm = (mrun[qd] < -1e29f ? 0.f : -mrun[qd] * L2E) + boff; float ps = 0.f;
.LBB0_1229:
	v_and_b32_e32 v192, s0, v191
	v_cmp_eq_u32_e64 s[4:5], 0, v192
	v_max3_f32 v192, v150, v151, v152
	v_max3_f32 v192, v192, v153, v146
	v_max3_f32 v192, v192, v147, v148
	v_max3_f32 v192, v192, v149, v142
	v_max3_f32 v192, v192, v143, v144
	v_max3_f32 v192, v192, v145, v110
	v_max3_f32 v192, v192, v111, v112
	v_max_f32_e32 v192, v192, v113
	v_add_f32_e32 v192, v239, v192
	v_cndmask_b32_e64 v192, v192, v190, s[4:5]
	v_cmp_gt_f32_e32 vcc, v192, v188
	s_cbranch_vccz .LBB0_1231
	ds_bpermute_b32 v193, v230, v192
	v_max_f32_e32 v192, v192, v192
	s_waitcnt lgkmcnt(0)
	v_max_f32_e32 v193, v193, v193
	v_max_f32_e32 v192, v192, v193
	ds_bpermute_b32 v193, v231, v192
	s_waitcnt lgkmcnt(0)
	v_max3_f32 v193, v167, v192, v193
	v_sub_f32_e32 v167, v167, v193
	v_mul_f32_e32 v167, 0x3fb8aa3b, v167
	v_exp_f32_e32 v192, v167
	v_mov_b32_e32 v167, v193
	v_mul_f32_e32 v203, v203, v192
	v_mul_f32_e32 v104, v104, v192
	v_mul_f32_e32 v105, v105, v192
	v_mul_f32_e32 v102, v102, v192
	v_mul_f32_e32 v103, v103, v192
	v_mul_f32_e32 v100, v100, v192
	v_mul_f32_e32 v101, v101, v192
	v_mul_f32_e32 v98, v98, v192
	v_mul_f32_e32 v99, v99, v192
	v_mul_f32_e32 v96, v96, v192
	v_mul_f32_e32 v97, v97, v192
	v_mul_f32_e32 v94, v94, v192
	v_mul_f32_e32 v95, v95, v192
	v_mul_f32_e32 v92, v92, v192
	v_mul_f32_e32 v93, v93, v192
	v_mul_f32_e32 v90, v90, v192
	v_mul_f32_e32 v91, v91, v192
	v_add_f32_e32 v188, 0x40c00000, v193
	v_mul_f32_e32 v186, 0xbfb8aa3b, v193
	v_cmp_ngt_f32_e32 vcc, s30, v193
	s_nop 1
	v_cndmask_b32_e32 v186, 0, v186, vcc

; #define LAS __attribute__((address_space(3)))
;     ...
; #pragma unroll
;                         for (int kt = 0; kt < 4; ++kt) { sc[kt] = (f32x4){0.f, 0.f, 0.f, 0.f};
; #pragma unroll
;                             for (int ks = 0; ks < 2; ++ks) { const bf16x8 ak = (MODE != 3) ? akf[kt][ks] : akq[kt][ks];
;                                 sc[kt] = __builtin_amdgcn_mfma_f32_16x16x32_bf16(ak, Bq[qd][ks], sc[kt], 0, 0, 0); } }
;                         if (MODE == 3) {
; #pragma unroll
;                             for (int st = 0; st < 2; ++st)
; #pragma unroll
;                                 for (int dt = 0; dt < 4; ++dt) avq[st][dt] = *(const LAS bf16x8*)(L + LV + (16 * dt + n) * 128 + ((((4 * st + q) ^ n) & 7) << 4));
;                             __builtin_amdgcn_sched_barrier(0);
;                         }
;                         if (!far) {
;                             const LAS float* tp = (MODE == 2) ? biasd + hr * NT + (DOFF - tq + 31 + 16 * p0) + 64 * q : biasd + hr * NT + (DOFF - tq + p0) + 4 * q;
; #pragma unroll
;                             for (int kt = 0; kt < 4; ++kt)
; #pragma unroll
;                                 for (int r = 0; r < 4; ++r) sc[kt][r] += (MODE == 3) ? bia[kt][r] : ((MODE == 2) ? tp[256 * kt + 16 * r] : tp[16 * kt + r]);
;                         }
.LBB0_1235:
	s_waitcnt lgkmcnt(7)
	v_mfma_f32_16x16x32_bf16 v[106:109], v[106:109], v[66:69], 0
	s_waitcnt lgkmcnt(5)
	v_mfma_f32_16x16x32_bf16 v[150:153], v[126:129], v[70:73], v[106:109]
	v_mfma_f32_16x16x32_bf16 v[106:109], v[110:113], v[66:69], 0
	s_waitcnt lgkmcnt(4)
	v_mfma_f32_16x16x32_bf16 v[146:149], v[114:117], v[70:73], v[106:109]
	s_waitcnt lgkmcnt(3)
	v_mfma_f32_16x16x32_bf16 v[106:109], v[118:121], v[66:69], 0
	s_waitcnt lgkmcnt(1)
	v_mfma_f32_16x16x32_bf16 v[142:145], v[134:137], v[70:73], v[106:109]
	v_mfma_f32_16x16x32_bf16 v[106:109], v[122:125], v[66:69], 0
	s_waitcnt lgkmcnt(0)
	v_mfma_f32_16x16x32_bf16 v[110:113], v[130:133], v[70:73], v[106:109]
	ds_read_b128 v[138:141], v238 offset:57344
	ds_read_b128 v[134:137], v238 offset:59392
	ds_read_b128 v[130:133], v238 offset:61440
	ds_read_b128 v[126:129], v238 offset:63488
	ds_read_b128 v[122:125], v237 offset:57344
	ds_read_b128 v[118:121], v237 offset:59392
	ds_read_b128 v[114:117], v237 offset:61440
	ds_read_b128 v[106:109], v237 offset:63488
	s_and_b64 vcc, exec, s[2:3]
	s_cbranch_vccnz .LBB0_1237
	v_add_f32_e32 v152, v170, v152
	v_add_f32_e32 v153, v171, v153
	v_add_f32_e32 v150, v168, v150
	v_add_f32_e32 v151, v169, v151
	v_add_f32_e32 v148, v174, v148
	v_add_f32_e32 v149, v175, v149
	v_add_f32_e32 v146, v172, v146
	v_add_f32_e32 v147, v173, v147
	v_add_f32_e32 v144, v178, v144
	v_add_f32_e32 v145, v179, v145
	v_add_f32_e32 v142, v176, v142
	v_add_f32_e32 v143, v177, v143
	v_add_f32_e32 v112, v182, v112
	v_add_f32_e32 v113, v183, v113
	v_add_f32_e32 v110, v180, v110
	v_add_f32_e32 v111, v181, v111
	v_mov_b32_e32 v237, 0
	s_branch .LBB0_1238

; #define LAS __attribute__((address_space(3)))
;     ...
; #pragma unroll
;                         for (int kt = 0; kt < 4; ++kt) { sc[kt] = (f32x4){0.f, 0.f, 0.f, 0.f};
; #pragma unroll
;                             for (int ks = 0; ks < 2; ++ks) { const bf16x8 ak = (MODE != 3) ? akf[kt][ks] : akq[kt][ks];
;                                 sc[kt] = __builtin_amdgcn_mfma_f32_16x16x32_bf16(ak, Bq[qd][ks], sc[kt], 0, 0, 0); } }
;                         if (MODE == 3) {
; #pragma unroll
;                             for (int st = 0; st < 2; ++st)
; #pragma unroll
;                                 for (int dt = 0; dt < 4; ++dt) avq[st][dt] = *(const LAS bf16x8*)(L + LV + (16 * dt + n) * 128 + ((((4 * st + q) ^ n) & 7) << 4));
;                             __builtin_amdgcn_sched_barrier(0);
;                         }
;                         if (!far) {
;                             const LAS float* tp = (MODE == 2) ? biasd + hr * NT + (DOFF - tq + 31 + 16 * p0) + 64 * q : biasd + hr * NT + (DOFF - tq + p0) + 4 * q;
; #pragma unroll
;                             for (int kt = 0; kt < 4; ++kt)
; #pragma unroll
;                                 for (int r = 0; r < 4; ++r) sc[kt][r] += (MODE == 3) ? bia[kt][r] : ((MODE == 2) ? tp[256 * kt + 16 * r] : tp[16 * kt + r]);
;                         }
.LBB0_1248:
	s_waitcnt lgkmcnt(7)
	v_mfma_f32_16x16x32_bf16 v[106:109], v[106:109], v[58:61], 0
	s_waitcnt lgkmcnt(6)
	v_mfma_f32_16x16x32_bf16 v[150:153], v[110:113], v[62:65], v[106:109]
	v_add_u32_e32 v110, v207, v195
	s_waitcnt lgkmcnt(5)
	v_mfma_f32_16x16x32_bf16 v[106:109], v[114:117], v[58:61], 0
	s_waitcnt lgkmcnt(4)
	v_mfma_f32_16x16x32_bf16 v[146:149], v[118:121], v[62:65], v[106:109]
	s_waitcnt lgkmcnt(3)
	v_mfma_f32_16x16x32_bf16 v[106:109], v[122:125], v[58:61], 0
	s_waitcnt lgkmcnt(2)
	v_mfma_f32_16x16x32_bf16 v[142:145], v[126:129], v[62:65], v[106:109]
	s_waitcnt lgkmcnt(1)
	v_mfma_f32_16x16x32_bf16 v[106:109], v[130:133], v[58:61], 0
	s_waitcnt lgkmcnt(0)
	v_mfma_f32_16x16x32_bf16 v[106:109], v[134:137], v[62:65], v[106:109]
	ds_read_b128 v[138:141], v110
	ds_read_b128 v[130:133], v110 offset:2048
	ds_read_b128 v[134:137], v110 offset:4096
	ds_read_b128 v[126:129], v110 offset:6144
	v_add_u32_e32 v110, v207, v204
	ds_read_b128 v[122:125], v110
	ds_read_b128 v[118:121], v110 offset:2048
	ds_read_b128 v[114:117], v110 offset:4096
	ds_read_b128 v[110:113], v110 offset:6144
	s_and_b64 vcc, exec, s[2:3]
	s_cbranch_vccnz .LBB0_1250
	v_add_f32_e32 v152, v170, v152
	v_add_f32_e32 v153, v171, v153
	v_add_f32_e32 v150, v168, v150
	v_add_f32_e32 v151, v169, v151
	v_add_f32_e32 v148, v174, v148
	v_add_f32_e32 v149, v175, v149
	v_add_f32_e32 v146, v172, v146
	v_add_f32_e32 v147, v173, v147
	v_add_f32_e32 v144, v178, v144
	v_add_f32_e32 v145, v179, v145
	v_add_f32_e32 v142, v176, v142
	v_add_f32_e32 v143, v177, v143
	v_add_f32_e32 v108, v182, v108
	v_add_f32_e32 v109, v183, v109
	v_add_f32_e32 v106, v180, v106
	v_add_f32_e32 v107, v181, v107
	v_mov_b32_e32 v248, 0
	s_branch .LBB0_1251

;     ...
;                         const float bshift = far ? bfar : 0.f, boff = bshift * 1.4426950408889634f;
;                         float mx;
;                         { float m = fmaxf(fmaxf(sc[0][0], sc[0][1]), sc[0][2]);
;                           m = fmaxf(fmaxf(m, sc[0][3]), sc[1][0]); m = fmaxf(fmaxf(m, sc[1][1]), sc[1][2]); m = fmaxf(fmaxf(m, sc[1][3]), sc[2][0]);
;                           m = fmaxf(fmaxf(m, sc[2][1]), sc[2][2]); m = fmaxf(fmaxf(m, sc[2][3]), sc[3][0]); m = fmaxf(fmaxf(m, sc[3][1]), sc[3][2]); mx = fmaxf(m, sc[3][3]) + bshift; }
;                         if (MODE == 3 && !colsel) mx = -1e30f;
;                         float p[4][4];
;                         constexpr float L2E = 1.4426950408889634f;
;                         if (MODE == 2 && pass == 1) {
;                             const float negm1 = (mrun[qd] < -1e29f ? 0.f : -mrun[qd] * L2E) + boff + linv[qd];
; #pragma unroll
;                             for (int kt = 0; kt < 4; ++kt)
; #pragma unroll
;                                 for (int r = 0; r < 4; ++r) p[kt][r] = __builtin_amdgcn_exp2f(__builtin_fmaf(sc[kt][r], L2E, negm1));
;                         } else if (MODE == 2) {
;                             const float mn = fmaxf(mrun[qd], mx), corr = __expf(mrun[qd] - mn); mrun[qd] = mn; float ps = 0.f;
;                             const float negm0 = (mn < -1e29f ? 0.f : -mn * L2E) + boff;
; #pragma unroll
;                             for (int kt = 0; kt < 4; ++kt)
; #pragma unroll
;                                 for (int r = 0; r < 4; ++r) ps += __builtin_amdgcn_exp2f(__builtin_fmaf(sc[kt][r], L2E, negm0));
;                             lrun[qd] = lrun[qd] * corr + ps;
;                         } else {
;                             if (__any(mx > mrun[qd] + 6.0f)) {
;                                 mx = fmaxf(mx, __shfl_xor(mx, 16)); mx = fmaxf(mx, __shfl_xor(mx, 32));
;                                 const float mn = fmaxf(mrun[qd], mx), corr = __expf(mrun[qd] - mn); mrun[qd] = mn;
;                                 lrun[qd] *= corr;
; #pragma unroll
;                                 for (int dt = 0; dt < 4; ++dt) O[qd][dt] = O[qd][dt] * corr;
;                             }
;                             float negm = (mrun[qd] < -1e29f ? 0.f : -mrun[qd] * L2E) + boff; float ps = 0.f;
.LBB0_1251:
	v_and_b32_e32 v192, s0, v191
	v_cmp_eq_u32_e64 s[4:5], 0, v192
	v_max3_f32 v192, v150, v151, v152
	v_max3_f32 v192, v192, v153, v146
	v_max3_f32 v192, v192, v147, v148
	v_max3_f32 v192, v192, v149, v142
	v_max3_f32 v192, v192, v143, v144
	v_max3_f32 v192, v192, v145, v106
	v_max3_f32 v192, v192, v107, v108
	v_max_f32_e32 v192, v192, v109
	v_add_f32_e32 v192, v248, v192
	v_cndmask_b32_e64 v192, v192, v190, s[4:5]
	v_cmp_gt_f32_e32 vcc, v192, v188
	s_cbranch_vccz .LBB0_1253
	ds_bpermute_b32 v193, v230, v192
	v_max_f32_e32 v192, v192, v192
	s_waitcnt lgkmcnt(0)
	v_max_f32_e32 v193, v193, v193
	v_max_f32_e32 v192, v192, v193
	ds_bpermute_b32 v193, v231, v192
	s_waitcnt lgkmcnt(0)
	v_max3_f32 v193, v167, v192, v193
	v_sub_f32_e32 v167, v167, v193
	v_mul_f32_e32 v167, 0x3fb8aa3b, v167
	v_exp_f32_e32 v192, v167
	v_mov_b32_e32 v167, v193
	v_mul_f32_e32 v203, v203, v192
	v_mul_f32_e32 v104, v104, v192
	v_mul_f32_e32 v105, v105, v192
	v_mul_f32_e32 v102, v102, v192
	v_mul_f32_e32 v103, v103, v192
	v_mul_f32_e32 v100, v100, v192
	v_mul_f32_e32 v101, v101, v192
	v_mul_f32_e32 v98, v98, v192
	v_mul_f32_e32 v99, v99, v192
	v_mul_f32_e32 v96, v96, v192
	v_mul_f32_e32 v97, v97, v192
	v_mul_f32_e32 v94, v94, v192
	v_mul_f32_e32 v95, v95, v192
	v_mul_f32_e32 v92, v92, v192
	v_mul_f32_e32 v93, v93, v192
	v_mul_f32_e32 v90, v90, v192
	v_mul_f32_e32 v91, v91, v192
	v_add_f32_e32 v188, 0x40c00000, v193
	v_mul_f32_e32 v186, 0xbfb8aa3b, v193
	v_cmp_ngt_f32_e32 vcc, s30, v193
	s_nop 1
	v_cndmask_b32_e32 v186, 0, v186, vcc

; #define LAS __attribute__((address_space(3)))
;     ...
; #pragma unroll
;                         for (int kt = 0; kt < 4; ++kt) { sc[kt] = (f32x4){0.f, 0.f, 0.f, 0.f};
; #pragma unroll
;                             for (int ks = 0; ks < 2; ++ks) { const bf16x8 ak = (MODE != 3) ? akf[kt][ks] : akq[kt][ks];
;                                 sc[kt] = __builtin_amdgcn_mfma_f32_16x16x32_bf16(ak, Bq[qd][ks], sc[kt], 0, 0, 0); } }
;                         if (MODE == 3) {
; #pragma unroll
;                             for (int st = 0; st < 2; ++st)
; #pragma unroll
;                                 for (int dt = 0; dt < 4; ++dt) avq[st][dt] = *(const LAS bf16x8*)(L + LV + (16 * dt + n) * 128 + ((((4 * st + q) ^ n) & 7) << 4));
;                             __builtin_amdgcn_sched_barrier(0);
;                         }
;                         if (!far) {
;                             const LAS float* tp = (MODE == 2) ? biasd + hr * NT + (DOFF - tq + 31 + 16 * p0) + 64 * q : biasd + hr * NT + (DOFF - tq + p0) + 4 * q;
; #pragma unroll
;                             for (int kt = 0; kt < 4; ++kt)
; #pragma unroll
;                                 for (int r = 0; r < 4; ++r) sc[kt][r] += (MODE == 3) ? bia[kt][r] : ((MODE == 2) ? tp[256 * kt + 16 * r] : tp[16 * kt + r]);
;                         }
.LBB0_1257:
	s_waitcnt lgkmcnt(7)
	v_mfma_f32_16x16x32_bf16 v[106:109], v[106:109], v[66:69], 0
	s_waitcnt lgkmcnt(6)
	v_mfma_f32_16x16x32_bf16 v[150:153], v[110:113], v[70:73], v[106:109]
	v_add_u32_e32 v110, v207, v195
	s_waitcnt lgkmcnt(5)
	v_mfma_f32_16x16x32_bf16 v[106:109], v[114:117], v[66:69], 0
	s_waitcnt lgkmcnt(4)
	v_mfma_f32_16x16x32_bf16 v[146:149], v[118:121], v[70:73], v[106:109]
	s_waitcnt lgkmcnt(3)
	v_mfma_f32_16x16x32_bf16 v[106:109], v[122:125], v[66:69], 0
	s_waitcnt lgkmcnt(2)
	v_mfma_f32_16x16x32_bf16 v[142:145], v[126:129], v[70:73], v[106:109]
	s_waitcnt lgkmcnt(1)
	v_mfma_f32_16x16x32_bf16 v[106:109], v[130:133], v[66:69], 0
	s_waitcnt lgkmcnt(0)
	v_mfma_f32_16x16x32_bf16 v[106:109], v[134:137], v[70:73], v[106:109]
	ds_read_b128 v[138:141], v110
	ds_read_b128 v[130:133], v110 offset:2048
	ds_read_b128 v[134:137], v110 offset:4096
	ds_read_b128 v[126:129], v110 offset:6144
	v_add_u32_e32 v110, v207, v204
	ds_read_b128 v[122:125], v110
	ds_read_b128 v[118:121], v110 offset:2048
	ds_read_b128 v[114:117], v110 offset:4096
	ds_read_b128 v[110:113], v110 offset:6144
	s_and_b64 vcc, exec, s[2:3]
	s_cbranch_vccnz .LBB0_1259
	v_add_f32_e32 v152, v170, v152
	v_add_f32_e32 v153, v171, v153
	v_add_f32_e32 v150, v168, v150
	v_add_f32_e32 v151, v169, v151
	v_add_f32_e32 v148, v174, v148
	v_add_f32_e32 v149, v175, v149
	v_add_f32_e32 v146, v172, v146
	v_add_f32_e32 v147, v173, v147
	v_add_f32_e32 v144, v178, v144
	v_add_f32_e32 v145, v179, v145
	v_add_f32_e32 v142, v176, v142
	v_add_f32_e32 v143, v177, v143
	v_add_f32_e32 v108, v182, v108
	v_add_f32_e32 v109, v183, v109
	v_add_f32_e32 v106, v180, v106
	v_add_f32_e32 v107, v181, v107
	v_mov_b32_e32 v237, 0
	s_branch .LBB0_1260

;     ...
;                         const float bshift = far ? bfar : 0.f, boff = bshift * 1.4426950408889634f;
;                         float mx;
;                         { float m = fmaxf(fmaxf(sc[0][0], sc[0][1]), sc[0][2]);
;                           m = fmaxf(fmaxf(m, sc[0][3]), sc[1][0]); m = fmaxf(fmaxf(m, sc[1][1]), sc[1][2]); m = fmaxf(fmaxf(m, sc[1][3]), sc[2][0]);
;                           m = fmaxf(fmaxf(m, sc[2][1]), sc[2][2]); m = fmaxf(fmaxf(m, sc[2][3]), sc[3][0]); m = fmaxf(fmaxf(m, sc[3][1]), sc[3][2]); mx = fmaxf(m, sc[3][3]) + bshift; }
;                         if (MODE == 3 && !colsel) mx = -1e30f;
;                         float p[4][4];
;                         constexpr float L2E = 1.4426950408889634f;
;                         if (MODE == 2 && pass == 1) {
;                             const float negm1 = (mrun[qd] < -1e29f ? 0.f : -mrun[qd] * L2E) + boff + linv[qd];
; #pragma unroll
;                             for (int kt = 0; kt < 4; ++kt)
; #pragma unroll
;                                 for (int r = 0; r < 4; ++r) p[kt][r] = __builtin_amdgcn_exp2f(__builtin_fmaf(sc[kt][r], L2E, negm1));
;                         } else if (MODE == 2) {
;                             const float mn = fmaxf(mrun[qd], mx), corr = __expf(mrun[qd] - mn); mrun[qd] = mn; float ps = 0.f;
;                             const float negm0 = (mn < -1e29f ? 0.f : -mn * L2E) + boff;
; #pragma unroll
;                             for (int kt = 0; kt < 4; ++kt)
; #pragma unroll
;                                 for (int r = 0; r < 4; ++r) ps += __builtin_amdgcn_exp2f(__builtin_fmaf(sc[kt][r], L2E, negm0));
;                             lrun[qd] = lrun[qd] * corr + ps;
;                         } else {
;                             if (__any(mx > mrun[qd] + 6.0f)) {
;                                 mx = fmaxf(mx, __shfl_xor(mx, 16)); mx = fmaxf(mx, __shfl_xor(mx, 32));
;                                 const float mn = fmaxf(mrun[qd], mx), corr = __expf(mrun[qd] - mn); mrun[qd] = mn;
;                                 lrun[qd] *= corr;
; #pragma unroll
;                                 for (int dt = 0; dt < 4; ++dt) O[qd][dt] = O[qd][dt] * corr;
;                             }
;                             float negm = (mrun[qd] < -1e29f ? 0.f : -mrun[qd] * L2E) + boff; float ps = 0.f;
.LBB0_1260:
	v_and_b32_e32 v192, s0, v205
	v_cmp_eq_u32_e64 s[0:1], 0, v192
	v_max3_f32 v192, v150, v151, v152
	v_max3_f32 v192, v192, v153, v146
	v_max3_f32 v192, v192, v147, v148
	v_max3_f32 v192, v192, v149, v142
	v_max3_f32 v192, v192, v143, v144
	v_max3_f32 v192, v192, v145, v106
	v_max3_f32 v192, v192, v107, v108
	v_max_f32_e32 v192, v192, v109
	v_add_f32_e32 v192, v237, v192
	v_cndmask_b32_e64 v192, v192, v190, s[0:1]
	v_add_f32_e32 v193, 0x40c00000, v236
	v_cmp_gt_f32_e32 vcc, v192, v193
	s_cbranch_vccz .LBB0_1262
	ds_bpermute_b32 v193, v230, v192
	v_max_f32_e32 v192, v192, v192
	s_waitcnt lgkmcnt(0)
	v_max_f32_e32 v193, v193, v193
	v_max_f32_e32 v192, v192, v193
	ds_bpermute_b32 v193, v231, v192
	s_waitcnt lgkmcnt(0)
	v_max3_f32 v193, v236, v192, v193
	v_sub_f32_e32 v192, v236, v193
	v_mul_f32_e32 v192, 0x3fb8aa3b, v192
	v_exp_f32_e32 v192, v192
	v_mov_b32_e32 v236, v193
	v_mul_f32_e32 v202, v202, v192
	v_mul_f32_e32 v88, v88, v192
	v_mul_f32_e32 v89, v89, v192
	v_mul_f32_e32 v86, v86, v192
	v_mul_f32_e32 v87, v87, v192
	v_mul_f32_e32 v84, v84, v192
	v_mul_f32_e32 v85, v85, v192
	v_mul_f32_e32 v82, v82, v192
	v_mul_f32_e32 v83, v83, v192
	v_mul_f32_e32 v80, v80, v192
	v_mul_f32_e32 v81, v81, v192
	v_mul_f32_e32 v78, v78, v192
	v_mul_f32_e32 v79, v79, v192
	v_mul_f32_e32 v76, v76, v192
	v_mul_f32_e32 v77, v77, v192
	v_mul_f32_e32 v74, v74, v192
	v_mul_f32_e32 v75, v75, v192
	v_mul_f32_e32 v250, 0xbfb8aa3b, v193
	v_cmp_ngt_f32_e32 vcc, s30, v193
	s_nop 1
	v_cndmask_b32_e32 v250, 0, v250, vcc

; #define LAS __attribute__((address_space(3)))
;     ...
; #pragma unroll
;                         for (int kt = 0; kt < 4; ++kt) { sc[kt] = (f32x4){0.f, 0.f, 0.f, 0.f};
; #pragma unroll
;                             for (int ks = 0; ks < 2; ++ks) { const bf16x8 ak = (MODE != 3) ? akf[kt][ks] : akq[kt][ks];
;                                 sc[kt] = __builtin_amdgcn_mfma_f32_16x16x32_bf16(ak, Bq[qd][ks], sc[kt], 0, 0, 0); } }
;                         if (MODE == 3) {
; #pragma unroll
;                             for (int st = 0; st < 2; ++st)
; #pragma unroll
;                                 for (int dt = 0; dt < 4; ++dt) avq[st][dt] = *(const LAS bf16x8*)(L + LV + (16 * dt + n) * 128 + ((((4 * st + q) ^ n) & 7) << 4));
;                             __builtin_amdgcn_sched_barrier(0);
;                         }
;                         if (!far) {
;                             const LAS float* tp = (MODE == 2) ? biasd + hr * NT + (DOFF - tq + 31 + 16 * p0) + 64 * q : biasd + hr * NT + (DOFF - tq + p0) + 4 * q;
; #pragma unroll
;                             for (int kt = 0; kt < 4; ++kt)
; #pragma unroll
;                                 for (int r = 0; r < 4; ++r) sc[kt][r] += (MODE == 3) ? bia[kt][r] : ((MODE == 2) ? tp[256 * kt + 16 * r] : tp[16 * kt + r]);
;                         }
.LBB0_1270:
	s_waitcnt lgkmcnt(7)
	v_mfma_f32_16x16x32_bf16 v[106:109], v[106:109], v[58:61], 0
	s_waitcnt lgkmcnt(6)
	v_mfma_f32_16x16x32_bf16 v[150:153], v[110:113], v[62:65], v[106:109]
	v_add_u32_e32 v110, v212, v195
	s_waitcnt lgkmcnt(5)
	v_mfma_f32_16x16x32_bf16 v[106:109], v[114:117], v[58:61], 0
	s_waitcnt lgkmcnt(4)
	v_mfma_f32_16x16x32_bf16 v[146:149], v[118:121], v[62:65], v[106:109]
	s_waitcnt lgkmcnt(3)
	v_mfma_f32_16x16x32_bf16 v[106:109], v[122:125], v[58:61], 0
	s_waitcnt lgkmcnt(2)
	v_mfma_f32_16x16x32_bf16 v[142:145], v[126:129], v[62:65], v[106:109]
	s_waitcnt lgkmcnt(1)
	v_mfma_f32_16x16x32_bf16 v[106:109], v[130:133], v[58:61], 0
	s_waitcnt lgkmcnt(0)
	v_mfma_f32_16x16x32_bf16 v[106:109], v[134:137], v[62:65], v[106:109]
	ds_read_b128 v[138:141], v110
	ds_read_b128 v[130:133], v110 offset:2048
	ds_read_b128 v[134:137], v110 offset:4096
	ds_read_b128 v[126:129], v110 offset:6144
	v_add_u32_e32 v110, v212, v204
	ds_read_b128 v[122:125], v110
	ds_read_b128 v[118:121], v110 offset:2048
	ds_read_b128 v[114:117], v110 offset:4096
	ds_read_b128 v[110:113], v110 offset:6144
	s_and_b64 vcc, exec, s[2:3]
	s_cbranch_vccnz .LBB0_1272
	v_add_f32_e32 v152, v170, v152
	v_add_f32_e32 v153, v171, v153
	v_add_f32_e32 v150, v168, v150
	v_add_f32_e32 v151, v169, v151
	v_add_f32_e32 v148, v174, v148
	v_add_f32_e32 v149, v175, v149
	v_add_f32_e32 v146, v172, v146
	v_add_f32_e32 v147, v173, v147
	v_add_f32_e32 v144, v178, v144
	v_add_f32_e32 v145, v179, v145
	v_add_f32_e32 v142, v176, v142
	v_add_f32_e32 v143, v177, v143
	v_add_f32_e32 v108, v182, v108
	v_add_f32_e32 v109, v183, v109
	v_add_f32_e32 v106, v180, v106
	v_add_f32_e32 v107, v181, v107
	v_mov_b32_e32 v248, 0
	s_branch .LBB0_1273

; #define LAS __attribute__((address_space(3)))
;     ...
; #pragma unroll
;                         for (int kt = 0; kt < 4; ++kt) { sc[kt] = (f32x4){0.f, 0.f, 0.f, 0.f};
; #pragma unroll
;                             for (int ks = 0; ks < 2; ++ks) { const bf16x8 ak = (MODE != 3) ? akf[kt][ks] : akq[kt][ks];
;                                 sc[kt] = __builtin_amdgcn_mfma_f32_16x16x32_bf16(ak, Bq[qd][ks], sc[kt], 0, 0, 0); } }
;                         if (MODE == 3) {
; #pragma unroll
;                             for (int st = 0; st < 2; ++st)
; #pragma unroll
;                                 for (int dt = 0; dt < 4; ++dt) avq[st][dt] = *(const LAS bf16x8*)(L + LV + (16 * dt + n) * 128 + ((((4 * st + q) ^ n) & 7) << 4));
;                             __builtin_amdgcn_sched_barrier(0);
;                         }
;                         if (!far) {
;                             const LAS float* tp = (MODE == 2) ? biasd + hr * NT + (DOFF - tq + 31 + 16 * p0) + 64 * q : biasd + hr * NT + (DOFF - tq + p0) + 4 * q;
; #pragma unroll
;                             for (int kt = 0; kt < 4; ++kt)
; #pragma unroll
;                                 for (int r = 0; r < 4; ++r) sc[kt][r] += (MODE == 3) ? bia[kt][r] : ((MODE == 2) ? tp[256 * kt + 16 * r] : tp[16 * kt + r]);
;                         }
.LBB0_1279:
	s_waitcnt lgkmcnt(7)
	v_mfma_f32_16x16x32_bf16 v[106:109], v[106:109], v[66:69], 0
	s_waitcnt lgkmcnt(6)
	v_mfma_f32_16x16x32_bf16 v[150:153], v[110:113], v[70:73], v[106:109]
	v_add_u32_e32 v110, v212, v195
	s_waitcnt lgkmcnt(5)
	v_mfma_f32_16x16x32_bf16 v[106:109], v[114:117], v[66:69], 0
	s_waitcnt lgkmcnt(4)
	v_mfma_f32_16x16x32_bf16 v[146:149], v[118:121], v[70:73], v[106:109]
	s_waitcnt lgkmcnt(3)
	v_mfma_f32_16x16x32_bf16 v[106:109], v[122:125], v[66:69], 0
	s_waitcnt lgkmcnt(2)
	v_mfma_f32_16x16x32_bf16 v[142:145], v[126:129], v[70:73], v[106:109]
	s_waitcnt lgkmcnt(1)
	v_mfma_f32_16x16x32_bf16 v[106:109], v[130:133], v[66:69], 0
	s_waitcnt lgkmcnt(0)
	v_mfma_f32_16x16x32_bf16 v[106:109], v[134:137], v[70:73], v[106:109]
	ds_read_b128 v[138:141], v110
	ds_read_b128 v[130:133], v110 offset:2048
	ds_read_b128 v[134:137], v110 offset:4096
	ds_read_b128 v[126:129], v110 offset:6144
	v_add_u32_e32 v110, v212, v204
	ds_read_b128 v[122:125], v110
	ds_read_b128 v[118:121], v110 offset:2048
	ds_read_b128 v[114:117], v110 offset:4096
	ds_read_b128 v[110:113], v110 offset:6144
	s_and_b64 vcc, exec, s[2:3]
	s_cbranch_vccnz .LBB0_1281
	v_add_f32_e32 v152, v170, v152
	v_add_f32_e32 v153, v171, v153
	v_add_f32_e32 v150, v168, v150
	v_add_f32_e32 v151, v169, v151
	v_add_f32_e32 v148, v174, v148
	v_add_f32_e32 v149, v175, v149
	v_add_f32_e32 v146, v172, v146
	v_add_f32_e32 v147, v173, v147
	v_add_f32_e32 v144, v178, v144
	v_add_f32_e32 v145, v179, v145
	v_add_f32_e32 v142, v176, v142
	v_add_f32_e32 v143, v177, v143
	v_add_f32_e32 v108, v182, v108
	v_add_f32_e32 v109, v183, v109
	v_add_f32_e32 v106, v180, v106
	v_add_f32_e32 v107, v181, v107
	v_mov_b32_e32 v237, 0
	s_branch .LBB0_1282

; #define LAS __attribute__((address_space(3)))
;     ...
; #pragma unroll
;                         for (int kt = 0; kt < 4; ++kt) { sc[kt] = (f32x4){0.f, 0.f, 0.f, 0.f};
; #pragma unroll
;                             for (int ks = 0; ks < 2; ++ks) { const bf16x8 ak = (MODE != 3) ? akf[kt][ks] : akq[kt][ks];
;                                 sc[kt] = __builtin_amdgcn_mfma_f32_16x16x32_bf16(ak, Bq[qd][ks], sc[kt], 0, 0, 0); } }
;                         if (MODE == 3) {
; #pragma unroll
;                             for (int st = 0; st < 2; ++st)
; #pragma unroll
;                                 for (int dt = 0; dt < 4; ++dt) avq[st][dt] = *(const LAS bf16x8*)(L + LV + (16 * dt + n) * 128 + ((((4 * st + q) ^ n) & 7) << 4));
;                             __builtin_amdgcn_sched_barrier(0);
;                         }
;                         if (!far) {
;                             const LAS float* tp = (MODE == 2) ? biasd + hr * NT + (DOFF - tq + 31 + 16 * p0) + 64 * q : biasd + hr * NT + (DOFF - tq + p0) + 4 * q;
; #pragma unroll
;                             for (int kt = 0; kt < 4; ++kt)
; #pragma unroll
;                                 for (int r = 0; r < 4; ++r) sc[kt][r] += (MODE == 3) ? bia[kt][r] : ((MODE == 2) ? tp[256 * kt + 16 * r] : tp[16 * kt + r]);
;                         }
.LBB0_1292:
	s_waitcnt lgkmcnt(7)
	v_mfma_f32_16x16x32_bf16 v[106:109], v[106:109], v[58:61], 0
	s_waitcnt lgkmcnt(6)
	v_mfma_f32_16x16x32_bf16 v[150:153], v[110:113], v[62:65], v[106:109]
	v_add_u32_e32 v110, v217, v195
	s_waitcnt lgkmcnt(5)
	v_mfma_f32_16x16x32_bf16 v[106:109], v[114:117], v[58:61], 0
	s_waitcnt lgkmcnt(4)
	v_mfma_f32_16x16x32_bf16 v[146:149], v[118:121], v[62:65], v[106:109]
	s_waitcnt lgkmcnt(3)
	v_mfma_f32_16x16x32_bf16 v[106:109], v[122:125], v[58:61], 0
	s_waitcnt lgkmcnt(2)
	v_mfma_f32_16x16x32_bf16 v[142:145], v[126:129], v[62:65], v[106:109]
	s_waitcnt lgkmcnt(1)
	v_mfma_f32_16x16x32_bf16 v[106:109], v[130:133], v[58:61], 0
	s_waitcnt lgkmcnt(0)
	v_mfma_f32_16x16x32_bf16 v[106:109], v[134:137], v[62:65], v[106:109]
	ds_read_b128 v[138:141], v110
	ds_read_b128 v[130:133], v110 offset:2048
	ds_read_b128 v[134:137], v110 offset:4096
	ds_read_b128 v[126:129], v110 offset:6144
	v_add_u32_e32 v110, v217, v204
	ds_read_b128 v[122:125], v110
	ds_read_b128 v[118:121], v110 offset:2048
	ds_read_b128 v[114:117], v110 offset:4096
	ds_read_b128 v[110:113], v110 offset:6144
	s_and_b64 vcc, exec, s[2:3]
	s_cbranch_vccnz .LBB0_1294
	v_add_f32_e32 v152, v170, v152
	v_add_f32_e32 v153, v171, v153
	v_add_f32_e32 v150, v168, v150
	v_add_f32_e32 v151, v169, v151
	v_add_f32_e32 v148, v174, v148
	v_add_f32_e32 v149, v175, v149
	v_add_f32_e32 v146, v172, v146
	v_add_f32_e32 v147, v173, v147
	v_add_f32_e32 v144, v178, v144
	v_add_f32_e32 v145, v179, v145
	v_add_f32_e32 v142, v176, v142
	v_add_f32_e32 v143, v177, v143
	v_add_f32_e32 v108, v182, v108
	v_add_f32_e32 v109, v183, v109
	v_add_f32_e32 v106, v180, v106
	v_add_f32_e32 v107, v181, v107
	v_mov_b32_e32 v248, 0
	s_branch .LBB0_1295

; #define LAS __attribute__((address_space(3)))
;     ...
; #pragma unroll
;                         for (int kt = 0; kt < 4; ++kt) { sc[kt] = (f32x4){0.f, 0.f, 0.f, 0.f};
; #pragma unroll
;                             for (int ks = 0; ks < 2; ++ks) { const bf16x8 ak = (MODE != 3) ? akf[kt][ks] : akq[kt][ks];
;                                 sc[kt] = __builtin_amdgcn_mfma_f32_16x16x32_bf16(ak, Bq[qd][ks], sc[kt], 0, 0, 0); } }
;                         if (MODE == 3) {
; #pragma unroll
;                             for (int st = 0; st < 2; ++st)
; #pragma unroll
;                                 for (int dt = 0; dt < 4; ++dt) avq[st][dt] = *(const LAS bf16x8*)(L + LV + (16 * dt + n) * 128 + ((((4 * st + q) ^ n) & 7) << 4));
;                             __builtin_amdgcn_sched_barrier(0);
;                         }
;                         if (!far) {
;                             const LAS float* tp = (MODE == 2) ? biasd + hr * NT + (DOFF - tq + 31 + 16 * p0) + 64 * q : biasd + hr * NT + (DOFF - tq + p0) + 4 * q;
; #pragma unroll
;                             for (int kt = 0; kt < 4; ++kt)
; #pragma unroll
;                                 for (int r = 0; r < 4; ++r) sc[kt][r] += (MODE == 3) ? bia[kt][r] : ((MODE == 2) ? tp[256 * kt + 16 * r] : tp[16 * kt + r]);
;                         }
.LBB0_1301:
	s_waitcnt lgkmcnt(7)
	v_mfma_f32_16x16x32_bf16 v[106:109], v[106:109], v[66:69], 0
	s_waitcnt lgkmcnt(6)
	v_mfma_f32_16x16x32_bf16 v[150:153], v[110:113], v[70:73], v[106:109]
	v_add_u32_e32 v110, v217, v195
	s_waitcnt lgkmcnt(5)
	v_mfma_f32_16x16x32_bf16 v[106:109], v[114:117], v[66:69], 0
	s_waitcnt lgkmcnt(4)
	v_mfma_f32_16x16x32_bf16 v[146:149], v[118:121], v[70:73], v[106:109]
	s_waitcnt lgkmcnt(3)
	v_mfma_f32_16x16x32_bf16 v[106:109], v[122:125], v[66:69], 0
	s_waitcnt lgkmcnt(2)
	v_mfma_f32_16x16x32_bf16 v[142:145], v[126:129], v[70:73], v[106:109]
	s_waitcnt lgkmcnt(1)
	v_mfma_f32_16x16x32_bf16 v[106:109], v[130:133], v[66:69], 0
	s_waitcnt lgkmcnt(0)
	v_mfma_f32_16x16x32_bf16 v[106:109], v[134:137], v[70:73], v[106:109]
	ds_read_b128 v[138:141], v110
	ds_read_b128 v[130:133], v110 offset:2048
	ds_read_b128 v[134:137], v110 offset:4096
	ds_read_b128 v[126:129], v110 offset:6144
	v_add_u32_e32 v110, v217, v204
	ds_read_b128 v[122:125], v110
	ds_read_b128 v[118:121], v110 offset:2048
	ds_read_b128 v[114:117], v110 offset:4096
	ds_read_b128 v[110:113], v110 offset:6144
	s_and_b64 vcc, exec, s[2:3]
	s_cbranch_vccnz .LBB0_1303
	v_add_f32_e32 v152, v170, v152
	v_add_f32_e32 v153, v171, v153
	v_add_f32_e32 v150, v168, v150
	v_add_f32_e32 v151, v169, v151
	v_add_f32_e32 v148, v174, v148
	v_add_f32_e32 v149, v175, v149
	v_add_f32_e32 v146, v172, v146
	v_add_f32_e32 v147, v173, v147
	v_add_f32_e32 v144, v178, v144
	v_add_f32_e32 v145, v179, v145
	v_add_f32_e32 v142, v176, v142
	v_add_f32_e32 v143, v177, v143
	v_add_f32_e32 v108, v182, v108
	v_add_f32_e32 v109, v183, v109
	v_add_f32_e32 v106, v180, v106
	v_add_f32_e32 v107, v181, v107
	v_mov_b32_e32 v237, 0
	s_branch .LBB0_1304
